# GEMM K-loops: priority 1 during load segments, 0 during MFMA blocks (inverse of the baseline flips), on top of the barrier change
# baseline (speedup 1.0000x reference)
; #define PG8_LDA(dst, b, h) do { _Pragma("unroll") for (int m = 0; m < 4; ++m) _Pragma("unroll") for (int k = 0; k < 2; ++k) dst[m][k] = *(const PG8_LAS bf16x8*)(lds + PG8_SA(b, h) + aoff + m * 2048 + k * 1024); } while (0)
; #define PG8_LDB(dst, b, h) do { _Pragma("unroll") for (int n = 0; n < 2; ++n) _Pragma("unroll") for (int k = 0; k < 2; ++k) dst[n][k] = *(const PG8_LAS bf16x8*)(lds + PG8_SB(b, h) + boff + n * 2048 + k * 1024); } while (0)
; #define PG8_WAIT_V(n) asm volatile("s_waitcnt vmcnt(" #n ")" ::: "memory")
; #define PG8_WAIT_L(n) asm volatile("s_waitcnt lgkmcnt(" #n ")" ::: "memory")
; #define PG8_BAR __builtin_amdgcn_s_barrier()
; #define PG8_SCHED __builtin_amdgcn_sched_barrier(0)
; template <class Epi, class Sched, bool ALIGN_EPI = false, bool SP2 = false, bool F8 = false, bool I8 = false, bool PF = false>
; __device__ __forceinline__ void gemm_phase(PG8_LAS unsigned char* lds, const Gemm g, const Sched& S, const Epi& E, const int wave_) {
;     ...
;             PG8_LDB(B0, 0, 0); PG8_LDB(B1, 0, 1); PG8_SCHED; PG8_LDA(At, 0, 0); PG8_STAGE(PG8_SA(1, 1), a1 + hstep, voffA);
;             PG8_WAIT_V(8); PG8_WAIT_L(0); PG8_BAR; PG8_MMA(0, 0, At, B0); PG8_MMA(0, 1, At, B1); PG8_BAR; PG8_SCHED;
;             PG8_LDA(At, 0, 1); PG8_STAGE(PG8_SB(0, 0), b2, voffB); PG8_STAGE(PG8_SB(0, 1), b2 + hstep, voffB); PG8_STAGE(PG8_SA(0, 0), a2, voffA);
;             PG8_WAIT_V(8); PG8_WAIT_L(0); PG8_BAR; PG8_MMA(1, 0, At, B0); PG8_MMA(1, 1, At, B1); PG8_BAR; PG8_SCHED;
.LBB0_242:
	ds_read_b128 v[128:131], v180
	ds_read_b128 v[132:135], v180 offset:1024
	ds_read_b128 v[150:153], v180 offset:2048
	ds_read_b128 v[154:157], v180 offset:3072
	ds_read_b128 v[158:161], v181
	ds_read_b128 v[162:165], v181 offset:1024
	ds_read_b128 v[166:169], v181 offset:2048
	ds_read_b128 v[170:173], v181 offset:3072
	s_add_u32 s50, s48, 0xfffe0080
	s_addc_u32 s51, s49, -1
	s_cmp_eq_u32 s79, 4
	s_cselect_b32 s53, s1, s51
	s_cselect_b32 s52, s5, s50
	s_cselect_b32 s51, s39, s78
	s_cselect_b32 s50, s41, s75
	v_lshl_add_u64 v[212:213], s[48:49], 0, v[144:145]
	s_add_i32 m0, s35, 0xc000
	ds_read_b128 v[174:177], v182
	ds_read_b128 v[184:187], v182 offset:1024
	ds_read_b128 v[188:191], v182 offset:2048
	ds_read_b128 v[192:195], v182 offset:3072
	ds_read_b128 v[196:199], v182 offset:4096
	ds_read_b128 v[200:203], v182 offset:5120
	ds_read_b128 v[204:207], v182 offset:6144
	ds_read_b128 v[208:211], v182 offset:7168
	global_load_lds_dwordx4 v[212:213], off
	v_lshl_add_u64 v[212:213], s[48:49], 0, v[146:147]
	s_add_i32 m0, s35, 0xe000
	s_nop 0
	global_load_lds_dwordx4 v[212:213], off
	s_waitcnt vmcnt(8)
	s_waitcnt lgkmcnt(0)
	s_setprio 0
	s_barrier
	s_waitcnt lgkmcnt(0)
	v_mfma_i32_16x16x64_i8 v[124:127], v[128:131], v[174:177], v[124:127]
	v_mfma_i32_16x16x64_i8 v[120:123], v[150:153], v[174:177], v[120:123]
	v_mfma_i32_16x16x64_i8 v[108:111], v[128:131], v[188:191], v[108:111]
	v_mfma_i32_16x16x64_i8 v[104:107], v[150:153], v[188:191], v[104:107]
	v_mfma_i32_16x16x64_i8 v[92:95], v[128:131], v[196:199], v[92:95]
	v_mfma_i32_16x16x64_i8 v[88:91], v[150:153], v[196:199], v[88:91]
	v_mfma_i32_16x16x64_i8 v[76:79], v[128:131], v[204:207], v[76:79]
	v_mfma_i32_16x16x64_i8 v[72:75], v[150:153], v[204:207], v[72:75]
	v_mfma_i32_16x16x64_i8 v[124:127], v[132:135], v[184:187], v[124:127]
	v_mfma_i32_16x16x64_i8 v[120:123], v[154:157], v[184:187], v[120:123]
	v_mfma_i32_16x16x64_i8 v[108:111], v[132:135], v[192:195], v[108:111]
	v_mfma_i32_16x16x64_i8 v[104:107], v[154:157], v[192:195], v[104:107]
	v_mfma_i32_16x16x64_i8 v[92:95], v[132:135], v[200:203], v[92:95]
	v_mfma_i32_16x16x64_i8 v[88:91], v[154:157], v[200:203], v[88:91]
	v_mfma_i32_16x16x64_i8 v[76:79], v[132:135], v[208:211], v[76:79]
	v_mfma_i32_16x16x64_i8 v[72:75], v[154:157], v[208:211], v[72:75]
	v_mfma_i32_16x16x64_i8 v[116:119], v[158:161], v[174:177], v[116:119]
	v_mfma_i32_16x16x64_i8 v[112:115], v[166:169], v[174:177], v[112:115]
	v_mfma_i32_16x16x64_i8 v[100:103], v[158:161], v[188:191], v[100:103]
	v_mfma_i32_16x16x64_i8 v[96:99], v[166:169], v[188:191], v[96:99]
	v_mfma_i32_16x16x64_i8 v[84:87], v[158:161], v[196:199], v[84:87]
	v_mfma_i32_16x16x64_i8 v[80:83], v[166:169], v[196:199], v[80:83]
	v_mfma_i32_16x16x64_i8 v[68:71], v[158:161], v[204:207], v[68:71]
	v_mfma_i32_16x16x64_i8 v[64:67], v[166:169], v[204:207], v[64:67]
	v_mfma_i32_16x16x64_i8 v[116:119], v[162:165], v[184:187], v[116:119]
	v_mfma_i32_16x16x64_i8 v[112:115], v[170:173], v[184:187], v[112:115]
	v_mfma_i32_16x16x64_i8 v[100:103], v[162:165], v[192:195], v[100:103]
	v_mfma_i32_16x16x64_i8 v[96:99], v[170:173], v[192:195], v[96:99]
	v_mfma_i32_16x16x64_i8 v[84:87], v[162:165], v[200:203], v[84:87]
	v_mfma_i32_16x16x64_i8 v[80:83], v[170:173], v[200:203], v[80:83]
	v_mfma_i32_16x16x64_i8 v[68:71], v[162:165], v[208:211], v[68:71]
	v_mfma_i32_16x16x64_i8 v[64:67], v[170:173], v[208:211], v[64:67]
	s_barrier
	s_setprio 1
	s_add_i32 s86, s66, s27
	v_lshl_add_u64 v[212:213], s[50:51], 0, v[138:139]
	s_mov_b32 m0, s86
	ds_read_b128 v[174:177], v182 offset:16384
	ds_read_b128 v[184:187], v182 offset:17408
	ds_read_b128 v[188:191], v182 offset:18432
	ds_read_b128 v[192:195], v182 offset:19456
	ds_read_b128 v[196:199], v182 offset:20480
	ds_read_b128 v[200:203], v182 offset:21504
	ds_read_b128 v[204:207], v182 offset:22528
	ds_read_b128 v[208:211], v182 offset:23552
	global_load_lds_dwordx4 v[212:213], off
	s_add_i32 m0, s86, 0x2000
	s_add_u32 s86, s50, 0x20000
	v_lshl_add_u64 v[214:215], s[50:51], 0, v[142:143]
	s_addc_u32 s87, s51, 0
	s_add_i32 vcc_lo, s67, s27
	global_load_lds_dwordx4 v[214:215], off
	v_lshl_add_u64 v[216:217], s[86:87], 0, v[138:139]
	s_mov_b32 m0, vcc_lo
	v_lshl_add_u64 v[218:219], s[52:53], 0, v[140:141]
	global_load_lds_dwordx4 v[216:217], off
	v_lshl_add_u64 v[216:217], s[86:87], 0, v[142:143]
	s_add_i32 m0, vcc_lo, 0x2000
	s_nop 0
	global_load_lds_dwordx4 v[216:217], off
	v_lshl_add_u64 v[216:217], s[52:53], 0, v[136:137]
	s_mov_b32 m0, s35
	s_nop 0
	global_load_lds_dwordx4 v[216:217], off
	s_mov_b32 m0, s37
	s_nop 0
	global_load_lds_dwordx4 v[218:219], off
	s_waitcnt vmcnt(8)
	s_waitcnt lgkmcnt(0)
	s_setprio 0
	s_barrier
; #define PG8_LDA(dst, b, h) do { _Pragma("unroll") for (int m = 0; m < 4; ++m) _Pragma("unroll") for (int k = 0; k < 2; ++k) dst[m][k] = *(const PG8_LAS bf16x8*)(lds + PG8_SA(b, h) + aoff + m * 2048 + k * 1024); } while (0)
; #define PG8_LDB(dst, b, h) do { _Pragma("unroll") for (int n = 0; n < 2; ++n) _Pragma("unroll") for (int k = 0; k < 2; ++k) dst[n][k] = *(const PG8_LAS bf16x8*)(lds + PG8_SB(b, h) + boff + n * 2048 + k * 1024); } while (0)
; #define PG8_WAIT_V(n) asm volatile("s_waitcnt vmcnt(" #n ")" ::: "memory")
; #define PG8_WAIT_L(n) asm volatile("s_waitcnt lgkmcnt(" #n ")" ::: "memory")
; #define PG8_BAR __builtin_amdgcn_s_barrier()
; #define PG8_SCHED __builtin_amdgcn_sched_barrier(0)
; template <class Epi, class Sched, bool ALIGN_EPI = false, bool SP2 = false, bool F8 = false, bool I8 = false, bool PF = false>
; __device__ __forceinline__ void gemm_phase(PG8_LAS unsigned char* lds, const Gemm g, const Sched& S, const Epi& E, const int wave_) {
;     ...
;             PG8_WAIT_V(8); PG8_WAIT_L(0); PG8_BAR; PG8_MMA(1, 0, At, B0); PG8_MMA(1, 1, At, B1); PG8_BAR; PG8_SCHED;
;             PG8_LDB(B0, 1, 0); PG8_LDB(B1, 1, 1); PG8_SCHED; PG8_LDA(At, 1, 0); PG8_STAGE(PG8_SA(0, 1), a2 + hstep, voffA);
;             PG8_WAIT_V(8); PG8_WAIT_L(0); PG8_BAR; PG8_MMA(0, 0, At, B0); PG8_MMA(0, 1, At, B1); PG8_BAR; PG8_SCHED;
	s_waitcnt lgkmcnt(0)
	v_mfma_i32_16x16x64_i8 v[60:63], v[128:131], v[174:177], v[60:63]
	v_mfma_i32_16x16x64_i8 v[56:59], v[150:153], v[174:177], v[56:59]
	v_mfma_i32_16x16x64_i8 v[44:47], v[128:131], v[188:191], v[44:47]
	v_mfma_i32_16x16x64_i8 v[40:43], v[150:153], v[188:191], v[40:43]
	v_mfma_i32_16x16x64_i8 v[28:31], v[128:131], v[196:199], v[28:31]
	v_mfma_i32_16x16x64_i8 v[24:27], v[150:153], v[196:199], v[24:27]
	v_mfma_i32_16x16x64_i8 v[12:15], v[128:131], v[204:207], v[12:15]
	v_mfma_i32_16x16x64_i8 v[8:11], v[150:153], v[204:207], v[8:11]
	v_mfma_i32_16x16x64_i8 v[60:63], v[132:135], v[184:187], v[60:63]
	v_mfma_i32_16x16x64_i8 v[56:59], v[154:157], v[184:187], v[56:59]
	v_mfma_i32_16x16x64_i8 v[44:47], v[132:135], v[192:195], v[44:47]
	v_mfma_i32_16x16x64_i8 v[40:43], v[154:157], v[192:195], v[40:43]
	v_mfma_i32_16x16x64_i8 v[28:31], v[132:135], v[200:203], v[28:31]
	v_mfma_i32_16x16x64_i8 v[24:27], v[154:157], v[200:203], v[24:27]
	v_mfma_i32_16x16x64_i8 v[12:15], v[132:135], v[208:211], v[12:15]
	v_mfma_i32_16x16x64_i8 v[8:11], v[154:157], v[208:211], v[8:11]
	v_mfma_i32_16x16x64_i8 v[52:55], v[158:161], v[174:177], v[52:55]
	v_mfma_i32_16x16x64_i8 v[48:51], v[166:169], v[174:177], v[48:51]
	v_mfma_i32_16x16x64_i8 v[36:39], v[158:161], v[188:191], v[36:39]
	v_mfma_i32_16x16x64_i8 v[32:35], v[166:169], v[188:191], v[32:35]
	v_mfma_i32_16x16x64_i8 v[20:23], v[158:161], v[196:199], v[20:23]
	v_mfma_i32_16x16x64_i8 v[16:19], v[166:169], v[196:199], v[16:19]
	v_mfma_i32_16x16x64_i8 v[4:7], v[158:161], v[204:207], v[4:7]
	v_mfma_i32_16x16x64_i8 v[0:3], v[166:169], v[204:207], v[0:3]
	v_mfma_i32_16x16x64_i8 v[52:55], v[162:165], v[184:187], v[52:55]
	v_mfma_i32_16x16x64_i8 v[48:51], v[170:173], v[184:187], v[48:51]
	v_mfma_i32_16x16x64_i8 v[36:39], v[162:165], v[192:195], v[36:39]
	v_mfma_i32_16x16x64_i8 v[32:35], v[170:173], v[192:195], v[32:35]
	v_mfma_i32_16x16x64_i8 v[20:23], v[162:165], v[200:203], v[20:23]
	v_mfma_i32_16x16x64_i8 v[16:19], v[170:173], v[200:203], v[16:19]
	v_mfma_i32_16x16x64_i8 v[4:7], v[162:165], v[208:211], v[4:7]
	v_mfma_i32_16x16x64_i8 v[0:3], v[170:173], v[208:211], v[0:3]
	s_barrier
	s_setprio 1
	s_add_i32 s86, 0, 0x18000
	s_add_i32 s87, 0, 0x1c000
	v_add_u32_e32 v154, s86, v179
	v_add_u32_e32 v170, s87, v179
	ds_read_b128 v[128:131], v154
	ds_read_b128 v[132:135], v154 offset:1024
	ds_read_b128 v[150:153], v154 offset:2048
	ds_read_b128 v[154:157], v154 offset:3072
	ds_read_b128 v[158:161], v170
	ds_read_b128 v[162:165], v170 offset:1024
	ds_read_b128 v[166:169], v170 offset:2048
	ds_read_b128 v[170:173], v170 offset:3072
	s_add_u32 s52, s52, 0x20000
	s_addc_u32 s53, s53, 0
	s_mov_b32 m0, s54
	v_lshl_add_u64 v[220:221], s[52:53], 0, v[136:137]
	ds_read_b128 v[174:177], v182 offset:32768
	ds_read_b128 v[184:187], v182 offset:33792
	ds_read_b128 v[188:191], v182 offset:34816
	ds_read_b128 v[192:195], v182 offset:35840
	ds_read_b128 v[196:199], v182 offset:36864
	ds_read_b128 v[200:203], v182 offset:37888
	ds_read_b128 v[204:207], v182 offset:38912
	ds_read_b128 v[208:211], v182 offset:39936
	global_load_lds_dwordx4 v[220:221], off
	v_lshl_add_u64 v[220:221], s[52:53], 0, v[140:141]
	s_mov_b32 m0, s55
	s_nop 0
	global_load_lds_dwordx4 v[220:221], off
	s_waitcnt vmcnt(8)
	s_waitcnt lgkmcnt(0)
	s_setprio 0
	s_barrier
	s_waitcnt lgkmcnt(0)
	v_mfma_i32_16x16x64_i8 v[124:127], v[128:131], v[174:177], v[124:127]
	v_mfma_i32_16x16x64_i8 v[120:123], v[150:153], v[174:177], v[120:123]
	v_mfma_i32_16x16x64_i8 v[108:111], v[128:131], v[188:191], v[108:111]
	v_mfma_i32_16x16x64_i8 v[104:107], v[150:153], v[188:191], v[104:107]
	v_mfma_i32_16x16x64_i8 v[92:95], v[128:131], v[196:199], v[92:95]
	v_mfma_i32_16x16x64_i8 v[88:91], v[150:153], v[196:199], v[88:91]
	v_mfma_i32_16x16x64_i8 v[76:79], v[128:131], v[204:207], v[76:79]
	v_mfma_i32_16x16x64_i8 v[72:75], v[150:153], v[204:207], v[72:75]
	v_mfma_i32_16x16x64_i8 v[124:127], v[132:135], v[184:187], v[124:127]
	v_mfma_i32_16x16x64_i8 v[120:123], v[154:157], v[184:187], v[120:123]
	v_mfma_i32_16x16x64_i8 v[108:111], v[132:135], v[192:195], v[108:111]
	v_mfma_i32_16x16x64_i8 v[104:107], v[154:157], v[192:195], v[104:107]
	v_mfma_i32_16x16x64_i8 v[92:95], v[132:135], v[200:203], v[92:95]
	v_mfma_i32_16x16x64_i8 v[88:91], v[154:157], v[200:203], v[88:91]
	v_mfma_i32_16x16x64_i8 v[76:79], v[132:135], v[208:211], v[76:79]
	v_mfma_i32_16x16x64_i8 v[72:75], v[154:157], v[208:211], v[72:75]
	v_mfma_i32_16x16x64_i8 v[116:119], v[158:161], v[174:177], v[116:119]
	v_mfma_i32_16x16x64_i8 v[112:115], v[166:169], v[174:177], v[112:115]
	v_mfma_i32_16x16x64_i8 v[100:103], v[158:161], v[188:191], v[100:103]
	v_mfma_i32_16x16x64_i8 v[96:99], v[166:169], v[188:191], v[96:99]
	v_mfma_i32_16x16x64_i8 v[84:87], v[158:161], v[196:199], v[84:87]
	v_mfma_i32_16x16x64_i8 v[80:83], v[166:169], v[196:199], v[80:83]
	v_mfma_i32_16x16x64_i8 v[68:71], v[158:161], v[204:207], v[68:71]
	v_mfma_i32_16x16x64_i8 v[64:67], v[166:169], v[204:207], v[64:67]
	v_mfma_i32_16x16x64_i8 v[116:119], v[162:165], v[184:187], v[116:119]
	v_mfma_i32_16x16x64_i8 v[112:115], v[170:173], v[184:187], v[112:115]
	v_mfma_i32_16x16x64_i8 v[100:103], v[162:165], v[192:195], v[100:103]
	v_mfma_i32_16x16x64_i8 v[96:99], v[170:173], v[192:195], v[96:99]
	v_mfma_i32_16x16x64_i8 v[84:87], v[162:165], v[200:203], v[84:87]
	v_mfma_i32_16x16x64_i8 v[80:83], v[170:173], v[200:203], v[80:83]
	v_mfma_i32_16x16x64_i8 v[68:71], v[162:165], v[208:211], v[68:71]
	v_mfma_i32_16x16x64_i8 v[64:67], v[170:173], v[208:211], v[64:67]
	s_barrier
; #define PG8_LDA(dst, b, h) do { _Pragma("unroll") for (int m = 0; m < 4; ++m) _Pragma("unroll") for (int k = 0; k < 2; ++k) dst[m][k] = *(const PG8_LAS bf16x8*)(lds + PG8_SA(b, h) + aoff + m * 2048 + k * 1024); } while (0)
; #define PG8_WAIT_V(n) asm volatile("s_waitcnt vmcnt(" #n ")" ::: "memory")
; #define PG8_WAIT_L(n) asm volatile("s_waitcnt lgkmcnt(" #n ")" ::: "memory")
; #define PG8_BAR __builtin_amdgcn_s_barrier()
; #define PG8_SCHED __builtin_amdgcn_sched_barrier(0)
; template <class Epi, class Sched, bool ALIGN_EPI = false, bool SP2 = false, bool F8 = false, bool I8 = false, bool PF = false>
; __device__ __forceinline__ void gemm_phase(PG8_LAS unsigned char* lds, const Gemm g, const Sched& S, const Epi& E, const int wave_) {
;     ...
;         for (int t = 0; t < nt; t += 2) {
;             const bool last = (t == nt - 2);
;             const char* a1 = cA + (size_t)(t + 1) * kstep;
;             const char* a2 = last ? nA : cA + (size_t)(t + 2) * kstep; const char* b2 = last ? nB : cB + (size_t)(t + 2) * kstep;
;             const char* a3 = a2 + kstep; const char* b3 = b2 + kstep;
;             if (last && has_next) S.a_ready(nxt);
;     ...
;             PG8_LDA(At, 1, 1); PG8_STAGE(PG8_SB(1, 0), b3, voffB); PG8_STAGE(PG8_SB(1, 1), b3 + hstep, voffB); PG8_STAGE(PG8_SA(1, 0), a3, voffA);
;             PG8_WAIT_V(8); PG8_WAIT_L(0); PG8_BAR; PG8_MMA(1, 0, At, B0); PG8_MMA(1, 1, At, B1); PG8_BAR; PG8_SCHED;
	s_setprio 1
	s_add_i32 s52, s86, s27
	v_lshl_add_u64 v[212:213], v[212:213], 0, s[14:15]
	s_mov_b32 m0, s52
	ds_read_b128 v[174:177], v182 offset:49152
	ds_read_b128 v[184:187], v182 offset:50176
	ds_read_b128 v[188:191], v182 offset:51200
	ds_read_b128 v[192:195], v182 offset:52224
	ds_read_b128 v[196:199], v182 offset:53248
	ds_read_b128 v[200:203], v182 offset:54272
	ds_read_b128 v[204:207], v182 offset:55296
	ds_read_b128 v[208:211], v182 offset:56320
	global_load_lds_dwordx4 v[212:213], off
	s_add_i32 m0, s52, 0x2000
	s_add_u32 s50, s50, 0x20080
	v_lshl_add_u64 v[212:213], v[214:215], 0, s[14:15]
	s_addc_u32 s51, s51, 0
	s_add_i32 s52, s87, s27
	global_load_lds_dwordx4 v[212:213], off
	v_lshl_add_u64 v[212:213], s[50:51], 0, v[138:139]
	s_mov_b32 m0, s52
	s_nop 0
	global_load_lds_dwordx4 v[212:213], off
	v_lshl_add_u64 v[212:213], s[50:51], 0, v[142:143]
	s_add_i32 m0, s52, 0x2000
	s_nop 0
	global_load_lds_dwordx4 v[212:213], off
	v_lshl_add_u64 v[212:213], v[216:217], 0, s[14:15]
	s_mov_b32 m0, s63
	s_nop 0
	global_load_lds_dwordx4 v[212:213], off
	v_lshl_add_u64 v[212:213], v[218:219], 0, s[14:15]
	s_mov_b32 m0, s64
	s_nop 0
	global_load_lds_dwordx4 v[212:213], off
	s_waitcnt vmcnt(8)
	s_waitcnt lgkmcnt(0)
	s_setprio 0
	s_barrier
	s_waitcnt lgkmcnt(0)
	v_mfma_i32_16x16x64_i8 v[60:63], v[128:131], v[174:177], v[60:63]
	v_mfma_i32_16x16x64_i8 v[56:59], v[150:153], v[174:177], v[56:59]
	v_mfma_i32_16x16x64_i8 v[44:47], v[128:131], v[188:191], v[44:47]
	v_mfma_i32_16x16x64_i8 v[40:43], v[150:153], v[188:191], v[40:43]
	v_mfma_i32_16x16x64_i8 v[28:31], v[128:131], v[196:199], v[28:31]
	v_mfma_i32_16x16x64_i8 v[24:27], v[150:153], v[196:199], v[24:27]
	v_mfma_i32_16x16x64_i8 v[12:15], v[128:131], v[204:207], v[12:15]
	v_mfma_i32_16x16x64_i8 v[8:11], v[150:153], v[204:207], v[8:11]
	v_mfma_i32_16x16x64_i8 v[60:63], v[132:135], v[184:187], v[60:63]
	v_mfma_i32_16x16x64_i8 v[56:59], v[154:157], v[184:187], v[56:59]
	v_mfma_i32_16x16x64_i8 v[44:47], v[132:135], v[192:195], v[44:47]
	v_mfma_i32_16x16x64_i8 v[40:43], v[154:157], v[192:195], v[40:43]
	v_mfma_i32_16x16x64_i8 v[28:31], v[132:135], v[200:203], v[28:31]
	v_mfma_i32_16x16x64_i8 v[24:27], v[154:157], v[200:203], v[24:27]
	v_mfma_i32_16x16x64_i8 v[12:15], v[132:135], v[208:211], v[12:15]
	v_mfma_i32_16x16x64_i8 v[8:11], v[154:157], v[208:211], v[8:11]
	v_mfma_i32_16x16x64_i8 v[52:55], v[158:161], v[174:177], v[52:55]
	v_mfma_i32_16x16x64_i8 v[48:51], v[166:169], v[174:177], v[48:51]
	v_mfma_i32_16x16x64_i8 v[36:39], v[158:161], v[188:191], v[36:39]
	v_mfma_i32_16x16x64_i8 v[32:35], v[166:169], v[188:191], v[32:35]
	v_mfma_i32_16x16x64_i8 v[20:23], v[158:161], v[196:199], v[20:23]
	v_mfma_i32_16x16x64_i8 v[16:19], v[166:169], v[196:199], v[16:19]
	v_mfma_i32_16x16x64_i8 v[4:7], v[158:161], v[204:207], v[4:7]
	v_mfma_i32_16x16x64_i8 v[0:3], v[166:169], v[204:207], v[0:3]
	v_mfma_i32_16x16x64_i8 v[52:55], v[162:165], v[184:187], v[52:55]
	v_mfma_i32_16x16x64_i8 v[48:51], v[170:173], v[184:187], v[48:51]
	v_mfma_i32_16x16x64_i8 v[36:39], v[162:165], v[192:195], v[36:39]
	v_mfma_i32_16x16x64_i8 v[32:35], v[170:173], v[192:195], v[32:35]
	v_mfma_i32_16x16x64_i8 v[20:23], v[162:165], v[200:203], v[20:23]
	v_mfma_i32_16x16x64_i8 v[16:19], v[170:173], v[200:203], v[16:19]
	v_mfma_i32_16x16x64_i8 v[4:7], v[162:165], v[208:211], v[4:7]
	v_mfma_i32_16x16x64_i8 v[0:3], v[170:173], v[208:211], v[0:3]
	s_barrier
	s_setprio 1
	s_add_i32 s79, s79, 2
	s_add_u32 s48, s48, 0x100
	s_addc_u32 s49, s49, 0
	s_add_u32 s75, s75, 0x100
	s_addc_u32 s78, s78, 0
	s_cmp_gt_u32 s79, 5
	s_cbranch_scc0 .LBB0_242
	s_setprio 0
	s_and_b64 vcc, exec, s[16:17]
	s_cbranch_vccz .LBB0_245
	s_barrier

; #define PG8_LDA(dst, b, h) do { _Pragma("unroll") for (int m = 0; m < 4; ++m) _Pragma("unroll") for (int k = 0; k < 2; ++k) dst[m][k] = *(const PG8_LAS bf16x8*)(lds + PG8_SA(b, h) + aoff + m * 2048 + k * 1024); } while (0)
; #define PG8_LDB(dst, b, h) do { _Pragma("unroll") for (int n = 0; n < 2; ++n) _Pragma("unroll") for (int k = 0; k < 2; ++k) dst[n][k] = *(const PG8_LAS bf16x8*)(lds + PG8_SB(b, h) + boff + n * 2048 + k * 1024); } while (0)
; #define PG8_WAIT_V(n) asm volatile("s_waitcnt vmcnt(" #n ")" ::: "memory")
; #define PG8_WAIT_L(n) asm volatile("s_waitcnt lgkmcnt(" #n ")" ::: "memory")
; #define PG8_BAR __builtin_amdgcn_s_barrier()
; #define PG8_SCHED __builtin_amdgcn_sched_barrier(0)
; template <class Epi, class Sched, bool ALIGN_EPI = false, bool SP2 = false, bool F8 = false, bool I8 = false, bool PF = false>
; __device__ __forceinline__ void gemm_phase(PG8_LAS unsigned char* lds, const Gemm g, const Sched& S, const Epi& E, const int wave_) {
;     ...
;             PG8_LDB(B0, 0, 0); PG8_LDB(B1, 0, 1); PG8_SCHED; PG8_LDA(At, 0, 0); PG8_STAGE(PG8_SA(1, 1), a1 + hstep, voffA);
;             PG8_WAIT_V(8); PG8_WAIT_L(0); PG8_BAR; PG8_MMA(0, 0, At, B0); PG8_MMA(0, 1, At, B1); PG8_BAR; PG8_SCHED;
;             PG8_LDA(At, 0, 1); PG8_STAGE(PG8_SB(0, 0), b2, voffB); PG8_STAGE(PG8_SB(0, 1), b2 + hstep, voffB); PG8_STAGE(PG8_SA(0, 0), a2, voffA);
;             PG8_WAIT_V(8); PG8_WAIT_L(0); PG8_BAR; PG8_MMA(1, 0, At, B0); PG8_MMA(1, 1, At, B1); PG8_BAR; PG8_SCHED;
.LBB0_453:
	ds_read_b128 v[128:131], v175
	ds_read_b128 v[132:135], v175 offset:1024
	ds_read_b128 v[136:139], v175 offset:2048
	ds_read_b128 v[140:143], v175 offset:3072
	ds_read_b128 v[144:147], v176
	ds_read_b128 v[148:151], v176 offset:1024
	ds_read_b128 v[166:169], v176 offset:2048
	ds_read_b128 v[170:173], v176 offset:3072
	s_add_u32 s28, s22, 0xfffc0080
	s_addc_u32 s29, s23, -1
	s_cmp_eq_u32 s62, 12
	s_cselect_b32 s31, s13, s29
	s_cselect_b32 s30, s52, s28
	s_cselect_b32 s29, s11, s55
	s_cselect_b32 s28, s53, s54
	v_lshl_add_u64 v[210:211], s[22:23], 0, v[160:161]
	s_add_i32 m0, s21, 0xc000
	ds_read_b128 v[178:181], v177
	ds_read_b128 v[182:185], v177 offset:1024
	ds_read_b128 v[186:189], v177 offset:2048
	ds_read_b128 v[190:193], v177 offset:3072
	ds_read_b128 v[194:197], v177 offset:4096
	ds_read_b128 v[198:201], v177 offset:5120
	ds_read_b128 v[202:205], v177 offset:6144
	ds_read_b128 v[206:209], v177 offset:7168
	global_load_lds_dwordx4 v[210:211], off
	v_lshl_add_u64 v[210:211], s[22:23], 0, v[162:163]
	s_add_i32 m0, s21, 0xe000
	s_nop 0
	global_load_lds_dwordx4 v[210:211], off
	s_waitcnt vmcnt(8)
	s_waitcnt lgkmcnt(0)
	s_setprio 0
	s_barrier
	s_waitcnt lgkmcnt(0)
	v_mfma_f32_16x16x32_bf16 v[124:127], v[128:131], v[178:181], v[124:127]
	v_mfma_f32_16x16x32_bf16 v[120:123], v[136:139], v[178:181], v[120:123]
	v_mfma_f32_16x16x32_bf16 v[116:119], v[128:131], v[186:189], v[116:119]
	v_mfma_f32_16x16x32_bf16 v[112:115], v[136:139], v[186:189], v[112:115]
	v_mfma_f32_16x16x32_bf16 v[96:99], v[128:131], v[194:197], v[96:99]
	v_mfma_f32_16x16x32_bf16 v[88:91], v[136:139], v[194:197], v[88:91]
	v_mfma_f32_16x16x32_bf16 v[80:83], v[128:131], v[202:205], v[80:83]
	v_mfma_f32_16x16x32_bf16 v[72:75], v[136:139], v[202:205], v[72:75]
	v_mfma_f32_16x16x32_bf16 v[124:127], v[132:135], v[182:185], v[124:127]
	v_mfma_f32_16x16x32_bf16 v[120:123], v[140:143], v[182:185], v[120:123]
	v_mfma_f32_16x16x32_bf16 v[116:119], v[132:135], v[190:193], v[116:119]
	v_mfma_f32_16x16x32_bf16 v[112:115], v[140:143], v[190:193], v[112:115]
	v_mfma_f32_16x16x32_bf16 v[96:99], v[132:135], v[198:201], v[96:99]
	v_mfma_f32_16x16x32_bf16 v[88:91], v[140:143], v[198:201], v[88:91]
	v_mfma_f32_16x16x32_bf16 v[80:83], v[132:135], v[206:209], v[80:83]
	v_mfma_f32_16x16x32_bf16 v[72:75], v[140:143], v[206:209], v[72:75]
	v_mfma_f32_16x16x32_bf16 v[108:111], v[144:147], v[178:181], v[108:111]
	v_mfma_f32_16x16x32_bf16 v[104:107], v[166:169], v[178:181], v[104:107]
	v_mfma_f32_16x16x32_bf16 v[100:103], v[144:147], v[186:189], v[100:103]
	v_mfma_f32_16x16x32_bf16 v[92:95], v[166:169], v[186:189], v[92:95]
	v_mfma_f32_16x16x32_bf16 v[84:87], v[144:147], v[194:197], v[84:87]
	v_mfma_f32_16x16x32_bf16 v[76:79], v[166:169], v[194:197], v[76:79]
	v_mfma_f32_16x16x32_bf16 v[68:71], v[144:147], v[202:205], v[68:71]
	v_mfma_f32_16x16x32_bf16 v[64:67], v[166:169], v[202:205], v[64:67]
	v_mfma_f32_16x16x32_bf16 v[108:111], v[148:151], v[182:185], v[108:111]
	v_mfma_f32_16x16x32_bf16 v[104:107], v[170:173], v[182:185], v[104:107]
	v_mfma_f32_16x16x32_bf16 v[100:103], v[148:151], v[190:193], v[100:103]
	v_mfma_f32_16x16x32_bf16 v[92:95], v[170:173], v[190:193], v[92:95]
	v_mfma_f32_16x16x32_bf16 v[84:87], v[148:151], v[198:201], v[84:87]
	v_mfma_f32_16x16x32_bf16 v[76:79], v[170:173], v[198:201], v[76:79]
	v_mfma_f32_16x16x32_bf16 v[68:71], v[148:151], v[206:209], v[68:71]
	v_mfma_f32_16x16x32_bf16 v[64:67], v[170:173], v[206:209], v[64:67]
	s_barrier
	s_setprio 1
	s_add_i32 s63, s49, s36
	v_lshl_add_u64 v[210:211], s[28:29], 0, v[156:157]
	s_mov_b32 m0, s63
	ds_read_b128 v[178:181], v177 offset:16384
	ds_read_b128 v[182:185], v177 offset:17408
	ds_read_b128 v[186:189], v177 offset:18432
	ds_read_b128 v[190:193], v177 offset:19456
	ds_read_b128 v[194:197], v177 offset:20480
	ds_read_b128 v[198:201], v177 offset:21504
	ds_read_b128 v[202:205], v177 offset:22528
	ds_read_b128 v[206:209], v177 offset:23552
	global_load_lds_dwordx4 v[210:211], off
	s_add_i32 m0, s63, 0x2000
	s_add_u32 s64, s28, 0x40000
	v_lshl_add_u64 v[212:213], s[28:29], 0, v[152:153]
	s_addc_u32 s65, s29, 0
	s_add_i32 s63, s50, s36
	global_load_lds_dwordx4 v[212:213], off
	v_lshl_add_u64 v[214:215], s[64:65], 0, v[156:157]
	s_mov_b32 m0, s63
	v_lshl_add_u64 v[216:217], s[30:31], 0, v[154:155]
	global_load_lds_dwordx4 v[214:215], off
	v_lshl_add_u64 v[214:215], s[64:65], 0, v[152:153]
	s_add_i32 m0, s63, 0x2000
	s_nop 0
	global_load_lds_dwordx4 v[214:215], off
	v_lshl_add_u64 v[214:215], s[30:31], 0, v[158:159]
	s_mov_b32 m0, s21
	s_nop 0
	global_load_lds_dwordx4 v[214:215], off
	s_mov_b32 m0, s37
	s_nop 0
	global_load_lds_dwordx4 v[216:217], off
	s_waitcnt vmcnt(8)
	s_waitcnt lgkmcnt(0)
	s_setprio 0
	s_barrier
; #define PG8_LDA(dst, b, h) do { _Pragma("unroll") for (int m = 0; m < 4; ++m) _Pragma("unroll") for (int k = 0; k < 2; ++k) dst[m][k] = *(const PG8_LAS bf16x8*)(lds + PG8_SA(b, h) + aoff + m * 2048 + k * 1024); } while (0)
; #define PG8_LDB(dst, b, h) do { _Pragma("unroll") for (int n = 0; n < 2; ++n) _Pragma("unroll") for (int k = 0; k < 2; ++k) dst[n][k] = *(const PG8_LAS bf16x8*)(lds + PG8_SB(b, h) + boff + n * 2048 + k * 1024); } while (0)
; #define PG8_WAIT_V(n) asm volatile("s_waitcnt vmcnt(" #n ")" ::: "memory")
; #define PG8_WAIT_L(n) asm volatile("s_waitcnt lgkmcnt(" #n ")" ::: "memory")
; #define PG8_BAR __builtin_amdgcn_s_barrier()
; #define PG8_SCHED __builtin_amdgcn_sched_barrier(0)
; template <class Epi, class Sched, bool ALIGN_EPI = false, bool SP2 = false, bool F8 = false, bool I8 = false, bool PF = false>
; __device__ __forceinline__ void gemm_phase(PG8_LAS unsigned char* lds, const Gemm g, const Sched& S, const Epi& E, const int wave_) {
;     ...
;             PG8_WAIT_V(8); PG8_WAIT_L(0); PG8_BAR; PG8_MMA(1, 0, At, B0); PG8_MMA(1, 1, At, B1); PG8_BAR; PG8_SCHED;
;             PG8_LDB(B0, 1, 0); PG8_LDB(B1, 1, 1); PG8_SCHED; PG8_LDA(At, 1, 0); PG8_STAGE(PG8_SA(0, 1), a2 + hstep, voffA);
;             PG8_WAIT_V(8); PG8_WAIT_L(0); PG8_BAR; PG8_MMA(0, 0, At, B0); PG8_MMA(0, 1, At, B1); PG8_BAR; PG8_SCHED;
	s_waitcnt lgkmcnt(0)
	v_mfma_f32_16x16x32_bf16 v[60:63], v[128:131], v[178:181], v[60:63]
	v_mfma_f32_16x16x32_bf16 v[56:59], v[136:139], v[178:181], v[56:59]
	v_mfma_f32_16x16x32_bf16 v[48:51], v[128:131], v[186:189], v[48:51]
	v_mfma_f32_16x16x32_bf16 v[40:43], v[136:139], v[186:189], v[40:43]
	v_mfma_f32_16x16x32_bf16 v[32:35], v[128:131], v[194:197], v[32:35]
	v_mfma_f32_16x16x32_bf16 v[24:27], v[136:139], v[194:197], v[24:27]
	v_mfma_f32_16x16x32_bf16 v[16:19], v[128:131], v[202:205], v[16:19]
	v_mfma_f32_16x16x32_bf16 v[8:11], v[136:139], v[202:205], v[8:11]
	v_mfma_f32_16x16x32_bf16 v[60:63], v[132:135], v[182:185], v[60:63]
	v_mfma_f32_16x16x32_bf16 v[56:59], v[140:143], v[182:185], v[56:59]
	v_mfma_f32_16x16x32_bf16 v[48:51], v[132:135], v[190:193], v[48:51]
	v_mfma_f32_16x16x32_bf16 v[40:43], v[140:143], v[190:193], v[40:43]
	v_mfma_f32_16x16x32_bf16 v[32:35], v[132:135], v[198:201], v[32:35]
	v_mfma_f32_16x16x32_bf16 v[24:27], v[140:143], v[198:201], v[24:27]
	v_mfma_f32_16x16x32_bf16 v[16:19], v[132:135], v[206:209], v[16:19]
	v_mfma_f32_16x16x32_bf16 v[8:11], v[140:143], v[206:209], v[8:11]
	v_mfma_f32_16x16x32_bf16 v[52:55], v[144:147], v[178:181], v[52:55]
	v_mfma_f32_16x16x32_bf16 v[44:47], v[166:169], v[178:181], v[44:47]
	v_mfma_f32_16x16x32_bf16 v[36:39], v[144:147], v[186:189], v[36:39]
	v_mfma_f32_16x16x32_bf16 v[28:31], v[166:169], v[186:189], v[28:31]
	v_mfma_f32_16x16x32_bf16 v[20:23], v[144:147], v[194:197], v[20:23]
	v_mfma_f32_16x16x32_bf16 v[12:15], v[166:169], v[194:197], v[12:15]
	v_mfma_f32_16x16x32_bf16 v[4:7], v[144:147], v[202:205], v[4:7]
	v_mfma_f32_16x16x32_bf16 v[0:3], v[166:169], v[202:205], v[0:3]
	v_mfma_f32_16x16x32_bf16 v[52:55], v[148:151], v[182:185], v[52:55]
	v_mfma_f32_16x16x32_bf16 v[44:47], v[170:173], v[182:185], v[44:47]
	v_mfma_f32_16x16x32_bf16 v[36:39], v[148:151], v[190:193], v[36:39]
	v_mfma_f32_16x16x32_bf16 v[28:31], v[170:173], v[190:193], v[28:31]
	v_mfma_f32_16x16x32_bf16 v[20:23], v[148:151], v[198:201], v[20:23]
	v_mfma_f32_16x16x32_bf16 v[12:15], v[170:173], v[198:201], v[12:15]
	v_mfma_f32_16x16x32_bf16 v[4:7], v[148:151], v[206:209], v[4:7]
	v_mfma_f32_16x16x32_bf16 v[0:3], v[170:173], v[206:209], v[0:3]
	s_barrier
	s_setprio 1
	s_add_i32 s63, 0, 0x18000
	s_add_i32 s64, 0, 0x1c000
	v_add_u32_e32 v140, s63, v174
	v_add_u32_e32 v170, s64, v174
	ds_read_b128 v[128:131], v140
	ds_read_b128 v[132:135], v140 offset:1024
	ds_read_b128 v[136:139], v140 offset:2048
	ds_read_b128 v[140:143], v140 offset:3072
	ds_read_b128 v[144:147], v170
	ds_read_b128 v[148:151], v170 offset:1024
	ds_read_b128 v[166:169], v170 offset:2048
	ds_read_b128 v[170:173], v170 offset:3072
	s_add_u32 s30, s30, 0x40000
	s_addc_u32 s31, s31, 0
	s_mov_b32 m0, s38
	v_lshl_add_u64 v[218:219], s[30:31], 0, v[158:159]
	ds_read_b128 v[178:181], v177 offset:32768
	ds_read_b128 v[182:185], v177 offset:33792
	ds_read_b128 v[186:189], v177 offset:34816
	ds_read_b128 v[190:193], v177 offset:35840
	ds_read_b128 v[194:197], v177 offset:36864
	ds_read_b128 v[198:201], v177 offset:37888
	ds_read_b128 v[202:205], v177 offset:38912
	ds_read_b128 v[206:209], v177 offset:39936
	global_load_lds_dwordx4 v[218:219], off
	v_lshl_add_u64 v[218:219], s[30:31], 0, v[154:155]
	s_mov_b32 m0, s39
	s_nop 0
	global_load_lds_dwordx4 v[218:219], off
	s_waitcnt vmcnt(8)
	s_waitcnt lgkmcnt(0)
	s_setprio 0
	s_barrier
	s_waitcnt lgkmcnt(0)
	v_mfma_f32_16x16x32_bf16 v[124:127], v[128:131], v[178:181], v[124:127]
	v_mfma_f32_16x16x32_bf16 v[120:123], v[136:139], v[178:181], v[120:123]
	v_mfma_f32_16x16x32_bf16 v[116:119], v[128:131], v[186:189], v[116:119]
	v_mfma_f32_16x16x32_bf16 v[112:115], v[136:139], v[186:189], v[112:115]
	v_mfma_f32_16x16x32_bf16 v[96:99], v[128:131], v[194:197], v[96:99]
	v_mfma_f32_16x16x32_bf16 v[88:91], v[136:139], v[194:197], v[88:91]
	v_mfma_f32_16x16x32_bf16 v[80:83], v[128:131], v[202:205], v[80:83]
	v_mfma_f32_16x16x32_bf16 v[72:75], v[136:139], v[202:205], v[72:75]
	v_mfma_f32_16x16x32_bf16 v[124:127], v[132:135], v[182:185], v[124:127]
	v_mfma_f32_16x16x32_bf16 v[120:123], v[140:143], v[182:185], v[120:123]
	v_mfma_f32_16x16x32_bf16 v[116:119], v[132:135], v[190:193], v[116:119]
	v_mfma_f32_16x16x32_bf16 v[112:115], v[140:143], v[190:193], v[112:115]
	v_mfma_f32_16x16x32_bf16 v[96:99], v[132:135], v[198:201], v[96:99]
	v_mfma_f32_16x16x32_bf16 v[88:91], v[140:143], v[198:201], v[88:91]
	v_mfma_f32_16x16x32_bf16 v[80:83], v[132:135], v[206:209], v[80:83]
	v_mfma_f32_16x16x32_bf16 v[72:75], v[140:143], v[206:209], v[72:75]
	v_mfma_f32_16x16x32_bf16 v[108:111], v[144:147], v[178:181], v[108:111]
	v_mfma_f32_16x16x32_bf16 v[104:107], v[166:169], v[178:181], v[104:107]
	v_mfma_f32_16x16x32_bf16 v[100:103], v[144:147], v[186:189], v[100:103]
	v_mfma_f32_16x16x32_bf16 v[92:95], v[166:169], v[186:189], v[92:95]
	v_mfma_f32_16x16x32_bf16 v[84:87], v[144:147], v[194:197], v[84:87]
	v_mfma_f32_16x16x32_bf16 v[76:79], v[166:169], v[194:197], v[76:79]
	v_mfma_f32_16x16x32_bf16 v[68:71], v[144:147], v[202:205], v[68:71]
	v_mfma_f32_16x16x32_bf16 v[64:67], v[166:169], v[202:205], v[64:67]
	v_mfma_f32_16x16x32_bf16 v[108:111], v[148:151], v[182:185], v[108:111]
	v_mfma_f32_16x16x32_bf16 v[104:107], v[170:173], v[182:185], v[104:107]
	v_mfma_f32_16x16x32_bf16 v[100:103], v[148:151], v[190:193], v[100:103]
	v_mfma_f32_16x16x32_bf16 v[92:95], v[170:173], v[190:193], v[92:95]
	v_mfma_f32_16x16x32_bf16 v[84:87], v[148:151], v[198:201], v[84:87]
	v_mfma_f32_16x16x32_bf16 v[76:79], v[170:173], v[198:201], v[76:79]
	v_mfma_f32_16x16x32_bf16 v[68:71], v[148:151], v[206:209], v[68:71]
	v_mfma_f32_16x16x32_bf16 v[64:67], v[170:173], v[206:209], v[64:67]
	s_barrier
; #define PG8_LDA(dst, b, h) do { _Pragma("unroll") for (int m = 0; m < 4; ++m) _Pragma("unroll") for (int k = 0; k < 2; ++k) dst[m][k] = *(const PG8_LAS bf16x8*)(lds + PG8_SA(b, h) + aoff + m * 2048 + k * 1024); } while (0)
; #define PG8_WAIT_V(n) asm volatile("s_waitcnt vmcnt(" #n ")" ::: "memory")
; #define PG8_WAIT_L(n) asm volatile("s_waitcnt lgkmcnt(" #n ")" ::: "memory")
; #define PG8_BAR __builtin_amdgcn_s_barrier()
; #define PG8_SCHED __builtin_amdgcn_sched_barrier(0)
; template <class Epi, class Sched, bool ALIGN_EPI = false, bool SP2 = false, bool F8 = false, bool I8 = false, bool PF = false>
; __device__ __forceinline__ void gemm_phase(PG8_LAS unsigned char* lds, const Gemm g, const Sched& S, const Epi& E, const int wave_) {
;     ...
;         for (int t = 0; t < nt; t += 2) {
;             const bool last = (t == nt - 2);
;             const char* a1 = cA + (size_t)(t + 1) * kstep;
;             const char* a2 = last ? nA : cA + (size_t)(t + 2) * kstep; const char* b2 = last ? nB : cB + (size_t)(t + 2) * kstep;
;             const char* a3 = a2 + kstep; const char* b3 = b2 + kstep;
;             if (last && has_next) S.a_ready(nxt);
;     ...
;             PG8_LDA(At, 1, 1); PG8_STAGE(PG8_SB(1, 0), b3, voffB); PG8_STAGE(PG8_SB(1, 1), b3 + hstep, voffB); PG8_STAGE(PG8_SA(1, 0), a3, voffA);
;             PG8_WAIT_V(8); PG8_WAIT_L(0); PG8_BAR; PG8_MMA(1, 0, At, B0); PG8_MMA(1, 1, At, B1); PG8_BAR; PG8_SCHED;
	s_setprio 1
	s_add_i32 s30, s63, s36
	v_lshl_add_u64 v[210:211], v[210:211], 0, s[6:7]
	s_mov_b32 m0, s30
	ds_read_b128 v[178:181], v177 offset:49152
	ds_read_b128 v[182:185], v177 offset:50176
	ds_read_b128 v[186:189], v177 offset:51200
	ds_read_b128 v[190:193], v177 offset:52224
	ds_read_b128 v[194:197], v177 offset:53248
	ds_read_b128 v[198:201], v177 offset:54272
	ds_read_b128 v[202:205], v177 offset:55296
	ds_read_b128 v[206:209], v177 offset:56320
	global_load_lds_dwordx4 v[210:211], off
	s_add_i32 m0, s30, 0x2000
	s_add_u32 s28, s28, 0x40080
	v_lshl_add_u64 v[210:211], v[212:213], 0, s[6:7]
	s_addc_u32 s29, s29, 0
	s_add_i32 s30, s64, s36
	global_load_lds_dwordx4 v[210:211], off
	v_lshl_add_u64 v[210:211], s[28:29], 0, v[156:157]
	s_mov_b32 m0, s30
	s_nop 0
	global_load_lds_dwordx4 v[210:211], off
	v_lshl_add_u64 v[210:211], s[28:29], 0, v[152:153]
	s_add_i32 m0, s30, 0x2000
	s_nop 0
	global_load_lds_dwordx4 v[210:211], off
	v_lshl_add_u64 v[210:211], v[214:215], 0, s[6:7]
	s_mov_b32 m0, s46
	s_nop 0
	global_load_lds_dwordx4 v[210:211], off
	v_lshl_add_u64 v[210:211], v[216:217], 0, s[6:7]
	s_mov_b32 m0, s47
	s_nop 0
	global_load_lds_dwordx4 v[210:211], off
	s_waitcnt vmcnt(8)
	s_waitcnt lgkmcnt(0)
	s_setprio 0
	s_barrier
	s_waitcnt lgkmcnt(0)
	v_mfma_f32_16x16x32_bf16 v[60:63], v[128:131], v[178:181], v[60:63]
	v_mfma_f32_16x16x32_bf16 v[56:59], v[136:139], v[178:181], v[56:59]
	v_mfma_f32_16x16x32_bf16 v[48:51], v[128:131], v[186:189], v[48:51]
	v_mfma_f32_16x16x32_bf16 v[40:43], v[136:139], v[186:189], v[40:43]
	v_mfma_f32_16x16x32_bf16 v[32:35], v[128:131], v[194:197], v[32:35]
	v_mfma_f32_16x16x32_bf16 v[24:27], v[136:139], v[194:197], v[24:27]
	v_mfma_f32_16x16x32_bf16 v[16:19], v[128:131], v[202:205], v[16:19]
	v_mfma_f32_16x16x32_bf16 v[8:11], v[136:139], v[202:205], v[8:11]
	v_mfma_f32_16x16x32_bf16 v[60:63], v[132:135], v[182:185], v[60:63]
	v_mfma_f32_16x16x32_bf16 v[56:59], v[140:143], v[182:185], v[56:59]
	v_mfma_f32_16x16x32_bf16 v[48:51], v[132:135], v[190:193], v[48:51]
	v_mfma_f32_16x16x32_bf16 v[40:43], v[140:143], v[190:193], v[40:43]
	v_mfma_f32_16x16x32_bf16 v[32:35], v[132:135], v[198:201], v[32:35]
	v_mfma_f32_16x16x32_bf16 v[24:27], v[140:143], v[198:201], v[24:27]
	v_mfma_f32_16x16x32_bf16 v[16:19], v[132:135], v[206:209], v[16:19]
	v_mfma_f32_16x16x32_bf16 v[8:11], v[140:143], v[206:209], v[8:11]
	v_mfma_f32_16x16x32_bf16 v[52:55], v[144:147], v[178:181], v[52:55]
	v_mfma_f32_16x16x32_bf16 v[44:47], v[166:169], v[178:181], v[44:47]
	v_mfma_f32_16x16x32_bf16 v[36:39], v[144:147], v[186:189], v[36:39]
	v_mfma_f32_16x16x32_bf16 v[28:31], v[166:169], v[186:189], v[28:31]
	v_mfma_f32_16x16x32_bf16 v[20:23], v[144:147], v[194:197], v[20:23]
	v_mfma_f32_16x16x32_bf16 v[12:15], v[166:169], v[194:197], v[12:15]
	v_mfma_f32_16x16x32_bf16 v[4:7], v[144:147], v[202:205], v[4:7]
	v_mfma_f32_16x16x32_bf16 v[0:3], v[166:169], v[202:205], v[0:3]
	v_mfma_f32_16x16x32_bf16 v[52:55], v[148:151], v[182:185], v[52:55]
	v_mfma_f32_16x16x32_bf16 v[44:47], v[170:173], v[182:185], v[44:47]
	v_mfma_f32_16x16x32_bf16 v[36:39], v[148:151], v[190:193], v[36:39]
	v_mfma_f32_16x16x32_bf16 v[28:31], v[170:173], v[190:193], v[28:31]
	v_mfma_f32_16x16x32_bf16 v[20:23], v[148:151], v[198:201], v[20:23]
	v_mfma_f32_16x16x32_bf16 v[12:15], v[170:173], v[198:201], v[12:15]
	v_mfma_f32_16x16x32_bf16 v[4:7], v[148:151], v[206:209], v[4:7]
	v_mfma_f32_16x16x32_bf16 v[0:3], v[170:173], v[206:209], v[0:3]
	s_barrier
	s_setprio 1
	s_add_i32 s62, s62, 2
	s_add_u32 s22, s22, 0x100
	s_addc_u32 s23, s23, 0
	s_add_u32 s54, s54, 0x100
	s_addc_u32 s55, s55, 0
	s_cmp_gt_u32 s62, 13
	s_cbranch_scc0 .LBB0_453
	s_setprio 0
	s_and_b64 vcc, exec, s[8:9]
	s_cbranch_vccz .LBB0_456
	s_barrier

; #define PG8_LDA(dst, b, h) do { _Pragma("unroll") for (int m = 0; m < 4; ++m) _Pragma("unroll") for (int k = 0; k < 2; ++k) dst[m][k] = *(const PG8_LAS bf16x8*)(lds + PG8_SA(b, h) + aoff + m * 2048 + k * 1024); } while (0)
; #define PG8_LDB(dst, b, h) do { _Pragma("unroll") for (int n = 0; n < 2; ++n) _Pragma("unroll") for (int k = 0; k < 2; ++k) dst[n][k] = *(const PG8_LAS bf16x8*)(lds + PG8_SB(b, h) + boff + n * 2048 + k * 1024); } while (0)
; #define PG8_WAIT_V(n) asm volatile("s_waitcnt vmcnt(" #n ")" ::: "memory")
; #define PG8_WAIT_L(n) asm volatile("s_waitcnt lgkmcnt(" #n ")" ::: "memory")
; #define PG8_BAR __builtin_amdgcn_s_barrier()
; #define PG8_SCHED __builtin_amdgcn_sched_barrier(0)
; template <class Epi, class Sched, bool ALIGN_EPI = false, bool SP2 = false, bool F8 = false, bool I8 = false, bool PF = false>
; __device__ __forceinline__ void gemm_phase(PG8_LAS unsigned char* lds, const Gemm g, const Sched& S, const Epi& E, const int wave_) {
;     ...
;             PG8_LDB(B0, 0, 0); PG8_LDB(B1, 0, 1); PG8_SCHED; PG8_LDA(At, 0, 0); PG8_STAGE(PG8_SA(1, 1), a1 + hstep, voffA);
;             PG8_WAIT_V(8); PG8_WAIT_L(0); PG8_BAR; PG8_MMA(0, 0, At, B0); PG8_MMA(0, 1, At, B1); PG8_BAR; PG8_SCHED;
;             PG8_LDA(At, 0, 1); PG8_STAGE(PG8_SB(0, 0), b2, voffB); PG8_STAGE(PG8_SB(0, 1), b2 + hstep, voffB); PG8_STAGE(PG8_SA(0, 0), a2, voffA);
;             PG8_WAIT_V(8); PG8_WAIT_L(0); PG8_BAR; PG8_MMA(1, 0, At, B0); PG8_MMA(1, 1, At, B1); PG8_BAR; PG8_SCHED;
.LBB0_591:
	ds_read_b128 v[142:145], v153
	ds_read_b128 v[146:149], v153 offset:1024
	ds_read_b128 v[158:161], v153 offset:2048
	ds_read_b128 v[162:165], v153 offset:3072
	ds_read_b128 v[166:169], v154
	ds_read_b128 v[170:173], v154 offset:1024
	ds_read_b128 v[174:177], v154 offset:2048
	ds_read_b128 v[178:181], v154 offset:3072
	s_add_u32 s34, s30, 0xfffe0080
	s_addc_u32 s35, s31, -1
	s_cmp_eq_u32 s64, 4
	s_cselect_b32 s37, s19, s35
	s_cselect_b32 s36, s56, s34
	s_cselect_b32 s35, s17, s63
	s_cselect_b32 s34, s57, s62
	v_lshl_add_u64 v[150:151], s[30:31], 0, v[136:137]
	s_add_i32 m0, s29, 0xc000
	ds_read_b128 v[182:185], v155
	ds_read_b128 v[186:189], v155 offset:1024
	ds_read_b128 v[190:193], v155 offset:2048
	ds_read_b128 v[194:197], v155 offset:3072
	ds_read_b128 v[198:201], v155 offset:4096
	ds_read_b128 v[202:205], v155 offset:5120
	ds_read_b128 v[206:209], v155 offset:6144
	ds_read_b128 v[210:213], v155 offset:7168
	global_load_lds_dwordx4 v[150:151], off
	v_lshl_add_u64 v[150:151], s[30:31], 0, v[138:139]
	s_add_i32 m0, s29, 0xe000
	s_nop 0
	global_load_lds_dwordx4 v[150:151], off
	s_waitcnt vmcnt(8)
	s_waitcnt lgkmcnt(0)
	s_setprio 0
	s_barrier
	s_waitcnt lgkmcnt(0)
	v_mfma_i32_16x16x64_i8 v[124:127], v[142:145], v[182:185], v[124:127]
	v_mfma_i32_16x16x64_i8 v[120:123], v[158:161], v[182:185], v[120:123]
	v_mfma_i32_16x16x64_i8 v[108:111], v[142:145], v[190:193], v[108:111]
	v_mfma_i32_16x16x64_i8 v[104:107], v[158:161], v[190:193], v[104:107]
	v_mfma_i32_16x16x64_i8 v[92:95], v[142:145], v[198:201], v[92:95]
	v_mfma_i32_16x16x64_i8 v[88:91], v[158:161], v[198:201], v[88:91]
	v_mfma_i32_16x16x64_i8 v[76:79], v[142:145], v[206:209], v[76:79]
	v_mfma_i32_16x16x64_i8 v[72:75], v[158:161], v[206:209], v[72:75]
	v_mfma_i32_16x16x64_i8 v[124:127], v[146:149], v[186:189], v[124:127]
	v_mfma_i32_16x16x64_i8 v[120:123], v[162:165], v[186:189], v[120:123]
	v_mfma_i32_16x16x64_i8 v[108:111], v[146:149], v[194:197], v[108:111]
	v_mfma_i32_16x16x64_i8 v[104:107], v[162:165], v[194:197], v[104:107]
	v_mfma_i32_16x16x64_i8 v[92:95], v[146:149], v[202:205], v[92:95]
	v_mfma_i32_16x16x64_i8 v[88:91], v[162:165], v[202:205], v[88:91]
	v_mfma_i32_16x16x64_i8 v[76:79], v[146:149], v[210:213], v[76:79]
	v_mfma_i32_16x16x64_i8 v[72:75], v[162:165], v[210:213], v[72:75]
	v_mfma_i32_16x16x64_i8 v[116:119], v[166:169], v[182:185], v[116:119]
	v_mfma_i32_16x16x64_i8 v[112:115], v[174:177], v[182:185], v[112:115]
	v_mfma_i32_16x16x64_i8 v[100:103], v[166:169], v[190:193], v[100:103]
	v_mfma_i32_16x16x64_i8 v[96:99], v[174:177], v[190:193], v[96:99]
	v_mfma_i32_16x16x64_i8 v[84:87], v[166:169], v[198:201], v[84:87]
	v_mfma_i32_16x16x64_i8 v[80:83], v[174:177], v[198:201], v[80:83]
	v_mfma_i32_16x16x64_i8 v[68:71], v[166:169], v[206:209], v[68:71]
	v_mfma_i32_16x16x64_i8 v[64:67], v[174:177], v[206:209], v[64:67]
	v_mfma_i32_16x16x64_i8 v[116:119], v[170:173], v[186:189], v[116:119]
	v_mfma_i32_16x16x64_i8 v[112:115], v[178:181], v[186:189], v[112:115]
	v_mfma_i32_16x16x64_i8 v[100:103], v[170:173], v[194:197], v[100:103]
	v_mfma_i32_16x16x64_i8 v[96:99], v[178:181], v[194:197], v[96:99]
	v_mfma_i32_16x16x64_i8 v[84:87], v[170:173], v[202:205], v[84:87]
	v_mfma_i32_16x16x64_i8 v[80:83], v[178:181], v[202:205], v[80:83]
	v_mfma_i32_16x16x64_i8 v[68:71], v[170:173], v[210:213], v[68:71]
	v_mfma_i32_16x16x64_i8 v[64:67], v[178:181], v[210:213], v[64:67]
	s_barrier
	s_setprio 1
	s_add_i32 s65, s51, s39
	v_lshl_add_u64 v[150:151], s[34:35], 0, v[132:133]
	s_mov_b32 m0, s65
	ds_read_b128 v[182:185], v155 offset:16384
	ds_read_b128 v[186:189], v155 offset:17408
	ds_read_b128 v[190:193], v155 offset:18432
	ds_read_b128 v[194:197], v155 offset:19456
	ds_read_b128 v[198:201], v155 offset:20480
	ds_read_b128 v[202:205], v155 offset:21504
	ds_read_b128 v[206:209], v155 offset:22528
	ds_read_b128 v[210:213], v155 offset:23552
	global_load_lds_dwordx4 v[150:151], off
	s_add_i32 m0, s65, 0x2000
	s_add_u32 s66, s34, 0x20000
	v_lshl_add_u64 v[214:215], s[34:35], 0, v[128:129]
	s_addc_u32 s67, s35, 0
	s_add_i32 s65, s52, s39
	global_load_lds_dwordx4 v[214:215], off
	v_lshl_add_u64 v[216:217], s[66:67], 0, v[132:133]
	s_mov_b32 m0, s65
	v_lshl_add_u64 v[218:219], s[36:37], 0, v[130:131]
	global_load_lds_dwordx4 v[216:217], off
	v_lshl_add_u64 v[216:217], s[66:67], 0, v[128:129]
	s_add_i32 m0, s65, 0x2000
	s_nop 0
	global_load_lds_dwordx4 v[216:217], off
	v_lshl_add_u64 v[216:217], s[36:37], 0, v[134:135]
	s_mov_b32 m0, s29
	s_nop 0
	global_load_lds_dwordx4 v[216:217], off
	s_mov_b32 m0, s41
	s_nop 0
	global_load_lds_dwordx4 v[218:219], off
	s_waitcnt vmcnt(8)
	s_waitcnt lgkmcnt(0)
	s_setprio 0
	s_barrier
; #define PG8_LDA(dst, b, h) do { _Pragma("unroll") for (int m = 0; m < 4; ++m) _Pragma("unroll") for (int k = 0; k < 2; ++k) dst[m][k] = *(const PG8_LAS bf16x8*)(lds + PG8_SA(b, h) + aoff + m * 2048 + k * 1024); } while (0)
; #define PG8_LDB(dst, b, h) do { _Pragma("unroll") for (int n = 0; n < 2; ++n) _Pragma("unroll") for (int k = 0; k < 2; ++k) dst[n][k] = *(const PG8_LAS bf16x8*)(lds + PG8_SB(b, h) + boff + n * 2048 + k * 1024); } while (0)
; #define PG8_WAIT_V(n) asm volatile("s_waitcnt vmcnt(" #n ")" ::: "memory")
; #define PG8_WAIT_L(n) asm volatile("s_waitcnt lgkmcnt(" #n ")" ::: "memory")
; #define PG8_BAR __builtin_amdgcn_s_barrier()
; #define PG8_SCHED __builtin_amdgcn_sched_barrier(0)
; template <class Epi, class Sched, bool ALIGN_EPI = false, bool SP2 = false, bool F8 = false, bool I8 = false, bool PF = false>
; __device__ __forceinline__ void gemm_phase(PG8_LAS unsigned char* lds, const Gemm g, const Sched& S, const Epi& E, const int wave_) {
;     ...
;             PG8_WAIT_V(8); PG8_WAIT_L(0); PG8_BAR; PG8_MMA(1, 0, At, B0); PG8_MMA(1, 1, At, B1); PG8_BAR; PG8_SCHED;
;             PG8_LDB(B0, 1, 0); PG8_LDB(B1, 1, 1); PG8_SCHED; PG8_LDA(At, 1, 0); PG8_STAGE(PG8_SA(0, 1), a2 + hstep, voffA);
;             PG8_WAIT_V(8); PG8_WAIT_L(0); PG8_BAR; PG8_MMA(0, 0, At, B0); PG8_MMA(0, 1, At, B1); PG8_BAR; PG8_SCHED;
	s_waitcnt lgkmcnt(0)
	v_mfma_i32_16x16x64_i8 v[60:63], v[142:145], v[182:185], v[60:63]
	v_mfma_i32_16x16x64_i8 v[56:59], v[158:161], v[182:185], v[56:59]
	v_mfma_i32_16x16x64_i8 v[44:47], v[142:145], v[190:193], v[44:47]
	v_mfma_i32_16x16x64_i8 v[40:43], v[158:161], v[190:193], v[40:43]
	v_mfma_i32_16x16x64_i8 v[28:31], v[142:145], v[198:201], v[28:31]
	v_mfma_i32_16x16x64_i8 v[24:27], v[158:161], v[198:201], v[24:27]
	v_mfma_i32_16x16x64_i8 v[12:15], v[142:145], v[206:209], v[12:15]
	v_mfma_i32_16x16x64_i8 v[8:11], v[158:161], v[206:209], v[8:11]
	v_mfma_i32_16x16x64_i8 v[60:63], v[146:149], v[186:189], v[60:63]
	v_mfma_i32_16x16x64_i8 v[56:59], v[162:165], v[186:189], v[56:59]
	v_mfma_i32_16x16x64_i8 v[44:47], v[146:149], v[194:197], v[44:47]
	v_mfma_i32_16x16x64_i8 v[40:43], v[162:165], v[194:197], v[40:43]
	v_mfma_i32_16x16x64_i8 v[28:31], v[146:149], v[202:205], v[28:31]
	v_mfma_i32_16x16x64_i8 v[24:27], v[162:165], v[202:205], v[24:27]
	v_mfma_i32_16x16x64_i8 v[12:15], v[146:149], v[210:213], v[12:15]
	v_mfma_i32_16x16x64_i8 v[8:11], v[162:165], v[210:213], v[8:11]
	v_mfma_i32_16x16x64_i8 v[52:55], v[166:169], v[182:185], v[52:55]
	v_mfma_i32_16x16x64_i8 v[48:51], v[174:177], v[182:185], v[48:51]
	v_mfma_i32_16x16x64_i8 v[36:39], v[166:169], v[190:193], v[36:39]
	v_mfma_i32_16x16x64_i8 v[32:35], v[174:177], v[190:193], v[32:35]
	v_mfma_i32_16x16x64_i8 v[20:23], v[166:169], v[198:201], v[20:23]
	v_mfma_i32_16x16x64_i8 v[16:19], v[174:177], v[198:201], v[16:19]
	v_mfma_i32_16x16x64_i8 v[4:7], v[166:169], v[206:209], v[4:7]
	v_mfma_i32_16x16x64_i8 v[0:3], v[174:177], v[206:209], v[0:3]
	v_mfma_i32_16x16x64_i8 v[52:55], v[170:173], v[186:189], v[52:55]
	v_mfma_i32_16x16x64_i8 v[48:51], v[178:181], v[186:189], v[48:51]
	v_mfma_i32_16x16x64_i8 v[36:39], v[170:173], v[194:197], v[36:39]
	v_mfma_i32_16x16x64_i8 v[32:35], v[178:181], v[194:197], v[32:35]
	v_mfma_i32_16x16x64_i8 v[20:23], v[170:173], v[202:205], v[20:23]
	v_mfma_i32_16x16x64_i8 v[16:19], v[178:181], v[202:205], v[16:19]
	v_mfma_i32_16x16x64_i8 v[4:7], v[170:173], v[210:213], v[4:7]
	v_mfma_i32_16x16x64_i8 v[0:3], v[178:181], v[210:213], v[0:3]
	s_barrier
	s_setprio 1
	s_add_i32 s65, 0, 0x18000
	v_add_u32_e32 v157, s65, v152
	s_add_i32 s66, 0, 0x1c000
	ds_read_b128 v[142:145], v157
	ds_read_b128 v[146:149], v157 offset:1024
	ds_read_b128 v[158:161], v157 offset:2048
	ds_read_b128 v[162:165], v157 offset:3072
	v_add_u32_e32 v157, s66, v152
	ds_read_b128 v[166:169], v157
	ds_read_b128 v[170:173], v157 offset:1024
	ds_read_b128 v[174:177], v157 offset:2048
	ds_read_b128 v[178:181], v157 offset:3072
	s_add_u32 s36, s36, 0x20000
	s_addc_u32 s37, s37, 0
	s_mov_b32 m0, s42
	v_lshl_add_u64 v[220:221], s[36:37], 0, v[134:135]
	ds_read_b128 v[182:185], v155 offset:32768
	ds_read_b128 v[186:189], v155 offset:33792
	ds_read_b128 v[190:193], v155 offset:34816
	ds_read_b128 v[194:197], v155 offset:35840
	ds_read_b128 v[198:201], v155 offset:36864
	ds_read_b128 v[202:205], v155 offset:37888
	ds_read_b128 v[206:209], v155 offset:38912
	ds_read_b128 v[210:213], v155 offset:39936
	global_load_lds_dwordx4 v[220:221], off
	v_lshl_add_u64 v[220:221], s[36:37], 0, v[130:131]
	s_mov_b32 m0, s43
	s_nop 0
	global_load_lds_dwordx4 v[220:221], off
	s_waitcnt vmcnt(8)
	s_waitcnt lgkmcnt(0)
	s_setprio 0
	s_barrier
	s_waitcnt lgkmcnt(0)
	v_mfma_i32_16x16x64_i8 v[124:127], v[142:145], v[182:185], v[124:127]
	v_mfma_i32_16x16x64_i8 v[120:123], v[158:161], v[182:185], v[120:123]
	v_mfma_i32_16x16x64_i8 v[108:111], v[142:145], v[190:193], v[108:111]
	v_mfma_i32_16x16x64_i8 v[104:107], v[158:161], v[190:193], v[104:107]
	v_mfma_i32_16x16x64_i8 v[92:95], v[142:145], v[198:201], v[92:95]
	v_mfma_i32_16x16x64_i8 v[88:91], v[158:161], v[198:201], v[88:91]
	v_mfma_i32_16x16x64_i8 v[76:79], v[142:145], v[206:209], v[76:79]
	v_mfma_i32_16x16x64_i8 v[72:75], v[158:161], v[206:209], v[72:75]
	v_mfma_i32_16x16x64_i8 v[124:127], v[146:149], v[186:189], v[124:127]
	v_mfma_i32_16x16x64_i8 v[120:123], v[162:165], v[186:189], v[120:123]
	v_mfma_i32_16x16x64_i8 v[108:111], v[146:149], v[194:197], v[108:111]
	v_mfma_i32_16x16x64_i8 v[104:107], v[162:165], v[194:197], v[104:107]
	v_mfma_i32_16x16x64_i8 v[92:95], v[146:149], v[202:205], v[92:95]
	v_mfma_i32_16x16x64_i8 v[88:91], v[162:165], v[202:205], v[88:91]
	v_mfma_i32_16x16x64_i8 v[76:79], v[146:149], v[210:213], v[76:79]
	v_mfma_i32_16x16x64_i8 v[72:75], v[162:165], v[210:213], v[72:75]
	v_mfma_i32_16x16x64_i8 v[116:119], v[166:169], v[182:185], v[116:119]
	v_mfma_i32_16x16x64_i8 v[112:115], v[174:177], v[182:185], v[112:115]
	v_mfma_i32_16x16x64_i8 v[100:103], v[166:169], v[190:193], v[100:103]
	v_mfma_i32_16x16x64_i8 v[96:99], v[174:177], v[190:193], v[96:99]
	v_mfma_i32_16x16x64_i8 v[84:87], v[166:169], v[198:201], v[84:87]
	v_mfma_i32_16x16x64_i8 v[80:83], v[174:177], v[198:201], v[80:83]
	v_mfma_i32_16x16x64_i8 v[68:71], v[166:169], v[206:209], v[68:71]
	v_mfma_i32_16x16x64_i8 v[64:67], v[174:177], v[206:209], v[64:67]
	v_mfma_i32_16x16x64_i8 v[116:119], v[170:173], v[186:189], v[116:119]
	v_mfma_i32_16x16x64_i8 v[112:115], v[178:181], v[186:189], v[112:115]
	v_mfma_i32_16x16x64_i8 v[100:103], v[170:173], v[194:197], v[100:103]
	v_mfma_i32_16x16x64_i8 v[96:99], v[178:181], v[194:197], v[96:99]
	v_mfma_i32_16x16x64_i8 v[84:87], v[170:173], v[202:205], v[84:87]
	v_mfma_i32_16x16x64_i8 v[80:83], v[178:181], v[202:205], v[80:83]
	v_mfma_i32_16x16x64_i8 v[68:71], v[170:173], v[210:213], v[68:71]
	v_mfma_i32_16x16x64_i8 v[64:67], v[178:181], v[210:213], v[64:67]
	s_barrier
; #define PG8_LDA(dst, b, h) do { _Pragma("unroll") for (int m = 0; m < 4; ++m) _Pragma("unroll") for (int k = 0; k < 2; ++k) dst[m][k] = *(const PG8_LAS bf16x8*)(lds + PG8_SA(b, h) + aoff + m * 2048 + k * 1024); } while (0)
; #define PG8_WAIT_V(n) asm volatile("s_waitcnt vmcnt(" #n ")" ::: "memory")
; #define PG8_WAIT_L(n) asm volatile("s_waitcnt lgkmcnt(" #n ")" ::: "memory")
; #define PG8_BAR __builtin_amdgcn_s_barrier()
; #define PG8_SCHED __builtin_amdgcn_sched_barrier(0)
; template <class Epi, class Sched, bool ALIGN_EPI = false, bool SP2 = false, bool F8 = false, bool I8 = false, bool PF = false>
; __device__ __forceinline__ void gemm_phase(PG8_LAS unsigned char* lds, const Gemm g, const Sched& S, const Epi& E, const int wave_) {
;     ...
;         for (int t = 0; t < nt; t += 2) {
;             const bool last = (t == nt - 2);
;             const char* a1 = cA + (size_t)(t + 1) * kstep;
;             const char* a2 = last ? nA : cA + (size_t)(t + 2) * kstep; const char* b2 = last ? nB : cB + (size_t)(t + 2) * kstep;
;             const char* a3 = a2 + kstep; const char* b3 = b2 + kstep;
;             if (last && has_next) S.a_ready(nxt);
;     ...
;             PG8_LDA(At, 1, 1); PG8_STAGE(PG8_SB(1, 0), b3, voffB); PG8_STAGE(PG8_SB(1, 1), b3 + hstep, voffB); PG8_STAGE(PG8_SA(1, 0), a3, voffA);
;             PG8_WAIT_V(8); PG8_WAIT_L(0); PG8_BAR; PG8_MMA(1, 0, At, B0); PG8_MMA(1, 1, At, B1); PG8_BAR; PG8_SCHED;
	s_setprio 1
	s_add_i32 s36, s65, s39
	v_lshl_add_u64 v[150:151], v[150:151], 0, s[10:11]
	s_mov_b32 m0, s36
	ds_read_b128 v[182:185], v155 offset:49152
	ds_read_b128 v[186:189], v155 offset:50176
	ds_read_b128 v[190:193], v155 offset:51200
	ds_read_b128 v[194:197], v155 offset:52224
	ds_read_b128 v[198:201], v155 offset:53248
	ds_read_b128 v[202:205], v155 offset:54272
	ds_read_b128 v[206:209], v155 offset:55296
	ds_read_b128 v[210:213], v155 offset:56320
	global_load_lds_dwordx4 v[150:151], off
	s_add_i32 m0, s36, 0x2000
	s_add_u32 s34, s34, 0x20080
	v_lshl_add_u64 v[150:151], v[214:215], 0, s[10:11]
	s_addc_u32 s35, s35, 0
	s_add_i32 s36, s66, s39
	global_load_lds_dwordx4 v[150:151], off
	v_lshl_add_u64 v[150:151], s[34:35], 0, v[132:133]
	s_mov_b32 m0, s36
	s_nop 0
	global_load_lds_dwordx4 v[150:151], off
	v_lshl_add_u64 v[150:151], s[34:35], 0, v[128:129]
	s_add_i32 m0, s36, 0x2000
	s_nop 0
	global_load_lds_dwordx4 v[150:151], off
	v_lshl_add_u64 v[150:151], v[216:217], 0, s[10:11]
	s_mov_b32 m0, s48
	s_nop 0
	global_load_lds_dwordx4 v[150:151], off
	v_lshl_add_u64 v[150:151], v[218:219], 0, s[10:11]
	s_mov_b32 m0, s49
	s_nop 0
	global_load_lds_dwordx4 v[150:151], off
	s_waitcnt vmcnt(8)
	s_waitcnt lgkmcnt(0)
	s_setprio 0
	s_barrier
	s_waitcnt lgkmcnt(0)
	v_mfma_i32_16x16x64_i8 v[60:63], v[142:145], v[182:185], v[60:63]
	v_mfma_i32_16x16x64_i8 v[56:59], v[158:161], v[182:185], v[56:59]
	v_mfma_i32_16x16x64_i8 v[44:47], v[142:145], v[190:193], v[44:47]
	v_mfma_i32_16x16x64_i8 v[40:43], v[158:161], v[190:193], v[40:43]
	v_mfma_i32_16x16x64_i8 v[28:31], v[142:145], v[198:201], v[28:31]
	v_mfma_i32_16x16x64_i8 v[24:27], v[158:161], v[198:201], v[24:27]
	v_mfma_i32_16x16x64_i8 v[12:15], v[142:145], v[206:209], v[12:15]
	v_mfma_i32_16x16x64_i8 v[8:11], v[158:161], v[206:209], v[8:11]
	v_mfma_i32_16x16x64_i8 v[60:63], v[146:149], v[186:189], v[60:63]
	v_mfma_i32_16x16x64_i8 v[56:59], v[162:165], v[186:189], v[56:59]
	v_mfma_i32_16x16x64_i8 v[44:47], v[146:149], v[194:197], v[44:47]
	v_mfma_i32_16x16x64_i8 v[40:43], v[162:165], v[194:197], v[40:43]
	v_mfma_i32_16x16x64_i8 v[28:31], v[146:149], v[202:205], v[28:31]
	v_mfma_i32_16x16x64_i8 v[24:27], v[162:165], v[202:205], v[24:27]
	v_mfma_i32_16x16x64_i8 v[12:15], v[146:149], v[210:213], v[12:15]
	v_mfma_i32_16x16x64_i8 v[8:11], v[162:165], v[210:213], v[8:11]
	v_mfma_i32_16x16x64_i8 v[52:55], v[166:169], v[182:185], v[52:55]
	v_mfma_i32_16x16x64_i8 v[48:51], v[174:177], v[182:185], v[48:51]
	v_mfma_i32_16x16x64_i8 v[36:39], v[166:169], v[190:193], v[36:39]
	v_mfma_i32_16x16x64_i8 v[32:35], v[174:177], v[190:193], v[32:35]
	v_mfma_i32_16x16x64_i8 v[20:23], v[166:169], v[198:201], v[20:23]
	v_mfma_i32_16x16x64_i8 v[16:19], v[174:177], v[198:201], v[16:19]
	v_mfma_i32_16x16x64_i8 v[4:7], v[166:169], v[206:209], v[4:7]
	v_mfma_i32_16x16x64_i8 v[0:3], v[174:177], v[206:209], v[0:3]
	v_mfma_i32_16x16x64_i8 v[52:55], v[170:173], v[186:189], v[52:55]
	v_mfma_i32_16x16x64_i8 v[48:51], v[178:181], v[186:189], v[48:51]
	v_mfma_i32_16x16x64_i8 v[36:39], v[170:173], v[194:197], v[36:39]
	v_mfma_i32_16x16x64_i8 v[32:35], v[178:181], v[194:197], v[32:35]
	v_mfma_i32_16x16x64_i8 v[20:23], v[170:173], v[202:205], v[20:23]
	v_mfma_i32_16x16x64_i8 v[16:19], v[178:181], v[202:205], v[16:19]
	v_mfma_i32_16x16x64_i8 v[4:7], v[170:173], v[210:213], v[4:7]
	v_mfma_i32_16x16x64_i8 v[0:3], v[178:181], v[210:213], v[0:3]
	s_barrier
	s_setprio 1
	s_add_i32 s64, s64, 2
	s_add_u32 s30, s30, 0x100
	s_addc_u32 s31, s31, 0
	s_add_u32 s62, s62, 0x100
	s_addc_u32 s63, s63, 0
	s_cmp_gt_u32 s64, 5
	s_cbranch_scc0 .LBB0_591
	s_setprio 0
	s_and_b64 vcc, exec, s[12:13]
	s_cbranch_vccz .LBB0_594
	s_barrier

; #define PG8_LDA(dst, b, h) do { _Pragma("unroll") for (int m = 0; m < 4; ++m) _Pragma("unroll") for (int k = 0; k < 2; ++k) dst[m][k] = *(const PG8_LAS bf16x8*)(lds + PG8_SA(b, h) + aoff + m * 2048 + k * 1024); } while (0)
; #define PG8_LDB(dst, b, h) do { _Pragma("unroll") for (int n = 0; n < 2; ++n) _Pragma("unroll") for (int k = 0; k < 2; ++k) dst[n][k] = *(const PG8_LAS bf16x8*)(lds + PG8_SB(b, h) + boff + n * 2048 + k * 1024); } while (0)
; #define PG8_WAIT_V(n) asm volatile("s_waitcnt vmcnt(" #n ")" ::: "memory")
; #define PG8_WAIT_L(n) asm volatile("s_waitcnt lgkmcnt(" #n ")" ::: "memory")
; #define PG8_BAR __builtin_amdgcn_s_barrier()
; #define PG8_SCHED __builtin_amdgcn_sched_barrier(0)
; template <class Epi, class Sched, bool ALIGN_EPI = false, bool SP2 = false, bool F8 = false, bool I8 = false, bool PF = false>
; __device__ __forceinline__ void gemm_phase(PG8_LAS unsigned char* lds, const Gemm g, const Sched& S, const Epi& E, const int wave_) {
;     ...
;             PG8_LDB(B0, 0, 0); PG8_LDB(B1, 0, 1); PG8_SCHED; PG8_LDA(At, 0, 0); PG8_STAGE(PG8_SA(1, 1), a1 + hstep, voffA);
;             PG8_WAIT_V(8); PG8_WAIT_L(0); PG8_BAR; PG8_MMA(0, 0, At, B0); PG8_MMA(0, 1, At, B1); PG8_BAR; PG8_SCHED;
;             PG8_LDA(At, 0, 1); PG8_STAGE(PG8_SB(0, 0), b2, voffB); PG8_STAGE(PG8_SB(0, 1), b2 + hstep, voffB); PG8_STAGE(PG8_SA(0, 0), a2, voffA);
;             PG8_WAIT_V(8); PG8_WAIT_L(0); PG8_BAR; PG8_MMA(1, 0, At, B0); PG8_MMA(1, 1, At, B1); PG8_BAR; PG8_SCHED;
.LBB0_671:
	ds_read_b128 v[24:27], v209
	ds_read_b128 v[28:31], v209 offset:1024
	ds_read_b128 v[16:19], v209 offset:2048
	ds_read_b128 v[20:23], v209 offset:3072
	ds_read_b128 v[8:11], v210
	ds_read_b128 v[12:15], v210 offset:1024
	ds_read_b128 v[0:3], v210 offset:2048
	ds_read_b128 v[4:7], v210 offset:3072
	s_add_u32 s28, s30, 0x100
	s_addc_u32 s29, s31, 0
	s_cmp_eq_u32 s65, 18
	s_cselect_b32 s37, s23, s29
	s_cselect_b32 s36, s22, s28
	s_cselect_b32 s35, s27, s64
	s_cselect_b32 s34, s26, s63
	v_lshl_add_u64 v[160:161], s[30:31], 0, v[172:173]
	s_add_i32 m0, s40, 0xc000
	ds_read_b128 v[178:181], v211
	ds_read_b128 v[182:185], v211 offset:1024
	ds_read_b128 v[186:189], v211 offset:2048
	ds_read_b128 v[190:193], v211 offset:3072
	ds_read_b128 v[194:197], v211 offset:4096
	ds_read_b128 v[198:201], v211 offset:5120
	ds_read_b128 v[212:215], v211 offset:6144
	ds_read_b128 v[216:219], v211 offset:7168
	global_load_lds_dwordx4 v[160:161], off
	v_lshl_add_u64 v[160:161], s[30:31], 0, v[174:175]
	s_add_i32 m0, s40, 0xe000
	s_nop 0
	global_load_lds_dwordx4 v[160:161], off
	s_waitcnt vmcnt(8)
	s_waitcnt lgkmcnt(0)
	s_setprio 0
	s_barrier
	s_waitcnt lgkmcnt(0)
	v_mfma_f32_16x16x128_f8f6f4 v[156:159], v[24:31], v[178:185], v[156:159]
	v_mfma_f32_16x16x128_f8f6f4 v[152:155], v[16:23], v[178:185], v[152:155]
	v_mfma_f32_16x16x128_f8f6f4 v[140:143], v[24:31], v[186:193], v[140:143]
	v_mfma_f32_16x16x128_f8f6f4 v[136:139], v[16:23], v[186:193], v[136:139]
	v_mfma_f32_16x16x128_f8f6f4 v[124:127], v[24:31], v[194:201], v[124:127]
	v_mfma_f32_16x16x128_f8f6f4 v[120:123], v[16:23], v[194:201], v[120:123]
	v_mfma_f32_16x16x128_f8f6f4 v[108:111], v[24:31], v[212:219], v[108:111]
	v_mfma_f32_16x16x128_f8f6f4 v[104:107], v[16:23], v[212:219], v[104:107]
	v_mfma_f32_16x16x128_f8f6f4 v[148:151], v[8:15], v[178:185], v[148:151]
	v_mfma_f32_16x16x128_f8f6f4 v[144:147], v[0:7], v[178:185], v[144:147]
	v_mfma_f32_16x16x128_f8f6f4 v[132:135], v[8:15], v[186:193], v[132:135]
	v_mfma_f32_16x16x128_f8f6f4 v[128:131], v[0:7], v[186:193], v[128:131]
	v_mfma_f32_16x16x128_f8f6f4 v[116:119], v[8:15], v[194:201], v[116:119]
	v_mfma_f32_16x16x128_f8f6f4 v[112:115], v[0:7], v[194:201], v[112:115]
	v_mfma_f32_16x16x128_f8f6f4 v[100:103], v[8:15], v[212:219], v[100:103]
	v_mfma_f32_16x16x128_f8f6f4 v[96:99], v[0:7], v[212:219], v[96:99]
	s_barrier
	s_setprio 1
	s_add_i32 s30, s53, s39
	v_lshl_add_u64 v[160:161], s[34:35], 0, v[168:169]
	s_mov_b32 m0, s30
	ds_read_b128 v[182:185], v211 offset:16384
	ds_read_b128 v[186:189], v211 offset:17408
	ds_read_b128 v[190:193], v211 offset:18432
	ds_read_b128 v[194:197], v211 offset:19456
	ds_read_b128 v[198:201], v211 offset:20480
	ds_read_b128 v[202:205], v211 offset:21504
	ds_read_b128 v[212:215], v211 offset:22528
	ds_read_b128 v[216:219], v211 offset:23552
	global_load_lds_dwordx4 v[160:161], off
	s_add_i32 m0, s30, 0x2000
	s_add_u32 s30, s34, 0x58000
	v_lshl_add_u64 v[162:163], s[34:35], 0, v[164:165]
	s_addc_u32 s31, s35, 0
	s_add_i32 s66, s54, s39
	global_load_lds_dwordx4 v[162:163], off
	v_lshl_add_u64 v[178:179], s[30:31], 0, v[168:169]
	s_mov_b32 m0, s66
	v_lshl_add_u64 v[180:181], s[36:37], 0, v[166:167]
	global_load_lds_dwordx4 v[178:179], off
	v_lshl_add_u64 v[178:179], s[30:31], 0, v[164:165]
	s_add_i32 m0, s66, 0x2000
	s_nop 0
	global_load_lds_dwordx4 v[178:179], off
	v_lshl_add_u64 v[178:179], s[36:37], 0, v[170:171]
	s_mov_b32 m0, s40
	s_nop 0
	global_load_lds_dwordx4 v[178:179], off
	s_mov_b32 m0, s41
	s_nop 0
	global_load_lds_dwordx4 v[180:181], off
	s_waitcnt vmcnt(8)
	s_waitcnt lgkmcnt(0)
	s_setprio 0
	s_barrier
	s_waitcnt lgkmcnt(0)
	v_mfma_f32_16x16x128_f8f6f4 v[92:95], v[24:31], v[182:189], v[92:95]
	v_mfma_f32_16x16x128_f8f6f4 v[88:91], v[16:23], v[182:189], v[88:91]
	v_mfma_f32_16x16x128_f8f6f4 v[76:79], v[24:31], v[190:197], v[76:79]
	v_mfma_f32_16x16x128_f8f6f4 v[72:75], v[16:23], v[190:197], v[72:75]
	v_mfma_f32_16x16x128_f8f6f4 v[60:63], v[24:31], v[198:205], v[60:63]
	v_mfma_f32_16x16x128_f8f6f4 v[56:59], v[16:23], v[198:205], v[56:59]
	v_mfma_f32_16x16x128_f8f6f4 v[44:47], v[24:31], v[212:219], v[44:47]
	v_mfma_f32_16x16x128_f8f6f4 v[40:43], v[16:23], v[212:219], v[40:43]
	v_mfma_f32_16x16x128_f8f6f4 v[84:87], v[8:15], v[182:189], v[84:87]
	v_mfma_f32_16x16x128_f8f6f4 v[80:83], v[0:7], v[182:189], v[80:83]
	v_mfma_f32_16x16x128_f8f6f4 v[68:71], v[8:15], v[190:197], v[68:71]
	v_mfma_f32_16x16x128_f8f6f4 v[64:67], v[0:7], v[190:197], v[64:67]
	v_mfma_f32_16x16x128_f8f6f4 v[52:55], v[8:15], v[198:205], v[52:55]
	v_mfma_f32_16x16x128_f8f6f4 v[48:51], v[0:7], v[198:205], v[48:51]
	v_mfma_f32_16x16x128_f8f6f4 v[36:39], v[8:15], v[212:219], v[36:39]
	v_mfma_f32_16x16x128_f8f6f4 v[32:35], v[0:7], v[212:219], v[32:35]
	s_barrier
; #define PG8_LDA(dst, b, h) do { _Pragma("unroll") for (int m = 0; m < 4; ++m) _Pragma("unroll") for (int k = 0; k < 2; ++k) dst[m][k] = *(const PG8_LAS bf16x8*)(lds + PG8_SA(b, h) + aoff + m * 2048 + k * 1024); } while (0)
; #define PG8_LDB(dst, b, h) do { _Pragma("unroll") for (int n = 0; n < 2; ++n) _Pragma("unroll") for (int k = 0; k < 2; ++k) dst[n][k] = *(const PG8_LAS bf16x8*)(lds + PG8_SB(b, h) + boff + n * 2048 + k * 1024); } while (0)
; #define PG8_WAIT_V(n) asm volatile("s_waitcnt vmcnt(" #n ")" ::: "memory")
; #define PG8_WAIT_L(n) asm volatile("s_waitcnt lgkmcnt(" #n ")" ::: "memory")
; #define PG8_BAR __builtin_amdgcn_s_barrier()
; #define PG8_SCHED __builtin_amdgcn_sched_barrier(0)
; template <class Epi, class Sched, bool ALIGN_EPI = false, bool SP2 = false, bool F8 = false, bool I8 = false, bool PF = false>
; __device__ __forceinline__ void gemm_phase(PG8_LAS unsigned char* lds, const Gemm g, const Sched& S, const Epi& E, const int wave_) {
;     ...
;         for (int t = 0; t < nt; t += 2) {
;             const bool last = (t == nt - 2);
;             const char* a1 = cA + (size_t)(t + 1) * kstep;
;             const char* a2 = last ? nA : cA + (size_t)(t + 2) * kstep; const char* b2 = last ? nB : cB + (size_t)(t + 2) * kstep;
;     ...
;             PG8_LDB(B0, 1, 0); PG8_LDB(B1, 1, 1); PG8_SCHED; PG8_LDA(At, 1, 0); PG8_STAGE(PG8_SA(0, 1), a2 + hstep, voffA);
;             PG8_WAIT_V(8); PG8_WAIT_L(0); PG8_BAR; PG8_MMA(0, 0, At, B0); PG8_MMA(0, 1, At, B1); PG8_BAR; PG8_SCHED;
;             PG8_LDA(At, 1, 1); PG8_STAGE(PG8_SB(1, 0), b3, voffB); PG8_STAGE(PG8_SB(1, 1), b3 + hstep, voffB); PG8_STAGE(PG8_SA(1, 0), a3, voffA);
;             PG8_WAIT_V(8); PG8_WAIT_L(0); PG8_BAR; PG8_MMA(1, 0, At, B0); PG8_MMA(1, 1, At, B1); PG8_BAR; PG8_SCHED;
	s_setprio 1
	s_add_i32 s66, 0, 0x18000
	s_add_i32 s67, 0, 0x1c000
	v_add_u32_e32 v12, s66, v208
	v_add_u32_e32 v28, s67, v208
	ds_read_b128 v[0:3], v12
	ds_read_b128 v[4:7], v12 offset:1024
	ds_read_b128 v[8:11], v12 offset:2048
	ds_read_b128 v[12:15], v12 offset:3072
	ds_read_b128 v[16:19], v28
	ds_read_b128 v[20:23], v28 offset:1024
	ds_read_b128 v[24:27], v28 offset:2048
	ds_read_b128 v[28:31], v28 offset:3072
	s_add_u32 s30, s36, 0x58000
	s_addc_u32 s31, s37, 0
	s_mov_b32 m0, s42
	v_lshl_add_u64 v[206:207], s[30:31], 0, v[170:171]
	ds_read_b128 v[182:185], v211 offset:32768
	ds_read_b128 v[186:189], v211 offset:33792
	ds_read_b128 v[190:193], v211 offset:34816
	ds_read_b128 v[194:197], v211 offset:35840
	ds_read_b128 v[198:201], v211 offset:36864
	ds_read_b128 v[202:205], v211 offset:37888
	ds_read_b128 v[212:215], v211 offset:38912
	ds_read_b128 v[216:219], v211 offset:39936
	global_load_lds_dwordx4 v[206:207], off
	v_lshl_add_u64 v[206:207], s[30:31], 0, v[166:167]
	s_mov_b32 m0, s43
	s_nop 0
	global_load_lds_dwordx4 v[206:207], off
	s_waitcnt vmcnt(8)
	s_waitcnt lgkmcnt(0)
	s_setprio 0
	s_barrier
	s_waitcnt lgkmcnt(0)
	v_mfma_f32_16x16x128_f8f6f4 v[156:159], v[0:7], v[182:189], v[156:159]
	v_mfma_f32_16x16x128_f8f6f4 v[152:155], v[8:15], v[182:189], v[152:155]
	v_mfma_f32_16x16x128_f8f6f4 v[140:143], v[0:7], v[190:197], v[140:143]
	v_mfma_f32_16x16x128_f8f6f4 v[136:139], v[8:15], v[190:197], v[136:139]
	v_mfma_f32_16x16x128_f8f6f4 v[124:127], v[0:7], v[198:205], v[124:127]
	v_mfma_f32_16x16x128_f8f6f4 v[120:123], v[8:15], v[198:205], v[120:123]
	v_mfma_f32_16x16x128_f8f6f4 v[108:111], v[0:7], v[212:219], v[108:111]
	v_mfma_f32_16x16x128_f8f6f4 v[104:107], v[8:15], v[212:219], v[104:107]
	v_mfma_f32_16x16x128_f8f6f4 v[148:151], v[16:23], v[182:189], v[148:151]
	v_mfma_f32_16x16x128_f8f6f4 v[144:147], v[24:31], v[182:189], v[144:147]
	v_mfma_f32_16x16x128_f8f6f4 v[132:135], v[16:23], v[190:197], v[132:135]
	v_mfma_f32_16x16x128_f8f6f4 v[128:131], v[24:31], v[190:197], v[128:131]
	v_mfma_f32_16x16x128_f8f6f4 v[116:119], v[16:23], v[198:205], v[116:119]
	v_mfma_f32_16x16x128_f8f6f4 v[112:115], v[24:31], v[198:205], v[112:115]
	v_mfma_f32_16x16x128_f8f6f4 v[100:103], v[16:23], v[212:219], v[100:103]
	v_mfma_f32_16x16x128_f8f6f4 v[96:99], v[24:31], v[212:219], v[96:99]
	s_barrier
	s_setprio 1
	s_add_i32 s30, s66, s39
	v_lshl_add_u64 v[160:161], v[160:161], 0, s[10:11]
	s_mov_b32 m0, s30
	ds_read_b128 v[182:185], v211 offset:49152
	ds_read_b128 v[186:189], v211 offset:50176
	ds_read_b128 v[190:193], v211 offset:51200
	ds_read_b128 v[194:197], v211 offset:52224
	ds_read_b128 v[198:201], v211 offset:53248
	ds_read_b128 v[202:205], v211 offset:54272
	ds_read_b128 v[212:215], v211 offset:55296
	ds_read_b128 v[216:219], v211 offset:56320
	global_load_lds_dwordx4 v[160:161], off
	s_add_i32 m0, s30, 0x2000
	s_add_u32 s30, s34, 0x58080
	v_lshl_add_u64 v[160:161], v[162:163], 0, s[10:11]
	s_addc_u32 s31, s35, 0
	s_add_i32 s34, s67, s39
	global_load_lds_dwordx4 v[160:161], off
	v_lshl_add_u64 v[160:161], s[30:31], 0, v[168:169]
	s_mov_b32 m0, s34
	s_nop 0
	global_load_lds_dwordx4 v[160:161], off
	v_lshl_add_u64 v[160:161], s[30:31], 0, v[164:165]
	s_add_i32 m0, s34, 0x2000
	s_nop 0
	global_load_lds_dwordx4 v[160:161], off
	v_lshl_add_u64 v[160:161], v[178:179], 0, s[10:11]
	s_mov_b32 m0, s50
	s_nop 0
	global_load_lds_dwordx4 v[160:161], off
	v_lshl_add_u64 v[160:161], v[180:181], 0, s[10:11]
	s_mov_b32 m0, s51
	s_nop 0
	global_load_lds_dwordx4 v[160:161], off
	s_waitcnt vmcnt(8)
	s_waitcnt lgkmcnt(0)
	s_setprio 0
	s_barrier
	s_waitcnt lgkmcnt(0)
	v_mfma_f32_16x16x128_f8f6f4 v[92:95], v[0:7], v[182:189], v[92:95]
	v_mfma_f32_16x16x128_f8f6f4 v[88:91], v[8:15], v[182:189], v[88:91]
	v_mfma_f32_16x16x128_f8f6f4 v[76:79], v[0:7], v[190:197], v[76:79]
	v_mfma_f32_16x16x128_f8f6f4 v[72:75], v[8:15], v[190:197], v[72:75]
	v_mfma_f32_16x16x128_f8f6f4 v[60:63], v[0:7], v[198:205], v[60:63]
	v_mfma_f32_16x16x128_f8f6f4 v[56:59], v[8:15], v[198:205], v[56:59]
	v_mfma_f32_16x16x128_f8f6f4 v[44:47], v[0:7], v[212:219], v[44:47]
	v_mfma_f32_16x16x128_f8f6f4 v[40:43], v[8:15], v[212:219], v[40:43]
	v_mfma_f32_16x16x128_f8f6f4 v[84:87], v[16:23], v[182:189], v[84:87]
	v_mfma_f32_16x16x128_f8f6f4 v[80:83], v[24:31], v[182:189], v[80:83]
	v_mfma_f32_16x16x128_f8f6f4 v[68:71], v[16:23], v[190:197], v[68:71]
	v_mfma_f32_16x16x128_f8f6f4 v[64:67], v[24:31], v[190:197], v[64:67]
	v_mfma_f32_16x16x128_f8f6f4 v[52:55], v[16:23], v[198:205], v[52:55]
	v_mfma_f32_16x16x128_f8f6f4 v[48:51], v[24:31], v[198:205], v[48:51]
	v_mfma_f32_16x16x128_f8f6f4 v[36:39], v[16:23], v[212:219], v[36:39]
	v_mfma_f32_16x16x128_f8f6f4 v[32:35], v[24:31], v[212:219], v[32:35]
	s_barrier
	s_setprio 1
	s_add_i32 s65, s65, 2
	s_add_u32 s63, s63, 0x100
	s_addc_u32 s64, s64, 0
	s_cmp_gt_u32 s65, 19
	s_mov_b64 s[30:31], s[28:29]
	s_cbranch_scc0 .LBB0_671
	s_setprio 0
	s_and_b64 vcc, exec, s[12:13]
	s_cbranch_vccz .LBB0_674
	s_barrier

; #define PG8_LDA(dst, b, h) do { _Pragma("unroll") for (int m = 0; m < 4; ++m) _Pragma("unroll") for (int k = 0; k < 2; ++k) dst[m][k] = *(const PG8_LAS bf16x8*)(lds + PG8_SA(b, h) + aoff + m * 2048 + k * 1024); } while (0)
; #define PG8_LDB(dst, b, h) do { _Pragma("unroll") for (int n = 0; n < 2; ++n) _Pragma("unroll") for (int k = 0; k < 2; ++k) dst[n][k] = *(const PG8_LAS bf16x8*)(lds + PG8_SB(b, h) + boff + n * 2048 + k * 1024); } while (0)
; #define PG8_WAIT_V(n) asm volatile("s_waitcnt vmcnt(" #n ")" ::: "memory")
; #define PG8_WAIT_L(n) asm volatile("s_waitcnt lgkmcnt(" #n ")" ::: "memory")
; #define PG8_BAR __builtin_amdgcn_s_barrier()
; #define PG8_SCHED __builtin_amdgcn_sched_barrier(0)
; template <class Epi, class Sched, bool ALIGN_EPI = false, bool SP2 = false, bool F8 = false, bool I8 = false, bool PF = false>
; __device__ __forceinline__ void gemm_phase(PG8_LAS unsigned char* lds, const Gemm g, const Sched& S, const Epi& E, const int wave_) {
;     ...
;             PG8_LDB(B0, 0, 0); PG8_LDB(B1, 0, 1); PG8_SCHED; PG8_LDA(At, 0, 0); PG8_STAGE(PG8_SA(1, 1), a1 + hstep, voffA);
;             PG8_WAIT_V(8); PG8_WAIT_L(0); PG8_BAR; PG8_MMA(0, 0, At, B0); PG8_MMA(0, 1, At, B1); PG8_BAR; PG8_SCHED;
;             PG8_LDA(At, 0, 1); PG8_STAGE(PG8_SB(0, 0), b2, voffB); PG8_STAGE(PG8_SB(0, 1), b2 + hstep, voffB); PG8_STAGE(PG8_SA(0, 0), a2, voffA);
;             PG8_WAIT_V(8); PG8_WAIT_L(0); PG8_BAR; PG8_MMA(1, 0, At, B0); PG8_MMA(1, 1, At, B1); PG8_BAR; PG8_SCHED;
.LBB0_809:
	ds_read_b128 v[142:145], v151
	ds_read_b128 v[156:159], v151 offset:1024
	ds_read_b128 v[160:163], v151 offset:2048
	ds_read_b128 v[164:167], v151 offset:3072
	ds_read_b128 v[168:171], v153
	ds_read_b128 v[172:175], v153 offset:1024
	ds_read_b128 v[176:179], v153 offset:2048
	ds_read_b128 v[180:183], v153 offset:3072
	s_add_u32 s34, s30, 0xfffe0080
	s_addc_u32 s35, s31, -1
	s_cmp_eq_u32 s63, 4
	s_cselect_b32 s37, s19, s35
	s_cselect_b32 s36, s55, s34
	s_cselect_b32 s35, s17, s62
	s_cselect_b32 s34, s56, s57
	v_lshl_add_u64 v[146:147], s[30:31], 0, v[136:137]
	s_add_i32 m0, s29, 0xc000
	ds_read_b128 v[184:187], v155
	ds_read_b128 v[188:191], v155 offset:1024
	ds_read_b128 v[192:195], v155 offset:2048
	ds_read_b128 v[196:199], v155 offset:3072
	ds_read_b128 v[200:203], v155 offset:4096
	ds_read_b128 v[204:207], v155 offset:5120
	ds_read_b128 v[208:211], v155 offset:6144
	ds_read_b128 v[212:215], v155 offset:7168
	global_load_lds_dwordx4 v[146:147], off
	v_lshl_add_u64 v[146:147], s[30:31], 0, v[138:139]
	s_add_i32 m0, s29, 0xe000
	s_nop 0
	global_load_lds_dwordx4 v[146:147], off
	s_waitcnt vmcnt(8)
	s_waitcnt lgkmcnt(0)
	s_setprio 0
	s_barrier
	s_waitcnt lgkmcnt(0)
	v_mfma_i32_16x16x64_i8 v[124:127], v[142:145], v[184:187], v[124:127]
	v_mfma_i32_16x16x64_i8 v[120:123], v[160:163], v[184:187], v[120:123]
	v_mfma_i32_16x16x64_i8 v[108:111], v[142:145], v[192:195], v[108:111]
	v_mfma_i32_16x16x64_i8 v[104:107], v[160:163], v[192:195], v[104:107]
	v_mfma_i32_16x16x64_i8 v[92:95], v[142:145], v[200:203], v[92:95]
	v_mfma_i32_16x16x64_i8 v[88:91], v[160:163], v[200:203], v[88:91]
	v_mfma_i32_16x16x64_i8 v[76:79], v[142:145], v[208:211], v[76:79]
	v_mfma_i32_16x16x64_i8 v[72:75], v[160:163], v[208:211], v[72:75]
	v_mfma_i32_16x16x64_i8 v[124:127], v[156:159], v[188:191], v[124:127]
	v_mfma_i32_16x16x64_i8 v[120:123], v[164:167], v[188:191], v[120:123]
	v_mfma_i32_16x16x64_i8 v[108:111], v[156:159], v[196:199], v[108:111]
	v_mfma_i32_16x16x64_i8 v[104:107], v[164:167], v[196:199], v[104:107]
	v_mfma_i32_16x16x64_i8 v[92:95], v[156:159], v[204:207], v[92:95]
	v_mfma_i32_16x16x64_i8 v[88:91], v[164:167], v[204:207], v[88:91]
	v_mfma_i32_16x16x64_i8 v[76:79], v[156:159], v[212:215], v[76:79]
	v_mfma_i32_16x16x64_i8 v[72:75], v[164:167], v[212:215], v[72:75]
	v_mfma_i32_16x16x64_i8 v[116:119], v[168:171], v[184:187], v[116:119]
	v_mfma_i32_16x16x64_i8 v[112:115], v[176:179], v[184:187], v[112:115]
	v_mfma_i32_16x16x64_i8 v[100:103], v[168:171], v[192:195], v[100:103]
	v_mfma_i32_16x16x64_i8 v[96:99], v[176:179], v[192:195], v[96:99]
	v_mfma_i32_16x16x64_i8 v[84:87], v[168:171], v[200:203], v[84:87]
	v_mfma_i32_16x16x64_i8 v[80:83], v[176:179], v[200:203], v[80:83]
	v_mfma_i32_16x16x64_i8 v[68:71], v[168:171], v[208:211], v[68:71]
	v_mfma_i32_16x16x64_i8 v[64:67], v[176:179], v[208:211], v[64:67]
	v_mfma_i32_16x16x64_i8 v[116:119], v[172:175], v[188:191], v[116:119]
	v_mfma_i32_16x16x64_i8 v[112:115], v[180:183], v[188:191], v[112:115]
	v_mfma_i32_16x16x64_i8 v[100:103], v[172:175], v[196:199], v[100:103]
	v_mfma_i32_16x16x64_i8 v[96:99], v[180:183], v[196:199], v[96:99]
	v_mfma_i32_16x16x64_i8 v[84:87], v[172:175], v[204:207], v[84:87]
	v_mfma_i32_16x16x64_i8 v[80:83], v[180:183], v[204:207], v[80:83]
	v_mfma_i32_16x16x64_i8 v[68:71], v[172:175], v[212:215], v[68:71]
	v_mfma_i32_16x16x64_i8 v[64:67], v[180:183], v[212:215], v[64:67]
	s_barrier
	s_setprio 1
	s_add_i32 s64, s51, s39
	v_lshl_add_u64 v[146:147], s[34:35], 0, v[132:133]
	s_mov_b32 m0, s64
	ds_read_b128 v[184:187], v155 offset:16384
	ds_read_b128 v[188:191], v155 offset:17408
	ds_read_b128 v[192:195], v155 offset:18432
	ds_read_b128 v[196:199], v155 offset:19456
	ds_read_b128 v[200:203], v155 offset:20480
	ds_read_b128 v[204:207], v155 offset:21504
	ds_read_b128 v[208:211], v155 offset:22528
	ds_read_b128 v[212:215], v155 offset:23552
	global_load_lds_dwordx4 v[146:147], off
	s_add_i32 m0, s64, 0x2000
	s_add_u32 s64, s34, 0x20000
	v_lshl_add_u64 v[216:217], s[34:35], 0, v[128:129]
	s_addc_u32 s65, s35, 0
	s_add_i32 s66, s52, s39
	global_load_lds_dwordx4 v[216:217], off
	v_lshl_add_u64 v[218:219], s[64:65], 0, v[132:133]
	s_mov_b32 m0, s66
	v_lshl_add_u64 v[220:221], s[36:37], 0, v[130:131]
	global_load_lds_dwordx4 v[218:219], off
	v_lshl_add_u64 v[218:219], s[64:65], 0, v[128:129]
	s_add_i32 m0, s66, 0x2000
	s_nop 0
	global_load_lds_dwordx4 v[218:219], off
	v_lshl_add_u64 v[218:219], s[36:37], 0, v[134:135]
	s_mov_b32 m0, s29
	s_nop 0
	global_load_lds_dwordx4 v[218:219], off
	s_mov_b32 m0, s41
	s_nop 0
	global_load_lds_dwordx4 v[220:221], off
	s_waitcnt vmcnt(8)
	s_waitcnt lgkmcnt(0)
	s_setprio 0
	s_barrier
; #define PG8_LDA(dst, b, h) do { _Pragma("unroll") for (int m = 0; m < 4; ++m) _Pragma("unroll") for (int k = 0; k < 2; ++k) dst[m][k] = *(const PG8_LAS bf16x8*)(lds + PG8_SA(b, h) + aoff + m * 2048 + k * 1024); } while (0)
; #define PG8_LDB(dst, b, h) do { _Pragma("unroll") for (int n = 0; n < 2; ++n) _Pragma("unroll") for (int k = 0; k < 2; ++k) dst[n][k] = *(const PG8_LAS bf16x8*)(lds + PG8_SB(b, h) + boff + n * 2048 + k * 1024); } while (0)
; #define PG8_WAIT_V(n) asm volatile("s_waitcnt vmcnt(" #n ")" ::: "memory")
; #define PG8_WAIT_L(n) asm volatile("s_waitcnt lgkmcnt(" #n ")" ::: "memory")
; #define PG8_BAR __builtin_amdgcn_s_barrier()
; #define PG8_SCHED __builtin_amdgcn_sched_barrier(0)
; template <class Epi, class Sched, bool ALIGN_EPI = false, bool SP2 = false, bool F8 = false, bool I8 = false, bool PF = false>
; __device__ __forceinline__ void gemm_phase(PG8_LAS unsigned char* lds, const Gemm g, const Sched& S, const Epi& E, const int wave_) {
;     ...
;             PG8_WAIT_V(8); PG8_WAIT_L(0); PG8_BAR; PG8_MMA(1, 0, At, B0); PG8_MMA(1, 1, At, B1); PG8_BAR; PG8_SCHED;
;             PG8_LDB(B0, 1, 0); PG8_LDB(B1, 1, 1); PG8_SCHED; PG8_LDA(At, 1, 0); PG8_STAGE(PG8_SA(0, 1), a2 + hstep, voffA);
;             PG8_WAIT_V(8); PG8_WAIT_L(0); PG8_BAR; PG8_MMA(0, 0, At, B0); PG8_MMA(0, 1, At, B1); PG8_BAR; PG8_SCHED;
	s_waitcnt lgkmcnt(0)
	v_mfma_i32_16x16x64_i8 v[60:63], v[142:145], v[184:187], v[60:63]
	v_mfma_i32_16x16x64_i8 v[56:59], v[160:163], v[184:187], v[56:59]
	v_mfma_i32_16x16x64_i8 v[44:47], v[142:145], v[192:195], v[44:47]
	v_mfma_i32_16x16x64_i8 v[40:43], v[160:163], v[192:195], v[40:43]
	v_mfma_i32_16x16x64_i8 v[28:31], v[142:145], v[200:203], v[28:31]
	v_mfma_i32_16x16x64_i8 v[24:27], v[160:163], v[200:203], v[24:27]
	v_mfma_i32_16x16x64_i8 v[12:15], v[142:145], v[208:211], v[12:15]
	v_mfma_i32_16x16x64_i8 v[8:11], v[160:163], v[208:211], v[8:11]
	v_mfma_i32_16x16x64_i8 v[60:63], v[156:159], v[188:191], v[60:63]
	v_mfma_i32_16x16x64_i8 v[56:59], v[164:167], v[188:191], v[56:59]
	v_mfma_i32_16x16x64_i8 v[44:47], v[156:159], v[196:199], v[44:47]
	v_mfma_i32_16x16x64_i8 v[40:43], v[164:167], v[196:199], v[40:43]
	v_mfma_i32_16x16x64_i8 v[28:31], v[156:159], v[204:207], v[28:31]
	v_mfma_i32_16x16x64_i8 v[24:27], v[164:167], v[204:207], v[24:27]
	v_mfma_i32_16x16x64_i8 v[12:15], v[156:159], v[212:215], v[12:15]
	v_mfma_i32_16x16x64_i8 v[8:11], v[164:167], v[212:215], v[8:11]
	v_mfma_i32_16x16x64_i8 v[52:55], v[168:171], v[184:187], v[52:55]
	v_mfma_i32_16x16x64_i8 v[48:51], v[176:179], v[184:187], v[48:51]
	v_mfma_i32_16x16x64_i8 v[36:39], v[168:171], v[192:195], v[36:39]
	v_mfma_i32_16x16x64_i8 v[32:35], v[176:179], v[192:195], v[32:35]
	v_mfma_i32_16x16x64_i8 v[20:23], v[168:171], v[200:203], v[20:23]
	v_mfma_i32_16x16x64_i8 v[16:19], v[176:179], v[200:203], v[16:19]
	v_mfma_i32_16x16x64_i8 v[4:7], v[168:171], v[208:211], v[4:7]
	v_mfma_i32_16x16x64_i8 v[0:3], v[176:179], v[208:211], v[0:3]
	v_mfma_i32_16x16x64_i8 v[52:55], v[172:175], v[188:191], v[52:55]
	v_mfma_i32_16x16x64_i8 v[48:51], v[180:183], v[188:191], v[48:51]
	v_mfma_i32_16x16x64_i8 v[36:39], v[172:175], v[196:199], v[36:39]
	v_mfma_i32_16x16x64_i8 v[32:35], v[180:183], v[196:199], v[32:35]
	v_mfma_i32_16x16x64_i8 v[20:23], v[172:175], v[204:207], v[20:23]
	v_mfma_i32_16x16x64_i8 v[16:19], v[180:183], v[204:207], v[16:19]
	v_mfma_i32_16x16x64_i8 v[4:7], v[172:175], v[212:215], v[4:7]
	v_mfma_i32_16x16x64_i8 v[0:3], v[180:183], v[212:215], v[0:3]
	s_barrier
	s_setprio 1
	s_add_i32 s64, 0, 0x18000
	v_add_u32_e32 v148, s64, v149
	s_add_i32 s65, 0, 0x1c000
	ds_read_b128 v[142:145], v148
	ds_read_b128 v[156:159], v148 offset:1024
	ds_read_b128 v[160:163], v148 offset:2048
	ds_read_b128 v[164:167], v148 offset:3072
	v_add_u32_e32 v148, s65, v149
	ds_read_b128 v[168:171], v148
	ds_read_b128 v[172:175], v148 offset:1024
	ds_read_b128 v[176:179], v148 offset:2048
	ds_read_b128 v[180:183], v148 offset:3072
	s_add_u32 s36, s36, 0x20000
	s_addc_u32 s37, s37, 0
	s_mov_b32 m0, s42
	v_lshl_add_u64 v[222:223], s[36:37], 0, v[134:135]
	ds_read_b128 v[184:187], v155 offset:32768
	ds_read_b128 v[188:191], v155 offset:33792
	ds_read_b128 v[192:195], v155 offset:34816
	ds_read_b128 v[196:199], v155 offset:35840
	ds_read_b128 v[200:203], v155 offset:36864
	ds_read_b128 v[204:207], v155 offset:37888
	ds_read_b128 v[208:211], v155 offset:38912
	ds_read_b128 v[212:215], v155 offset:39936
	global_load_lds_dwordx4 v[222:223], off
	v_lshl_add_u64 v[222:223], s[36:37], 0, v[130:131]
	s_mov_b32 m0, s43
	s_nop 0
	global_load_lds_dwordx4 v[222:223], off
	s_waitcnt vmcnt(8)
	s_waitcnt lgkmcnt(0)
	s_setprio 0
	s_barrier
	s_waitcnt lgkmcnt(0)
	v_mfma_i32_16x16x64_i8 v[124:127], v[142:145], v[184:187], v[124:127]
	v_mfma_i32_16x16x64_i8 v[120:123], v[160:163], v[184:187], v[120:123]
	v_mfma_i32_16x16x64_i8 v[108:111], v[142:145], v[192:195], v[108:111]
	v_mfma_i32_16x16x64_i8 v[104:107], v[160:163], v[192:195], v[104:107]
	v_mfma_i32_16x16x64_i8 v[92:95], v[142:145], v[200:203], v[92:95]
	v_mfma_i32_16x16x64_i8 v[88:91], v[160:163], v[200:203], v[88:91]
	v_mfma_i32_16x16x64_i8 v[76:79], v[142:145], v[208:211], v[76:79]
	v_mfma_i32_16x16x64_i8 v[72:75], v[160:163], v[208:211], v[72:75]
	v_mfma_i32_16x16x64_i8 v[124:127], v[156:159], v[188:191], v[124:127]
	v_mfma_i32_16x16x64_i8 v[120:123], v[164:167], v[188:191], v[120:123]
	v_mfma_i32_16x16x64_i8 v[108:111], v[156:159], v[196:199], v[108:111]
	v_mfma_i32_16x16x64_i8 v[104:107], v[164:167], v[196:199], v[104:107]
	v_mfma_i32_16x16x64_i8 v[92:95], v[156:159], v[204:207], v[92:95]
	v_mfma_i32_16x16x64_i8 v[88:91], v[164:167], v[204:207], v[88:91]
	v_mfma_i32_16x16x64_i8 v[76:79], v[156:159], v[212:215], v[76:79]
	v_mfma_i32_16x16x64_i8 v[72:75], v[164:167], v[212:215], v[72:75]
	v_mfma_i32_16x16x64_i8 v[116:119], v[168:171], v[184:187], v[116:119]
	v_mfma_i32_16x16x64_i8 v[112:115], v[176:179], v[184:187], v[112:115]
	v_mfma_i32_16x16x64_i8 v[100:103], v[168:171], v[192:195], v[100:103]
	v_mfma_i32_16x16x64_i8 v[96:99], v[176:179], v[192:195], v[96:99]
	v_mfma_i32_16x16x64_i8 v[84:87], v[168:171], v[200:203], v[84:87]
	v_mfma_i32_16x16x64_i8 v[80:83], v[176:179], v[200:203], v[80:83]
	v_mfma_i32_16x16x64_i8 v[68:71], v[168:171], v[208:211], v[68:71]
	v_mfma_i32_16x16x64_i8 v[64:67], v[176:179], v[208:211], v[64:67]
	v_mfma_i32_16x16x64_i8 v[116:119], v[172:175], v[188:191], v[116:119]
	v_mfma_i32_16x16x64_i8 v[112:115], v[180:183], v[188:191], v[112:115]
	v_mfma_i32_16x16x64_i8 v[100:103], v[172:175], v[196:199], v[100:103]
	v_mfma_i32_16x16x64_i8 v[96:99], v[180:183], v[196:199], v[96:99]
	v_mfma_i32_16x16x64_i8 v[84:87], v[172:175], v[204:207], v[84:87]
	v_mfma_i32_16x16x64_i8 v[80:83], v[180:183], v[204:207], v[80:83]
	v_mfma_i32_16x16x64_i8 v[68:71], v[172:175], v[212:215], v[68:71]
	v_mfma_i32_16x16x64_i8 v[64:67], v[180:183], v[212:215], v[64:67]
	s_barrier
; #define PG8_LDA(dst, b, h) do { _Pragma("unroll") for (int m = 0; m < 4; ++m) _Pragma("unroll") for (int k = 0; k < 2; ++k) dst[m][k] = *(const PG8_LAS bf16x8*)(lds + PG8_SA(b, h) + aoff + m * 2048 + k * 1024); } while (0)
; #define PG8_WAIT_V(n) asm volatile("s_waitcnt vmcnt(" #n ")" ::: "memory")
; #define PG8_WAIT_L(n) asm volatile("s_waitcnt lgkmcnt(" #n ")" ::: "memory")
; #define PG8_BAR __builtin_amdgcn_s_barrier()
; #define PG8_SCHED __builtin_amdgcn_sched_barrier(0)
; template <class Epi, class Sched, bool ALIGN_EPI = false, bool SP2 = false, bool F8 = false, bool I8 = false, bool PF = false>
; __device__ __forceinline__ void gemm_phase(PG8_LAS unsigned char* lds, const Gemm g, const Sched& S, const Epi& E, const int wave_) {
;     ...
;         for (int t = 0; t < nt; t += 2) {
;             const bool last = (t == nt - 2);
;             const char* a1 = cA + (size_t)(t + 1) * kstep;
;             const char* a2 = last ? nA : cA + (size_t)(t + 2) * kstep; const char* b2 = last ? nB : cB + (size_t)(t + 2) * kstep;
;             const char* a3 = a2 + kstep; const char* b3 = b2 + kstep;
;             if (last && has_next) S.a_ready(nxt);
;     ...
;             PG8_LDA(At, 1, 1); PG8_STAGE(PG8_SB(1, 0), b3, voffB); PG8_STAGE(PG8_SB(1, 1), b3 + hstep, voffB); PG8_STAGE(PG8_SA(1, 0), a3, voffA);
;             PG8_WAIT_V(8); PG8_WAIT_L(0); PG8_BAR; PG8_MMA(1, 0, At, B0); PG8_MMA(1, 1, At, B1); PG8_BAR; PG8_SCHED;
	s_setprio 1
	s_add_i32 s36, s64, s39
	v_lshl_add_u64 v[146:147], v[146:147], 0, s[10:11]
	s_mov_b32 m0, s36
	ds_read_b128 v[184:187], v155 offset:49152
	ds_read_b128 v[188:191], v155 offset:50176
	ds_read_b128 v[192:195], v155 offset:51200
	ds_read_b128 v[196:199], v155 offset:52224
	ds_read_b128 v[200:203], v155 offset:53248
	ds_read_b128 v[204:207], v155 offset:54272
	ds_read_b128 v[208:211], v155 offset:55296
	ds_read_b128 v[212:215], v155 offset:56320
	global_load_lds_dwordx4 v[146:147], off
	s_add_i32 m0, s36, 0x2000
	s_add_u32 s34, s34, 0x20080
	v_lshl_add_u64 v[146:147], v[216:217], 0, s[10:11]
	s_addc_u32 s35, s35, 0
	s_add_i32 s36, s65, s39
	global_load_lds_dwordx4 v[146:147], off
	v_lshl_add_u64 v[146:147], s[34:35], 0, v[132:133]
	s_mov_b32 m0, s36
	s_nop 0
	global_load_lds_dwordx4 v[146:147], off
	v_lshl_add_u64 v[146:147], s[34:35], 0, v[128:129]
	s_add_i32 m0, s36, 0x2000
	s_nop 0
	global_load_lds_dwordx4 v[146:147], off
	v_lshl_add_u64 v[146:147], v[218:219], 0, s[10:11]
	s_mov_b32 m0, s48
	s_nop 0
	global_load_lds_dwordx4 v[146:147], off
	v_lshl_add_u64 v[146:147], v[220:221], 0, s[10:11]
	s_mov_b32 m0, s49
	s_nop 0
	global_load_lds_dwordx4 v[146:147], off
	s_waitcnt vmcnt(8)
	s_waitcnt lgkmcnt(0)
	s_setprio 0
	s_barrier
	s_waitcnt lgkmcnt(0)
	v_mfma_i32_16x16x64_i8 v[60:63], v[142:145], v[184:187], v[60:63]
	v_mfma_i32_16x16x64_i8 v[56:59], v[160:163], v[184:187], v[56:59]
	v_mfma_i32_16x16x64_i8 v[44:47], v[142:145], v[192:195], v[44:47]
	v_mfma_i32_16x16x64_i8 v[40:43], v[160:163], v[192:195], v[40:43]
	v_mfma_i32_16x16x64_i8 v[28:31], v[142:145], v[200:203], v[28:31]
	v_mfma_i32_16x16x64_i8 v[24:27], v[160:163], v[200:203], v[24:27]
	v_mfma_i32_16x16x64_i8 v[12:15], v[142:145], v[208:211], v[12:15]
	v_mfma_i32_16x16x64_i8 v[8:11], v[160:163], v[208:211], v[8:11]
	v_mfma_i32_16x16x64_i8 v[60:63], v[156:159], v[188:191], v[60:63]
	v_mfma_i32_16x16x64_i8 v[56:59], v[164:167], v[188:191], v[56:59]
	v_mfma_i32_16x16x64_i8 v[44:47], v[156:159], v[196:199], v[44:47]
	v_mfma_i32_16x16x64_i8 v[40:43], v[164:167], v[196:199], v[40:43]
	v_mfma_i32_16x16x64_i8 v[28:31], v[156:159], v[204:207], v[28:31]
	v_mfma_i32_16x16x64_i8 v[24:27], v[164:167], v[204:207], v[24:27]
	v_mfma_i32_16x16x64_i8 v[12:15], v[156:159], v[212:215], v[12:15]
	v_mfma_i32_16x16x64_i8 v[8:11], v[164:167], v[212:215], v[8:11]
	v_mfma_i32_16x16x64_i8 v[52:55], v[168:171], v[184:187], v[52:55]
	v_mfma_i32_16x16x64_i8 v[48:51], v[176:179], v[184:187], v[48:51]
	v_mfma_i32_16x16x64_i8 v[36:39], v[168:171], v[192:195], v[36:39]
	v_mfma_i32_16x16x64_i8 v[32:35], v[176:179], v[192:195], v[32:35]
	v_mfma_i32_16x16x64_i8 v[20:23], v[168:171], v[200:203], v[20:23]
	v_mfma_i32_16x16x64_i8 v[16:19], v[176:179], v[200:203], v[16:19]
	v_mfma_i32_16x16x64_i8 v[4:7], v[168:171], v[208:211], v[4:7]
	v_mfma_i32_16x16x64_i8 v[0:3], v[176:179], v[208:211], v[0:3]
	v_mfma_i32_16x16x64_i8 v[52:55], v[172:175], v[188:191], v[52:55]
	v_mfma_i32_16x16x64_i8 v[48:51], v[180:183], v[188:191], v[48:51]
	v_mfma_i32_16x16x64_i8 v[36:39], v[172:175], v[196:199], v[36:39]
	v_mfma_i32_16x16x64_i8 v[32:35], v[180:183], v[196:199], v[32:35]
	v_mfma_i32_16x16x64_i8 v[20:23], v[172:175], v[204:207], v[20:23]
	v_mfma_i32_16x16x64_i8 v[16:19], v[180:183], v[204:207], v[16:19]
	v_mfma_i32_16x16x64_i8 v[4:7], v[172:175], v[212:215], v[4:7]
	v_mfma_i32_16x16x64_i8 v[0:3], v[180:183], v[212:215], v[0:3]
	s_barrier
	s_setprio 1
	s_add_i32 s63, s63, 2
	s_add_u32 s30, s30, 0x100
	s_addc_u32 s31, s31, 0
	s_add_u32 s57, s57, 0x100
	s_addc_u32 s62, s62, 0
	s_cmp_gt_u32 s63, 5
	s_cbranch_scc0 .LBB0_809
	s_setprio 0
	s_and_b64 vcc, exec, s[12:13]
	s_cbranch_vccz .LBB0_812
	s_barrier

; #define PG8_LDA(dst, b, h) do { _Pragma("unroll") for (int m = 0; m < 4; ++m) _Pragma("unroll") for (int k = 0; k < 2; ++k) dst[m][k] = *(const PG8_LAS bf16x8*)(lds + PG8_SA(b, h) + aoff + m * 2048 + k * 1024); } while (0)
; #define PG8_LDB(dst, b, h) do { _Pragma("unroll") for (int n = 0; n < 2; ++n) _Pragma("unroll") for (int k = 0; k < 2; ++k) dst[n][k] = *(const PG8_LAS bf16x8*)(lds + PG8_SB(b, h) + boff + n * 2048 + k * 1024); } while (0)
; #define PG8_WAIT_V(n) asm volatile("s_waitcnt vmcnt(" #n ")" ::: "memory")
; #define PG8_WAIT_L(n) asm volatile("s_waitcnt lgkmcnt(" #n ")" ::: "memory")
; #define PG8_BAR __builtin_amdgcn_s_barrier()
; #define PG8_SCHED __builtin_amdgcn_sched_barrier(0)
; template <class Epi, class Sched, bool ALIGN_EPI = false, bool SP2 = false, bool F8 = false, bool I8 = false, bool PF = false>
; __device__ __forceinline__ void gemm_phase(PG8_LAS unsigned char* lds, const Gemm g, const Sched& S, const Epi& E, const int wave_) {
;     ...
;             PG8_LDB(B0, 0, 0); PG8_LDB(B1, 0, 1); PG8_SCHED; PG8_LDA(At, 0, 0); PG8_STAGE(PG8_SA(1, 1), a1 + hstep, voffA);
;             PG8_WAIT_V(8); PG8_WAIT_L(0); PG8_BAR; PG8_MMA(0, 0, At, B0); PG8_MMA(0, 1, At, B1); PG8_BAR; PG8_SCHED;
;             PG8_LDA(At, 0, 1); PG8_STAGE(PG8_SB(0, 0), b2, voffB); PG8_STAGE(PG8_SB(0, 1), b2 + hstep, voffB); PG8_STAGE(PG8_SA(0, 0), a2, voffA);
;             PG8_WAIT_V(8); PG8_WAIT_L(0); PG8_BAR; PG8_MMA(1, 0, At, B0); PG8_MMA(1, 1, At, B1); PG8_BAR; PG8_SCHED;
.LBB0_967:
	ds_read_b128 v[144:147], v151
	ds_read_b128 v[154:157], v151 offset:1024
	ds_read_b128 v[158:161], v151 offset:2048
	ds_read_b128 v[162:165], v151 offset:3072
	ds_read_b128 v[166:169], v152
	ds_read_b128 v[170:173], v152 offset:1024
	ds_read_b128 v[174:177], v152 offset:2048
	ds_read_b128 v[178:181], v152 offset:3072
	s_add_u32 s40, s38, 0xfffe0080
	s_addc_u32 s41, s39, -1
	s_cmp_eq_u32 s72, 4
	s_cselect_b32 s43, s5, s41
	s_cselect_b32 s42, s27, s40
	s_cselect_b32 s41, s23, s71
	s_cselect_b32 s40, s37, s70
	v_lshl_add_u64 v[148:149], s[38:39], 0, v[138:139]
	s_add_i32 m0, s51, 0xc000
	ds_read_b128 v[182:185], v153
	ds_read_b128 v[186:189], v153 offset:1024
	ds_read_b128 v[190:193], v153 offset:2048
	ds_read_b128 v[194:197], v153 offset:3072
	ds_read_b128 v[198:201], v153 offset:4096
	ds_read_b128 v[202:205], v153 offset:5120
	ds_read_b128 v[206:209], v153 offset:6144
	ds_read_b128 v[210:213], v153 offset:7168
	global_load_lds_dwordx4 v[148:149], off
	v_lshl_add_u64 v[148:149], s[38:39], 0, v[140:141]
	s_add_i32 m0, s51, 0xe000
	s_nop 0
	global_load_lds_dwordx4 v[148:149], off
	s_waitcnt vmcnt(8)
	s_waitcnt lgkmcnt(0)
	s_setprio 0
	s_barrier
	s_waitcnt lgkmcnt(0)
	v_mfma_f32_16x16x32_bf16 v[124:127], v[144:147], v[182:185], v[124:127]
	v_mfma_f32_16x16x32_bf16 v[120:123], v[158:161], v[182:185], v[120:123]
	v_mfma_f32_16x16x32_bf16 v[108:111], v[144:147], v[190:193], v[108:111]
	v_mfma_f32_16x16x32_bf16 v[104:107], v[158:161], v[190:193], v[104:107]
	v_mfma_f32_16x16x32_bf16 v[92:95], v[144:147], v[198:201], v[92:95]
	v_mfma_f32_16x16x32_bf16 v[88:91], v[158:161], v[198:201], v[88:91]
	v_mfma_f32_16x16x32_bf16 v[76:79], v[144:147], v[206:209], v[76:79]
	v_mfma_f32_16x16x32_bf16 v[72:75], v[158:161], v[206:209], v[72:75]
	v_mfma_f32_16x16x32_bf16 v[124:127], v[154:157], v[186:189], v[124:127]
	v_mfma_f32_16x16x32_bf16 v[120:123], v[162:165], v[186:189], v[120:123]
	v_mfma_f32_16x16x32_bf16 v[108:111], v[154:157], v[194:197], v[108:111]
	v_mfma_f32_16x16x32_bf16 v[104:107], v[162:165], v[194:197], v[104:107]
	v_mfma_f32_16x16x32_bf16 v[92:95], v[154:157], v[202:205], v[92:95]
	v_mfma_f32_16x16x32_bf16 v[88:91], v[162:165], v[202:205], v[88:91]
	v_mfma_f32_16x16x32_bf16 v[76:79], v[154:157], v[210:213], v[76:79]
	v_mfma_f32_16x16x32_bf16 v[72:75], v[162:165], v[210:213], v[72:75]
	v_mfma_f32_16x16x32_bf16 v[116:119], v[166:169], v[182:185], v[116:119]
	v_mfma_f32_16x16x32_bf16 v[112:115], v[174:177], v[182:185], v[112:115]
	v_mfma_f32_16x16x32_bf16 v[100:103], v[166:169], v[190:193], v[100:103]
	v_mfma_f32_16x16x32_bf16 v[96:99], v[174:177], v[190:193], v[96:99]
	v_mfma_f32_16x16x32_bf16 v[84:87], v[166:169], v[198:201], v[84:87]
	v_mfma_f32_16x16x32_bf16 v[80:83], v[174:177], v[198:201], v[80:83]
	v_mfma_f32_16x16x32_bf16 v[68:71], v[166:169], v[206:209], v[68:71]
	v_mfma_f32_16x16x32_bf16 v[64:67], v[174:177], v[206:209], v[64:67]
	v_mfma_f32_16x16x32_bf16 v[116:119], v[170:173], v[186:189], v[116:119]
	v_mfma_f32_16x16x32_bf16 v[112:115], v[178:181], v[186:189], v[112:115]
	v_mfma_f32_16x16x32_bf16 v[100:103], v[170:173], v[194:197], v[100:103]
	v_mfma_f32_16x16x32_bf16 v[96:99], v[178:181], v[194:197], v[96:99]
	v_mfma_f32_16x16x32_bf16 v[84:87], v[170:173], v[202:205], v[84:87]
	v_mfma_f32_16x16x32_bf16 v[80:83], v[178:181], v[202:205], v[80:83]
	v_mfma_f32_16x16x32_bf16 v[68:71], v[170:173], v[210:213], v[68:71]
	v_mfma_f32_16x16x32_bf16 v[64:67], v[178:181], v[210:213], v[64:67]
	s_barrier
	s_setprio 1
	s_add_i32 s73, s67, s48
	v_lshl_add_u64 v[148:149], s[40:41], 0, v[130:131]
	s_mov_b32 m0, s73
	ds_read_b128 v[182:185], v153 offset:16384
	ds_read_b128 v[186:189], v153 offset:17408
	ds_read_b128 v[190:193], v153 offset:18432
	ds_read_b128 v[194:197], v153 offset:19456
	ds_read_b128 v[198:201], v153 offset:20480
	ds_read_b128 v[202:205], v153 offset:21504
	ds_read_b128 v[206:209], v153 offset:22528
	ds_read_b128 v[210:213], v153 offset:23552
	global_load_lds_dwordx4 v[148:149], off
	s_add_i32 m0, s73, 0x2000
	s_add_u32 s74, s40, 0x20000
	v_lshl_add_u64 v[214:215], s[40:41], 0, v[134:135]
	s_addc_u32 s75, s41, 0
	s_add_i32 s73, s68, s48
	global_load_lds_dwordx4 v[214:215], off
	v_lshl_add_u64 v[216:217], s[74:75], 0, v[130:131]
	s_mov_b32 m0, s73
	v_lshl_add_u64 v[218:219], s[42:43], 0, v[132:133]
	global_load_lds_dwordx4 v[216:217], off
	v_lshl_add_u64 v[216:217], s[74:75], 0, v[134:135]
	s_add_i32 m0, s73, 0x2000
	s_nop 0
	global_load_lds_dwordx4 v[216:217], off
	v_lshl_add_u64 v[216:217], s[42:43], 0, v[128:129]
	s_mov_b32 m0, s51
	s_nop 0
	global_load_lds_dwordx4 v[216:217], off
	s_mov_b32 m0, s52
	s_nop 0
	global_load_lds_dwordx4 v[218:219], off
	s_waitcnt vmcnt(8)
	s_waitcnt lgkmcnt(0)
	s_setprio 0
	s_barrier
; #define PG8_LDA(dst, b, h) do { _Pragma("unroll") for (int m = 0; m < 4; ++m) _Pragma("unroll") for (int k = 0; k < 2; ++k) dst[m][k] = *(const PG8_LAS bf16x8*)(lds + PG8_SA(b, h) + aoff + m * 2048 + k * 1024); } while (0)
; #define PG8_LDB(dst, b, h) do { _Pragma("unroll") for (int n = 0; n < 2; ++n) _Pragma("unroll") for (int k = 0; k < 2; ++k) dst[n][k] = *(const PG8_LAS bf16x8*)(lds + PG8_SB(b, h) + boff + n * 2048 + k * 1024); } while (0)
; #define PG8_WAIT_V(n) asm volatile("s_waitcnt vmcnt(" #n ")" ::: "memory")
; #define PG8_WAIT_L(n) asm volatile("s_waitcnt lgkmcnt(" #n ")" ::: "memory")
; #define PG8_BAR __builtin_amdgcn_s_barrier()
; #define PG8_SCHED __builtin_amdgcn_sched_barrier(0)
; template <class Epi, class Sched, bool ALIGN_EPI = false, bool SP2 = false, bool F8 = false, bool I8 = false, bool PF = false>
; __device__ __forceinline__ void gemm_phase(PG8_LAS unsigned char* lds, const Gemm g, const Sched& S, const Epi& E, const int wave_) {
;     ...
;             PG8_WAIT_V(8); PG8_WAIT_L(0); PG8_BAR; PG8_MMA(1, 0, At, B0); PG8_MMA(1, 1, At, B1); PG8_BAR; PG8_SCHED;
;             PG8_LDB(B0, 1, 0); PG8_LDB(B1, 1, 1); PG8_SCHED; PG8_LDA(At, 1, 0); PG8_STAGE(PG8_SA(0, 1), a2 + hstep, voffA);
;             PG8_WAIT_V(8); PG8_WAIT_L(0); PG8_BAR; PG8_MMA(0, 0, At, B0); PG8_MMA(0, 1, At, B1); PG8_BAR; PG8_SCHED;
	s_waitcnt lgkmcnt(0)
	v_mfma_f32_16x16x32_bf16 v[60:63], v[144:147], v[182:185], v[60:63]
	v_mfma_f32_16x16x32_bf16 v[56:59], v[158:161], v[182:185], v[56:59]
	v_mfma_f32_16x16x32_bf16 v[44:47], v[144:147], v[190:193], v[44:47]
	v_mfma_f32_16x16x32_bf16 v[40:43], v[158:161], v[190:193], v[40:43]
	v_mfma_f32_16x16x32_bf16 v[28:31], v[144:147], v[198:201], v[28:31]
	v_mfma_f32_16x16x32_bf16 v[24:27], v[158:161], v[198:201], v[24:27]
	v_mfma_f32_16x16x32_bf16 v[12:15], v[144:147], v[206:209], v[12:15]
	v_mfma_f32_16x16x32_bf16 v[8:11], v[158:161], v[206:209], v[8:11]
	v_mfma_f32_16x16x32_bf16 v[60:63], v[154:157], v[186:189], v[60:63]
	v_mfma_f32_16x16x32_bf16 v[56:59], v[162:165], v[186:189], v[56:59]
	v_mfma_f32_16x16x32_bf16 v[44:47], v[154:157], v[194:197], v[44:47]
	v_mfma_f32_16x16x32_bf16 v[40:43], v[162:165], v[194:197], v[40:43]
	v_mfma_f32_16x16x32_bf16 v[28:31], v[154:157], v[202:205], v[28:31]
	v_mfma_f32_16x16x32_bf16 v[24:27], v[162:165], v[202:205], v[24:27]
	v_mfma_f32_16x16x32_bf16 v[12:15], v[154:157], v[210:213], v[12:15]
	v_mfma_f32_16x16x32_bf16 v[8:11], v[162:165], v[210:213], v[8:11]
	v_mfma_f32_16x16x32_bf16 v[52:55], v[166:169], v[182:185], v[52:55]
	v_mfma_f32_16x16x32_bf16 v[48:51], v[174:177], v[182:185], v[48:51]
	v_mfma_f32_16x16x32_bf16 v[36:39], v[166:169], v[190:193], v[36:39]
	v_mfma_f32_16x16x32_bf16 v[32:35], v[174:177], v[190:193], v[32:35]
	v_mfma_f32_16x16x32_bf16 v[20:23], v[166:169], v[198:201], v[20:23]
	v_mfma_f32_16x16x32_bf16 v[16:19], v[174:177], v[198:201], v[16:19]
	v_mfma_f32_16x16x32_bf16 v[4:7], v[166:169], v[206:209], v[4:7]
	v_mfma_f32_16x16x32_bf16 v[0:3], v[174:177], v[206:209], v[0:3]
	v_mfma_f32_16x16x32_bf16 v[52:55], v[170:173], v[186:189], v[52:55]
	v_mfma_f32_16x16x32_bf16 v[48:51], v[178:181], v[186:189], v[48:51]
	v_mfma_f32_16x16x32_bf16 v[36:39], v[170:173], v[194:197], v[36:39]
	v_mfma_f32_16x16x32_bf16 v[32:35], v[178:181], v[194:197], v[32:35]
	v_mfma_f32_16x16x32_bf16 v[20:23], v[170:173], v[202:205], v[20:23]
	v_mfma_f32_16x16x32_bf16 v[16:19], v[178:181], v[202:205], v[16:19]
	v_mfma_f32_16x16x32_bf16 v[4:7], v[170:173], v[210:213], v[4:7]
	v_mfma_f32_16x16x32_bf16 v[0:3], v[178:181], v[210:213], v[0:3]
	s_barrier
	s_setprio 1
	s_add_i32 s73, 0, 0x18000
	v_add_u32_e32 v136, s73, v150
	s_add_i32 s74, 0, 0x1c000
	ds_read_b128 v[144:147], v136
	ds_read_b128 v[154:157], v136 offset:1024
	ds_read_b128 v[158:161], v136 offset:2048
	ds_read_b128 v[162:165], v136 offset:3072
	v_add_u32_e32 v136, s74, v150
	ds_read_b128 v[166:169], v136
	ds_read_b128 v[170:173], v136 offset:1024
	ds_read_b128 v[174:177], v136 offset:2048
	ds_read_b128 v[178:181], v136 offset:3072
	s_add_u32 s42, s42, 0x20000
	s_addc_u32 s43, s43, 0
	s_mov_b32 m0, s53
	v_lshl_add_u64 v[220:221], s[42:43], 0, v[128:129]
	ds_read_b128 v[182:185], v153 offset:32768
	ds_read_b128 v[186:189], v153 offset:33792
	ds_read_b128 v[190:193], v153 offset:34816
	ds_read_b128 v[194:197], v153 offset:35840
	ds_read_b128 v[198:201], v153 offset:36864
	ds_read_b128 v[202:205], v153 offset:37888
	ds_read_b128 v[206:209], v153 offset:38912
	ds_read_b128 v[210:213], v153 offset:39936
	global_load_lds_dwordx4 v[220:221], off
	v_lshl_add_u64 v[220:221], s[42:43], 0, v[132:133]
	s_mov_b32 m0, s54
	s_nop 0
	global_load_lds_dwordx4 v[220:221], off
	s_waitcnt vmcnt(8)
	s_waitcnt lgkmcnt(0)
	s_setprio 0
	s_barrier
	s_waitcnt lgkmcnt(0)
	v_mfma_f32_16x16x32_bf16 v[124:127], v[144:147], v[182:185], v[124:127]
	v_mfma_f32_16x16x32_bf16 v[120:123], v[158:161], v[182:185], v[120:123]
	v_mfma_f32_16x16x32_bf16 v[108:111], v[144:147], v[190:193], v[108:111]
	v_mfma_f32_16x16x32_bf16 v[104:107], v[158:161], v[190:193], v[104:107]
	v_mfma_f32_16x16x32_bf16 v[92:95], v[144:147], v[198:201], v[92:95]
	v_mfma_f32_16x16x32_bf16 v[88:91], v[158:161], v[198:201], v[88:91]
	v_mfma_f32_16x16x32_bf16 v[76:79], v[144:147], v[206:209], v[76:79]
	v_mfma_f32_16x16x32_bf16 v[72:75], v[158:161], v[206:209], v[72:75]
	v_mfma_f32_16x16x32_bf16 v[124:127], v[154:157], v[186:189], v[124:127]
	v_mfma_f32_16x16x32_bf16 v[120:123], v[162:165], v[186:189], v[120:123]
	v_mfma_f32_16x16x32_bf16 v[108:111], v[154:157], v[194:197], v[108:111]
	v_mfma_f32_16x16x32_bf16 v[104:107], v[162:165], v[194:197], v[104:107]
	v_mfma_f32_16x16x32_bf16 v[92:95], v[154:157], v[202:205], v[92:95]
	v_mfma_f32_16x16x32_bf16 v[88:91], v[162:165], v[202:205], v[88:91]
	v_mfma_f32_16x16x32_bf16 v[76:79], v[154:157], v[210:213], v[76:79]
	v_mfma_f32_16x16x32_bf16 v[72:75], v[162:165], v[210:213], v[72:75]
	v_mfma_f32_16x16x32_bf16 v[116:119], v[166:169], v[182:185], v[116:119]
	v_mfma_f32_16x16x32_bf16 v[112:115], v[174:177], v[182:185], v[112:115]
	v_mfma_f32_16x16x32_bf16 v[100:103], v[166:169], v[190:193], v[100:103]
	v_mfma_f32_16x16x32_bf16 v[96:99], v[174:177], v[190:193], v[96:99]
	v_mfma_f32_16x16x32_bf16 v[84:87], v[166:169], v[198:201], v[84:87]
	v_mfma_f32_16x16x32_bf16 v[80:83], v[174:177], v[198:201], v[80:83]
	v_mfma_f32_16x16x32_bf16 v[68:71], v[166:169], v[206:209], v[68:71]
	v_mfma_f32_16x16x32_bf16 v[64:67], v[174:177], v[206:209], v[64:67]
	v_mfma_f32_16x16x32_bf16 v[116:119], v[170:173], v[186:189], v[116:119]
	v_mfma_f32_16x16x32_bf16 v[112:115], v[178:181], v[186:189], v[112:115]
	v_mfma_f32_16x16x32_bf16 v[100:103], v[170:173], v[194:197], v[100:103]
	v_mfma_f32_16x16x32_bf16 v[96:99], v[178:181], v[194:197], v[96:99]
	v_mfma_f32_16x16x32_bf16 v[84:87], v[170:173], v[202:205], v[84:87]
	v_mfma_f32_16x16x32_bf16 v[80:83], v[178:181], v[202:205], v[80:83]
	v_mfma_f32_16x16x32_bf16 v[68:71], v[170:173], v[210:213], v[68:71]
	v_mfma_f32_16x16x32_bf16 v[64:67], v[178:181], v[210:213], v[64:67]
	s_barrier
; #define PG8_LDA(dst, b, h) do { _Pragma("unroll") for (int m = 0; m < 4; ++m) _Pragma("unroll") for (int k = 0; k < 2; ++k) dst[m][k] = *(const PG8_LAS bf16x8*)(lds + PG8_SA(b, h) + aoff + m * 2048 + k * 1024); } while (0)
; #define PG8_WAIT_V(n) asm volatile("s_waitcnt vmcnt(" #n ")" ::: "memory")
; #define PG8_WAIT_L(n) asm volatile("s_waitcnt lgkmcnt(" #n ")" ::: "memory")
; #define PG8_BAR __builtin_amdgcn_s_barrier()
; #define PG8_SCHED __builtin_amdgcn_sched_barrier(0)
; template <class Epi, class Sched, bool ALIGN_EPI = false, bool SP2 = false, bool F8 = false, bool I8 = false, bool PF = false>
; __device__ __forceinline__ void gemm_phase(PG8_LAS unsigned char* lds, const Gemm g, const Sched& S, const Epi& E, const int wave_) {
;     ...
;         for (int t = 0; t < nt; t += 2) {
;             const bool last = (t == nt - 2);
;             const char* a1 = cA + (size_t)(t + 1) * kstep;
;             const char* a2 = last ? nA : cA + (size_t)(t + 2) * kstep; const char* b2 = last ? nB : cB + (size_t)(t + 2) * kstep;
;             const char* a3 = a2 + kstep; const char* b3 = b2 + kstep;
;             if (last && has_next) S.a_ready(nxt);
;     ...
;             PG8_LDA(At, 1, 1); PG8_STAGE(PG8_SB(1, 0), b3, voffB); PG8_STAGE(PG8_SB(1, 1), b3 + hstep, voffB); PG8_STAGE(PG8_SA(1, 0), a3, voffA);
;             PG8_WAIT_V(8); PG8_WAIT_L(0); PG8_BAR; PG8_MMA(1, 0, At, B0); PG8_MMA(1, 1, At, B1); PG8_BAR; PG8_SCHED;
	s_setprio 1
	s_add_i32 s42, s73, s48
	v_lshl_add_u64 v[148:149], v[148:149], 0, s[16:17]
	s_mov_b32 m0, s42
	ds_read_b128 v[182:185], v153 offset:49152
	ds_read_b128 v[186:189], v153 offset:50176
	ds_read_b128 v[190:193], v153 offset:51200
	ds_read_b128 v[194:197], v153 offset:52224
	ds_read_b128 v[198:201], v153 offset:53248
	ds_read_b128 v[202:205], v153 offset:54272
	ds_read_b128 v[206:209], v153 offset:55296
	ds_read_b128 v[210:213], v153 offset:56320
	global_load_lds_dwordx4 v[148:149], off
	s_add_i32 m0, s42, 0x2000
	s_add_u32 s40, s40, 0x20080
	v_lshl_add_u64 v[148:149], v[214:215], 0, s[16:17]
	s_addc_u32 s41, s41, 0
	s_add_i32 s42, s74, s48
	global_load_lds_dwordx4 v[148:149], off
	v_lshl_add_u64 v[148:149], s[40:41], 0, v[130:131]
	s_mov_b32 m0, s42
	s_nop 0
	global_load_lds_dwordx4 v[148:149], off
	v_lshl_add_u64 v[148:149], s[40:41], 0, v[134:135]
	s_add_i32 m0, s42, 0x2000
	s_nop 0
	global_load_lds_dwordx4 v[148:149], off
	v_lshl_add_u64 v[148:149], v[216:217], 0, s[16:17]
	s_mov_b32 m0, s62
	s_nop 0
	global_load_lds_dwordx4 v[148:149], off
	v_lshl_add_u64 v[148:149], v[218:219], 0, s[16:17]
	s_mov_b32 m0, s63
	s_nop 0
	global_load_lds_dwordx4 v[148:149], off
	s_waitcnt vmcnt(8)
	s_waitcnt lgkmcnt(0)
	s_setprio 0
	s_barrier
	s_waitcnt lgkmcnt(0)
	v_mfma_f32_16x16x32_bf16 v[60:63], v[144:147], v[182:185], v[60:63]
	v_mfma_f32_16x16x32_bf16 v[56:59], v[158:161], v[182:185], v[56:59]
	v_mfma_f32_16x16x32_bf16 v[44:47], v[144:147], v[190:193], v[44:47]
	v_mfma_f32_16x16x32_bf16 v[40:43], v[158:161], v[190:193], v[40:43]
	v_mfma_f32_16x16x32_bf16 v[28:31], v[144:147], v[198:201], v[28:31]
	v_mfma_f32_16x16x32_bf16 v[24:27], v[158:161], v[198:201], v[24:27]
	v_mfma_f32_16x16x32_bf16 v[12:15], v[144:147], v[206:209], v[12:15]
	v_mfma_f32_16x16x32_bf16 v[8:11], v[158:161], v[206:209], v[8:11]
	v_mfma_f32_16x16x32_bf16 v[60:63], v[154:157], v[186:189], v[60:63]
	v_mfma_f32_16x16x32_bf16 v[56:59], v[162:165], v[186:189], v[56:59]
	v_mfma_f32_16x16x32_bf16 v[44:47], v[154:157], v[194:197], v[44:47]
	v_mfma_f32_16x16x32_bf16 v[40:43], v[162:165], v[194:197], v[40:43]
	v_mfma_f32_16x16x32_bf16 v[28:31], v[154:157], v[202:205], v[28:31]
	v_mfma_f32_16x16x32_bf16 v[24:27], v[162:165], v[202:205], v[24:27]
	v_mfma_f32_16x16x32_bf16 v[12:15], v[154:157], v[210:213], v[12:15]
	v_mfma_f32_16x16x32_bf16 v[8:11], v[162:165], v[210:213], v[8:11]
	v_mfma_f32_16x16x32_bf16 v[52:55], v[166:169], v[182:185], v[52:55]
	v_mfma_f32_16x16x32_bf16 v[48:51], v[174:177], v[182:185], v[48:51]
	v_mfma_f32_16x16x32_bf16 v[36:39], v[166:169], v[190:193], v[36:39]
	v_mfma_f32_16x16x32_bf16 v[32:35], v[174:177], v[190:193], v[32:35]
	v_mfma_f32_16x16x32_bf16 v[20:23], v[166:169], v[198:201], v[20:23]
	v_mfma_f32_16x16x32_bf16 v[16:19], v[174:177], v[198:201], v[16:19]
	v_mfma_f32_16x16x32_bf16 v[4:7], v[166:169], v[206:209], v[4:7]
	v_mfma_f32_16x16x32_bf16 v[0:3], v[174:177], v[206:209], v[0:3]
	v_mfma_f32_16x16x32_bf16 v[52:55], v[170:173], v[186:189], v[52:55]
	v_mfma_f32_16x16x32_bf16 v[48:51], v[178:181], v[186:189], v[48:51]
	v_mfma_f32_16x16x32_bf16 v[36:39], v[170:173], v[194:197], v[36:39]
	v_mfma_f32_16x16x32_bf16 v[32:35], v[178:181], v[194:197], v[32:35]
	v_mfma_f32_16x16x32_bf16 v[20:23], v[170:173], v[202:205], v[20:23]
	v_mfma_f32_16x16x32_bf16 v[16:19], v[178:181], v[202:205], v[16:19]
	v_mfma_f32_16x16x32_bf16 v[4:7], v[170:173], v[210:213], v[4:7]
	v_mfma_f32_16x16x32_bf16 v[0:3], v[178:181], v[210:213], v[0:3]
	s_barrier
	s_setprio 1
	s_add_i32 s72, s72, 2
	s_add_u32 s38, s38, 0x100
	s_addc_u32 s39, s39, 0
	s_add_u32 s70, s70, 0x100
	s_addc_u32 s71, s71, 0
	s_cmp_gt_u32 s72, 5
	s_cbranch_scc0 .LBB0_967
	s_setprio 0
	s_and_b64 vcc, exec, s[18:19]
	s_cbranch_vccz .LBB0_970
	s_barrier

; #define PG8_LDA(dst, b, h) do { _Pragma("unroll") for (int m = 0; m < 4; ++m) _Pragma("unroll") for (int k = 0; k < 2; ++k) dst[m][k] = *(const PG8_LAS bf16x8*)(lds + PG8_SA(b, h) + aoff + m * 2048 + k * 1024); } while (0)
; #define PG8_LDB(dst, b, h) do { _Pragma("unroll") for (int n = 0; n < 2; ++n) _Pragma("unroll") for (int k = 0; k < 2; ++k) dst[n][k] = *(const PG8_LAS bf16x8*)(lds + PG8_SB(b, h) + boff + n * 2048 + k * 1024); } while (0)
; #define PG8_WAIT_V(n) asm volatile("s_waitcnt vmcnt(" #n ")" ::: "memory")
; #define PG8_WAIT_L(n) asm volatile("s_waitcnt lgkmcnt(" #n ")" ::: "memory")
; #define PG8_BAR __builtin_amdgcn_s_barrier()
; #define PG8_SCHED __builtin_amdgcn_sched_barrier(0)
; template <class Epi, class Sched, bool ALIGN_EPI = false, bool SP2 = false, bool F8 = false, bool I8 = false, bool PF = false>
; __device__ __forceinline__ void gemm_phase(PG8_LAS unsigned char* lds, const Gemm g, const Sched& S, const Epi& E, const int wave_) {
;     ...
;             PG8_LDB(B0, 0, 0); PG8_LDB(B1, 0, 1); PG8_SCHED; PG8_LDA(At, 0, 0); PG8_STAGE(PG8_SA(1, 1), a1 + hstep, voffA);
;             PG8_WAIT_V(8); PG8_WAIT_L(0); PG8_BAR; PG8_MMA(0, 0, At, B0); PG8_MMA(0, 1, At, B1); PG8_BAR; PG8_SCHED;
;             PG8_LDA(At, 0, 1); PG8_STAGE(PG8_SB(0, 0), b2, voffB); PG8_STAGE(PG8_SB(0, 1), b2 + hstep, voffB); PG8_STAGE(PG8_SA(0, 0), a2, voffA);
;             PG8_WAIT_V(8); PG8_WAIT_L(0); PG8_BAR; PG8_MMA(1, 0, At, B0); PG8_MMA(1, 1, At, B1); PG8_BAR; PG8_SCHED;
.LBB0_1304:
	ds_read_b128 v[128:131], v209
	ds_read_b128 v[132:135], v209 offset:1024
	ds_read_b128 v[136:139], v209 offset:2048
	ds_read_b128 v[140:143], v209 offset:3072
	ds_read_b128 v[144:147], v210
	ds_read_b128 v[148:151], v210 offset:1024
	ds_read_b128 v[152:155], v210 offset:2048
	ds_read_b128 v[156:159], v210 offset:3072
	s_add_u32 s34, s30, 0xfffc0080
	s_addc_u32 s35, s31, -1
	s_cmp_eq_u32 s66, 12
	s_cselect_b32 s37, s21, s35
	s_cselect_b32 s36, s62, s34
	s_cselect_b32 s35, s19, s65
	s_cselect_b32 s34, s63, s64
	v_lshl_add_u64 v[206:207], s[30:31], 0, v[188:189]
	s_add_i32 m0, s29, 0xc000
	ds_read_b128 v[160:163], v211
	ds_read_b128 v[164:167], v211 offset:1024
	ds_read_b128 v[168:171], v211 offset:2048
	ds_read_b128 v[172:175], v211 offset:3072
	ds_read_b128 v[176:179], v211 offset:4096
	ds_read_b128 v[194:197], v211 offset:5120
	ds_read_b128 v[198:201], v211 offset:6144
	ds_read_b128 v[202:205], v211 offset:7168
	global_load_lds_dwordx4 v[206:207], off
	v_lshl_add_u64 v[206:207], s[30:31], 0, v[190:191]
	s_add_i32 m0, s29, 0xe000
	s_nop 0
	global_load_lds_dwordx4 v[206:207], off
	s_waitcnt vmcnt(8)
	s_waitcnt lgkmcnt(0)
	s_setprio 0
	s_barrier
	s_waitcnt lgkmcnt(0)
	v_mfma_f32_16x16x32_bf16 v[124:127], v[128:131], v[160:163], v[124:127]
	v_mfma_f32_16x16x32_bf16 v[120:123], v[136:139], v[160:163], v[120:123]
	v_mfma_f32_16x16x32_bf16 v[108:111], v[128:131], v[168:171], v[108:111]
	v_mfma_f32_16x16x32_bf16 v[104:107], v[136:139], v[168:171], v[104:107]
	v_mfma_f32_16x16x32_bf16 v[92:95], v[128:131], v[176:179], v[92:95]
	v_mfma_f32_16x16x32_bf16 v[88:91], v[136:139], v[176:179], v[88:91]
	v_mfma_f32_16x16x32_bf16 v[76:79], v[128:131], v[198:201], v[76:79]
	v_mfma_f32_16x16x32_bf16 v[72:75], v[136:139], v[198:201], v[72:75]
	v_mfma_f32_16x16x32_bf16 v[124:127], v[132:135], v[164:167], v[124:127]
	v_mfma_f32_16x16x32_bf16 v[120:123], v[140:143], v[164:167], v[120:123]
	v_mfma_f32_16x16x32_bf16 v[108:111], v[132:135], v[172:175], v[108:111]
	v_mfma_f32_16x16x32_bf16 v[104:107], v[140:143], v[172:175], v[104:107]
	v_mfma_f32_16x16x32_bf16 v[92:95], v[132:135], v[194:197], v[92:95]
	v_mfma_f32_16x16x32_bf16 v[88:91], v[140:143], v[194:197], v[88:91]
	v_mfma_f32_16x16x32_bf16 v[76:79], v[132:135], v[202:205], v[76:79]
	v_mfma_f32_16x16x32_bf16 v[72:75], v[140:143], v[202:205], v[72:75]
	v_mfma_f32_16x16x32_bf16 v[116:119], v[144:147], v[160:163], v[116:119]
	v_mfma_f32_16x16x32_bf16 v[112:115], v[152:155], v[160:163], v[112:115]
	v_mfma_f32_16x16x32_bf16 v[100:103], v[144:147], v[168:171], v[100:103]
	v_mfma_f32_16x16x32_bf16 v[96:99], v[152:155], v[168:171], v[96:99]
	v_mfma_f32_16x16x32_bf16 v[84:87], v[144:147], v[176:179], v[84:87]
	v_mfma_f32_16x16x32_bf16 v[80:83], v[152:155], v[176:179], v[80:83]
	v_mfma_f32_16x16x32_bf16 v[68:71], v[144:147], v[198:201], v[68:71]
	v_mfma_f32_16x16x32_bf16 v[64:67], v[152:155], v[198:201], v[64:67]
	v_mfma_f32_16x16x32_bf16 v[116:119], v[148:151], v[164:167], v[116:119]
	v_mfma_f32_16x16x32_bf16 v[112:115], v[156:159], v[164:167], v[112:115]
	v_mfma_f32_16x16x32_bf16 v[100:103], v[148:151], v[172:175], v[100:103]
	v_mfma_f32_16x16x32_bf16 v[96:99], v[156:159], v[172:175], v[96:99]
	v_mfma_f32_16x16x32_bf16 v[84:87], v[148:151], v[194:197], v[84:87]
	v_mfma_f32_16x16x32_bf16 v[80:83], v[156:159], v[194:197], v[80:83]
	v_mfma_f32_16x16x32_bf16 v[68:71], v[148:151], v[202:205], v[68:71]
	v_mfma_f32_16x16x32_bf16 v[64:67], v[156:159], v[202:205], v[64:67]
	s_barrier
	s_setprio 1
	s_add_i32 s67, s55, s40
	v_lshl_add_u64 v[206:207], s[34:35], 0, v[184:185]
	s_mov_b32 m0, s67
	ds_read_b128 v[160:163], v211 offset:16384
	ds_read_b128 v[164:167], v211 offset:17408
	ds_read_b128 v[168:171], v211 offset:18432
	ds_read_b128 v[172:175], v211 offset:19456
	ds_read_b128 v[176:179], v211 offset:20480
	ds_read_b128 v[194:197], v211 offset:21504
	ds_read_b128 v[198:201], v211 offset:22528
	ds_read_b128 v[202:205], v211 offset:23552
	global_load_lds_dwordx4 v[206:207], off
	s_add_i32 m0, s67, 0x2000
	s_add_u32 s68, s34, 0x40000
	v_lshl_add_u64 v[212:213], s[34:35], 0, v[180:181]
	s_addc_u32 s69, s35, 0
	s_add_i32 s67, s56, s40
	global_load_lds_dwordx4 v[212:213], off
	v_lshl_add_u64 v[214:215], s[68:69], 0, v[184:185]
	s_mov_b32 m0, s67
	v_lshl_add_u64 v[216:217], s[36:37], 0, v[182:183]
	global_load_lds_dwordx4 v[214:215], off
	v_lshl_add_u64 v[214:215], s[68:69], 0, v[180:181]
	s_add_i32 m0, s67, 0x2000
	s_nop 0
	global_load_lds_dwordx4 v[214:215], off
	v_lshl_add_u64 v[214:215], s[36:37], 0, v[186:187]
	s_mov_b32 m0, s29
	s_nop 0
	global_load_lds_dwordx4 v[214:215], off
	s_mov_b32 m0, s41
	s_nop 0
	global_load_lds_dwordx4 v[216:217], off
	s_waitcnt vmcnt(8)
	s_waitcnt lgkmcnt(0)
	s_setprio 0
	s_barrier
; #define PG8_LDA(dst, b, h) do { _Pragma("unroll") for (int m = 0; m < 4; ++m) _Pragma("unroll") for (int k = 0; k < 2; ++k) dst[m][k] = *(const PG8_LAS bf16x8*)(lds + PG8_SA(b, h) + aoff + m * 2048 + k * 1024); } while (0)
; #define PG8_LDB(dst, b, h) do { _Pragma("unroll") for (int n = 0; n < 2; ++n) _Pragma("unroll") for (int k = 0; k < 2; ++k) dst[n][k] = *(const PG8_LAS bf16x8*)(lds + PG8_SB(b, h) + boff + n * 2048 + k * 1024); } while (0)
; #define PG8_WAIT_V(n) asm volatile("s_waitcnt vmcnt(" #n ")" ::: "memory")
; #define PG8_WAIT_L(n) asm volatile("s_waitcnt lgkmcnt(" #n ")" ::: "memory")
; #define PG8_BAR __builtin_amdgcn_s_barrier()
; #define PG8_SCHED __builtin_amdgcn_sched_barrier(0)
; template <class Epi, class Sched, bool ALIGN_EPI = false, bool SP2 = false, bool F8 = false, bool I8 = false, bool PF = false>
; __device__ __forceinline__ void gemm_phase(PG8_LAS unsigned char* lds, const Gemm g, const Sched& S, const Epi& E, const int wave_) {
;     ...
;             PG8_WAIT_V(8); PG8_WAIT_L(0); PG8_BAR; PG8_MMA(1, 0, At, B0); PG8_MMA(1, 1, At, B1); PG8_BAR; PG8_SCHED;
;             PG8_LDB(B0, 1, 0); PG8_LDB(B1, 1, 1); PG8_SCHED; PG8_LDA(At, 1, 0); PG8_STAGE(PG8_SA(0, 1), a2 + hstep, voffA);
;             PG8_WAIT_V(8); PG8_WAIT_L(0); PG8_BAR; PG8_MMA(0, 0, At, B0); PG8_MMA(0, 1, At, B1); PG8_BAR; PG8_SCHED;
	s_waitcnt lgkmcnt(0)
	v_mfma_f32_16x16x32_bf16 v[60:63], v[128:131], v[160:163], v[60:63]
	v_mfma_f32_16x16x32_bf16 v[56:59], v[136:139], v[160:163], v[56:59]
	v_mfma_f32_16x16x32_bf16 v[44:47], v[128:131], v[168:171], v[44:47]
	v_mfma_f32_16x16x32_bf16 v[40:43], v[136:139], v[168:171], v[40:43]
	v_mfma_f32_16x16x32_bf16 v[28:31], v[128:131], v[176:179], v[28:31]
	v_mfma_f32_16x16x32_bf16 v[24:27], v[136:139], v[176:179], v[24:27]
	v_mfma_f32_16x16x32_bf16 v[12:15], v[128:131], v[198:201], v[12:15]
	v_mfma_f32_16x16x32_bf16 v[8:11], v[136:139], v[198:201], v[8:11]
	v_mfma_f32_16x16x32_bf16 v[60:63], v[132:135], v[164:167], v[60:63]
	v_mfma_f32_16x16x32_bf16 v[56:59], v[140:143], v[164:167], v[56:59]
	v_mfma_f32_16x16x32_bf16 v[44:47], v[132:135], v[172:175], v[44:47]
	v_mfma_f32_16x16x32_bf16 v[40:43], v[140:143], v[172:175], v[40:43]
	v_mfma_f32_16x16x32_bf16 v[28:31], v[132:135], v[194:197], v[28:31]
	v_mfma_f32_16x16x32_bf16 v[24:27], v[140:143], v[194:197], v[24:27]
	v_mfma_f32_16x16x32_bf16 v[12:15], v[132:135], v[202:205], v[12:15]
	v_mfma_f32_16x16x32_bf16 v[8:11], v[140:143], v[202:205], v[8:11]
	v_mfma_f32_16x16x32_bf16 v[52:55], v[144:147], v[160:163], v[52:55]
	v_mfma_f32_16x16x32_bf16 v[48:51], v[152:155], v[160:163], v[48:51]
	v_mfma_f32_16x16x32_bf16 v[36:39], v[144:147], v[168:171], v[36:39]
	v_mfma_f32_16x16x32_bf16 v[32:35], v[152:155], v[168:171], v[32:35]
	v_mfma_f32_16x16x32_bf16 v[20:23], v[144:147], v[176:179], v[20:23]
	v_mfma_f32_16x16x32_bf16 v[16:19], v[152:155], v[176:179], v[16:19]
	v_mfma_f32_16x16x32_bf16 v[4:7], v[144:147], v[198:201], v[4:7]
	v_mfma_f32_16x16x32_bf16 v[0:3], v[152:155], v[198:201], v[0:3]
	v_mfma_f32_16x16x32_bf16 v[52:55], v[148:151], v[164:167], v[52:55]
	v_mfma_f32_16x16x32_bf16 v[48:51], v[156:159], v[164:167], v[48:51]
	v_mfma_f32_16x16x32_bf16 v[36:39], v[148:151], v[172:175], v[36:39]
	v_mfma_f32_16x16x32_bf16 v[32:35], v[156:159], v[172:175], v[32:35]
	v_mfma_f32_16x16x32_bf16 v[20:23], v[148:151], v[194:197], v[20:23]
	v_mfma_f32_16x16x32_bf16 v[16:19], v[156:159], v[194:197], v[16:19]
	v_mfma_f32_16x16x32_bf16 v[4:7], v[148:151], v[202:205], v[4:7]
	v_mfma_f32_16x16x32_bf16 v[0:3], v[156:159], v[202:205], v[0:3]
	s_barrier
	s_setprio 1
	s_add_i32 s67, 0, 0x18000
	s_add_i32 s68, 0, 0x1c000
	v_add_u32_e32 v140, s67, v208
	v_add_u32_e32 v156, s68, v208
	ds_read_b128 v[128:131], v140
	ds_read_b128 v[132:135], v140 offset:1024
	ds_read_b128 v[136:139], v140 offset:2048
	ds_read_b128 v[140:143], v140 offset:3072
	ds_read_b128 v[144:147], v156
	ds_read_b128 v[148:151], v156 offset:1024
	ds_read_b128 v[152:155], v156 offset:2048
	ds_read_b128 v[156:159], v156 offset:3072
	s_add_u32 s36, s36, 0x40000
	s_addc_u32 s37, s37, 0
	s_mov_b32 m0, s42
	v_lshl_add_u64 v[218:219], s[36:37], 0, v[186:187]
	ds_read_b128 v[160:163], v211 offset:32768
	ds_read_b128 v[164:167], v211 offset:33792
	ds_read_b128 v[168:171], v211 offset:34816
	ds_read_b128 v[172:175], v211 offset:35840
	ds_read_b128 v[176:179], v211 offset:36864
	ds_read_b128 v[194:197], v211 offset:37888
	ds_read_b128 v[198:201], v211 offset:38912
	ds_read_b128 v[202:205], v211 offset:39936
	global_load_lds_dwordx4 v[218:219], off
	v_lshl_add_u64 v[218:219], s[36:37], 0, v[182:183]
	s_mov_b32 m0, s43
	s_nop 0
	global_load_lds_dwordx4 v[218:219], off
	s_waitcnt vmcnt(8)
	s_waitcnt lgkmcnt(0)
	s_setprio 0
	s_barrier
	s_waitcnt lgkmcnt(0)
	v_mfma_f32_16x16x32_bf16 v[124:127], v[128:131], v[160:163], v[124:127]
	v_mfma_f32_16x16x32_bf16 v[120:123], v[136:139], v[160:163], v[120:123]
	v_mfma_f32_16x16x32_bf16 v[108:111], v[128:131], v[168:171], v[108:111]
	v_mfma_f32_16x16x32_bf16 v[104:107], v[136:139], v[168:171], v[104:107]
	v_mfma_f32_16x16x32_bf16 v[92:95], v[128:131], v[176:179], v[92:95]
	v_mfma_f32_16x16x32_bf16 v[88:91], v[136:139], v[176:179], v[88:91]
	v_mfma_f32_16x16x32_bf16 v[76:79], v[128:131], v[198:201], v[76:79]
	v_mfma_f32_16x16x32_bf16 v[72:75], v[136:139], v[198:201], v[72:75]
	v_mfma_f32_16x16x32_bf16 v[124:127], v[132:135], v[164:167], v[124:127]
	v_mfma_f32_16x16x32_bf16 v[120:123], v[140:143], v[164:167], v[120:123]
	v_mfma_f32_16x16x32_bf16 v[108:111], v[132:135], v[172:175], v[108:111]
	v_mfma_f32_16x16x32_bf16 v[104:107], v[140:143], v[172:175], v[104:107]
	v_mfma_f32_16x16x32_bf16 v[92:95], v[132:135], v[194:197], v[92:95]
	v_mfma_f32_16x16x32_bf16 v[88:91], v[140:143], v[194:197], v[88:91]
	v_mfma_f32_16x16x32_bf16 v[76:79], v[132:135], v[202:205], v[76:79]
	v_mfma_f32_16x16x32_bf16 v[72:75], v[140:143], v[202:205], v[72:75]
	v_mfma_f32_16x16x32_bf16 v[116:119], v[144:147], v[160:163], v[116:119]
	v_mfma_f32_16x16x32_bf16 v[112:115], v[152:155], v[160:163], v[112:115]
	v_mfma_f32_16x16x32_bf16 v[100:103], v[144:147], v[168:171], v[100:103]
	v_mfma_f32_16x16x32_bf16 v[96:99], v[152:155], v[168:171], v[96:99]
	v_mfma_f32_16x16x32_bf16 v[84:87], v[144:147], v[176:179], v[84:87]
	v_mfma_f32_16x16x32_bf16 v[80:83], v[152:155], v[176:179], v[80:83]
	v_mfma_f32_16x16x32_bf16 v[68:71], v[144:147], v[198:201], v[68:71]
	v_mfma_f32_16x16x32_bf16 v[64:67], v[152:155], v[198:201], v[64:67]
	v_mfma_f32_16x16x32_bf16 v[116:119], v[148:151], v[164:167], v[116:119]
	v_mfma_f32_16x16x32_bf16 v[112:115], v[156:159], v[164:167], v[112:115]
	v_mfma_f32_16x16x32_bf16 v[100:103], v[148:151], v[172:175], v[100:103]
	v_mfma_f32_16x16x32_bf16 v[96:99], v[156:159], v[172:175], v[96:99]
	v_mfma_f32_16x16x32_bf16 v[84:87], v[148:151], v[194:197], v[84:87]
	v_mfma_f32_16x16x32_bf16 v[80:83], v[156:159], v[194:197], v[80:83]
	v_mfma_f32_16x16x32_bf16 v[68:71], v[148:151], v[202:205], v[68:71]
	v_mfma_f32_16x16x32_bf16 v[64:67], v[156:159], v[202:205], v[64:67]
	s_barrier
; #define PG8_LDA(dst, b, h) do { _Pragma("unroll") for (int m = 0; m < 4; ++m) _Pragma("unroll") for (int k = 0; k < 2; ++k) dst[m][k] = *(const PG8_LAS bf16x8*)(lds + PG8_SA(b, h) + aoff + m * 2048 + k * 1024); } while (0)
; #define PG8_WAIT_V(n) asm volatile("s_waitcnt vmcnt(" #n ")" ::: "memory")
; #define PG8_WAIT_L(n) asm volatile("s_waitcnt lgkmcnt(" #n ")" ::: "memory")
; #define PG8_BAR __builtin_amdgcn_s_barrier()
; #define PG8_SCHED __builtin_amdgcn_sched_barrier(0)
; template <class Epi, class Sched, bool ALIGN_EPI = false, bool SP2 = false, bool F8 = false, bool I8 = false, bool PF = false>
; __device__ __forceinline__ void gemm_phase(PG8_LAS unsigned char* lds, const Gemm g, const Sched& S, const Epi& E, const int wave_) {
;     ...
;         for (int t = 0; t < nt; t += 2) {
;             const bool last = (t == nt - 2);
;             const char* a1 = cA + (size_t)(t + 1) * kstep;
;             const char* a2 = last ? nA : cA + (size_t)(t + 2) * kstep; const char* b2 = last ? nB : cB + (size_t)(t + 2) * kstep;
;             const char* a3 = a2 + kstep; const char* b3 = b2 + kstep;
;             if (last && has_next) S.a_ready(nxt);
;     ...
;             PG8_LDA(At, 1, 1); PG8_STAGE(PG8_SB(1, 0), b3, voffB); PG8_STAGE(PG8_SB(1, 1), b3 + hstep, voffB); PG8_STAGE(PG8_SA(1, 0), a3, voffA);
;             PG8_WAIT_V(8); PG8_WAIT_L(0); PG8_BAR; PG8_MMA(1, 0, At, B0); PG8_MMA(1, 1, At, B1); PG8_BAR; PG8_SCHED;
	s_setprio 1
	s_add_i32 s36, s67, s40
	v_lshl_add_u64 v[206:207], v[206:207], 0, s[8:9]
	s_mov_b32 m0, s36
	ds_read_b128 v[160:163], v211 offset:49152
	ds_read_b128 v[164:167], v211 offset:50176
	ds_read_b128 v[168:171], v211 offset:51200
	ds_read_b128 v[172:175], v211 offset:52224
	ds_read_b128 v[176:179], v211 offset:53248
	ds_read_b128 v[194:197], v211 offset:54272
	ds_read_b128 v[198:201], v211 offset:55296
	ds_read_b128 v[202:205], v211 offset:56320
	global_load_lds_dwordx4 v[206:207], off
	s_add_i32 m0, s36, 0x2000
	s_add_u32 s34, s34, 0x40080
	v_lshl_add_u64 v[206:207], v[212:213], 0, s[8:9]
	s_addc_u32 s35, s35, 0
	s_add_i32 s36, s68, s40
	global_load_lds_dwordx4 v[206:207], off
	v_lshl_add_u64 v[206:207], s[34:35], 0, v[184:185]
	s_mov_b32 m0, s36
	s_nop 0
	global_load_lds_dwordx4 v[206:207], off
	v_lshl_add_u64 v[206:207], s[34:35], 0, v[180:181]
	s_add_i32 m0, s36, 0x2000
	s_nop 0
	global_load_lds_dwordx4 v[206:207], off
	v_lshl_add_u64 v[206:207], v[214:215], 0, s[8:9]
	s_mov_b32 m0, s52
	s_nop 0
	global_load_lds_dwordx4 v[206:207], off
	v_lshl_add_u64 v[206:207], v[216:217], 0, s[8:9]
	s_mov_b32 m0, s53
	s_nop 0
	global_load_lds_dwordx4 v[206:207], off
	s_waitcnt vmcnt(8)
	s_waitcnt lgkmcnt(0)
	s_setprio 0
	s_barrier
	s_waitcnt lgkmcnt(0)
	v_mfma_f32_16x16x32_bf16 v[60:63], v[128:131], v[160:163], v[60:63]
	v_mfma_f32_16x16x32_bf16 v[56:59], v[136:139], v[160:163], v[56:59]
	v_mfma_f32_16x16x32_bf16 v[44:47], v[128:131], v[168:171], v[44:47]
	v_mfma_f32_16x16x32_bf16 v[40:43], v[136:139], v[168:171], v[40:43]
	v_mfma_f32_16x16x32_bf16 v[28:31], v[128:131], v[176:179], v[28:31]
	v_mfma_f32_16x16x32_bf16 v[24:27], v[136:139], v[176:179], v[24:27]
	v_mfma_f32_16x16x32_bf16 v[12:15], v[128:131], v[198:201], v[12:15]
	v_mfma_f32_16x16x32_bf16 v[8:11], v[136:139], v[198:201], v[8:11]
	v_mfma_f32_16x16x32_bf16 v[60:63], v[132:135], v[164:167], v[60:63]
	v_mfma_f32_16x16x32_bf16 v[56:59], v[140:143], v[164:167], v[56:59]
	v_mfma_f32_16x16x32_bf16 v[44:47], v[132:135], v[172:175], v[44:47]
	v_mfma_f32_16x16x32_bf16 v[40:43], v[140:143], v[172:175], v[40:43]
	v_mfma_f32_16x16x32_bf16 v[28:31], v[132:135], v[194:197], v[28:31]
	v_mfma_f32_16x16x32_bf16 v[24:27], v[140:143], v[194:197], v[24:27]
	v_mfma_f32_16x16x32_bf16 v[12:15], v[132:135], v[202:205], v[12:15]
	v_mfma_f32_16x16x32_bf16 v[8:11], v[140:143], v[202:205], v[8:11]
	v_mfma_f32_16x16x32_bf16 v[52:55], v[144:147], v[160:163], v[52:55]
	v_mfma_f32_16x16x32_bf16 v[48:51], v[152:155], v[160:163], v[48:51]
	v_mfma_f32_16x16x32_bf16 v[36:39], v[144:147], v[168:171], v[36:39]
	v_mfma_f32_16x16x32_bf16 v[32:35], v[152:155], v[168:171], v[32:35]
	v_mfma_f32_16x16x32_bf16 v[20:23], v[144:147], v[176:179], v[20:23]
	v_mfma_f32_16x16x32_bf16 v[16:19], v[152:155], v[176:179], v[16:19]
	v_mfma_f32_16x16x32_bf16 v[4:7], v[144:147], v[198:201], v[4:7]
	v_mfma_f32_16x16x32_bf16 v[0:3], v[152:155], v[198:201], v[0:3]
	v_mfma_f32_16x16x32_bf16 v[52:55], v[148:151], v[164:167], v[52:55]
	v_mfma_f32_16x16x32_bf16 v[48:51], v[156:159], v[164:167], v[48:51]
	v_mfma_f32_16x16x32_bf16 v[36:39], v[148:151], v[172:175], v[36:39]
	v_mfma_f32_16x16x32_bf16 v[32:35], v[156:159], v[172:175], v[32:35]
	v_mfma_f32_16x16x32_bf16 v[20:23], v[148:151], v[194:197], v[20:23]
	v_mfma_f32_16x16x32_bf16 v[16:19], v[156:159], v[194:197], v[16:19]
	v_mfma_f32_16x16x32_bf16 v[4:7], v[148:151], v[202:205], v[4:7]
	v_mfma_f32_16x16x32_bf16 v[0:3], v[156:159], v[202:205], v[0:3]
	s_barrier
	s_setprio 1
	s_add_i32 s66, s66, 2
	s_add_u32 s30, s30, 0x100
	s_addc_u32 s31, s31, 0
	s_add_u32 s64, s64, 0x100
	s_addc_u32 s65, s65, 0
	s_cmp_gt_u32 s66, 13
	s_cbranch_scc0 .LBB0_1304
	s_setprio 0
	s_and_b64 vcc, exec, s[10:11]
	s_cbranch_vccz .LBB0_1307
	s_barrier

; #define PG8_LDA(dst, b, h) do { _Pragma("unroll") for (int m = 0; m < 4; ++m) _Pragma("unroll") for (int k = 0; k < 2; ++k) dst[m][k] = *(const PG8_LAS bf16x8*)(lds + PG8_SA(b, h) + aoff + m * 2048 + k * 1024); } while (0)
; #define PG8_LDB(dst, b, h) do { _Pragma("unroll") for (int n = 0; n < 2; ++n) _Pragma("unroll") for (int k = 0; k < 2; ++k) dst[n][k] = *(const PG8_LAS bf16x8*)(lds + PG8_SB(b, h) + boff + n * 2048 + k * 1024); } while (0)
; #define PG8_WAIT_V(n) asm volatile("s_waitcnt vmcnt(" #n ")" ::: "memory")
; #define PG8_WAIT_L(n) asm volatile("s_waitcnt lgkmcnt(" #n ")" ::: "memory")
; #define PG8_BAR __builtin_amdgcn_s_barrier()
; #define PG8_SCHED __builtin_amdgcn_sched_barrier(0)
; template <class Epi, class Sched, bool ALIGN_EPI = false, bool SP2 = false, bool F8 = false, bool I8 = false, bool PF = false>
; __device__ __forceinline__ void gemm_phase(PG8_LAS unsigned char* lds, const Gemm g, const Sched& S, const Epi& E, const int wave_) {
;     ...
;             PG8_LDB(B0, 0, 0); PG8_LDB(B1, 0, 1); PG8_SCHED; PG8_LDA(At, 0, 0); PG8_STAGE(PG8_SA(1, 1), a1 + hstep, voffA);
;             PG8_WAIT_V(8); PG8_WAIT_L(0); PG8_BAR; PG8_MMA(0, 0, At, B0); PG8_MMA(0, 1, At, B1); PG8_BAR; PG8_SCHED;
;             PG8_LDA(At, 0, 1); PG8_STAGE(PG8_SB(0, 0), b2, voffB); PG8_STAGE(PG8_SB(0, 1), b2 + hstep, voffB); PG8_STAGE(PG8_SA(0, 0), a2, voffA);
;             PG8_WAIT_V(8); PG8_WAIT_L(0); PG8_BAR; PG8_MMA(1, 0, At, B0); PG8_MMA(1, 1, At, B1); PG8_BAR; PG8_SCHED;
.LBB0_1540:
	ds_read_b128 v[24:27], v181
	ds_read_b128 v[28:31], v181 offset:1024
	ds_read_b128 v[16:19], v181 offset:2048
	ds_read_b128 v[20:23], v181 offset:3072
	ds_read_b128 v[8:11], v182
	ds_read_b128 v[12:15], v182 offset:1024
	ds_read_b128 v[0:3], v182 offset:2048
	ds_read_b128 v[4:7], v182 offset:3072
	s_add_u32 s34, s30, 0xfffe0080
	s_addc_u32 s35, s31, -1
	s_cmp_eq_u32 s74, 4
	s_cselect_b32 s37, s19, s35
	s_cselect_b32 s36, s21, s34
	s_cselect_b32 s35, s17, s73
	s_cselect_b32 s34, s71, s72
	v_lshl_add_u64 v[210:211], s[30:31], 0, v[168:169]
	s_add_i32 m0, s29, 0xc000
	ds_read_b128 v[172:175], v183
	ds_read_b128 v[176:179], v183 offset:1024
	ds_read_b128 v[186:189], v183 offset:2048
	ds_read_b128 v[190:193], v183 offset:3072
	ds_read_b128 v[194:197], v183 offset:4096
	ds_read_b128 v[198:201], v183 offset:5120
	ds_read_b128 v[202:205], v183 offset:6144
	ds_read_b128 v[206:209], v183 offset:7168
	global_load_lds_dwordx4 v[210:211], off
	v_lshl_add_u64 v[210:211], s[30:31], 0, v[170:171]
	s_add_i32 m0, s29, 0xe000
	s_nop 0
	global_load_lds_dwordx4 v[210:211], off
	s_waitcnt vmcnt(8)
	s_waitcnt lgkmcnt(0)
	s_setprio 0
	s_barrier
	s_waitcnt lgkmcnt(0)
	v_mfma_f32_16x16x128_f8f6f4 v[156:159], v[24:31], v[172:179], v[156:159]
	v_mfma_f32_16x16x128_f8f6f4 v[148:151], v[16:23], v[172:179], v[148:151]
	v_mfma_f32_16x16x128_f8f6f4 v[140:143], v[24:31], v[186:193], v[140:143]
	v_mfma_f32_16x16x128_f8f6f4 v[132:135], v[16:23], v[186:193], v[132:135]
	v_mfma_f32_16x16x128_f8f6f4 v[124:127], v[24:31], v[194:201], v[124:127]
	v_mfma_f32_16x16x128_f8f6f4 v[116:119], v[16:23], v[194:201], v[116:119]
	v_mfma_f32_16x16x128_f8f6f4 v[108:111], v[24:31], v[202:209], v[108:111]
	v_mfma_f32_16x16x128_f8f6f4 v[100:103], v[16:23], v[202:209], v[100:103]
	v_mfma_f32_16x16x128_f8f6f4 v[152:155], v[8:15], v[172:179], v[152:155]
	v_mfma_f32_16x16x128_f8f6f4 v[144:147], v[0:7], v[172:179], v[144:147]
	v_mfma_f32_16x16x128_f8f6f4 v[136:139], v[8:15], v[186:193], v[136:139]
	v_mfma_f32_16x16x128_f8f6f4 v[128:131], v[0:7], v[186:193], v[128:131]
	v_mfma_f32_16x16x128_f8f6f4 v[120:123], v[8:15], v[194:201], v[120:123]
	v_mfma_f32_16x16x128_f8f6f4 v[112:115], v[0:7], v[194:201], v[112:115]
	v_mfma_f32_16x16x128_f8f6f4 v[104:107], v[8:15], v[202:209], v[104:107]
	v_mfma_f32_16x16x128_f8f6f4 v[96:99], v[0:7], v[202:209], v[96:99]
	s_barrier
	s_setprio 1
	s_add_i32 s75, s55, s39
	v_lshl_add_u64 v[172:173], s[34:35], 0, v[160:161]
	s_mov_b32 m0, s75
	ds_read_b128 v[186:189], v183 offset:16384
	ds_read_b128 v[190:193], v183 offset:17408
	ds_read_b128 v[194:197], v183 offset:18432
	ds_read_b128 v[198:201], v183 offset:19456
	ds_read_b128 v[202:205], v183 offset:20480
	ds_read_b128 v[206:209], v183 offset:21504
	ds_read_b128 v[210:213], v183 offset:22528
	ds_read_b128 v[214:217], v183 offset:23552
	global_load_lds_dwordx4 v[172:173], off
	s_add_i32 m0, s75, 0x2000
	s_add_u32 s76, s34, 0x20000
	v_lshl_add_u64 v[174:175], s[34:35], 0, v[166:167]
	s_addc_u32 s77, s35, 0
	s_add_i32 s75, s64, s39
	global_load_lds_dwordx4 v[174:175], off
	v_lshl_add_u64 v[176:177], s[76:77], 0, v[160:161]
	s_mov_b32 m0, s75
	v_lshl_add_u64 v[178:179], s[36:37], 0, v[164:165]
	global_load_lds_dwordx4 v[176:177], off
	v_lshl_add_u64 v[176:177], s[76:77], 0, v[166:167]
	s_add_i32 m0, s75, 0x2000
	s_nop 0
	global_load_lds_dwordx4 v[176:177], off
	v_lshl_add_u64 v[176:177], s[36:37], 0, v[162:163]
	s_mov_b32 m0, s29
	s_nop 0
	global_load_lds_dwordx4 v[176:177], off
	s_mov_b32 m0, s42
	s_nop 0
	global_load_lds_dwordx4 v[178:179], off
	s_waitcnt vmcnt(8)
	s_waitcnt lgkmcnt(0)
	s_setprio 0
	s_barrier
	s_waitcnt lgkmcnt(0)
	v_mfma_f32_16x16x128_f8f6f4 v[92:95], v[24:31], v[186:193], v[92:95]
	v_mfma_f32_16x16x128_f8f6f4 v[84:87], v[16:23], v[186:193], v[84:87]
	v_mfma_f32_16x16x128_f8f6f4 v[76:79], v[24:31], v[194:201], v[76:79]
	v_mfma_f32_16x16x128_f8f6f4 v[68:71], v[16:23], v[194:201], v[68:71]
	v_mfma_f32_16x16x128_f8f6f4 v[60:63], v[24:31], v[202:209], v[60:63]
	v_mfma_f32_16x16x128_f8f6f4 v[52:55], v[16:23], v[202:209], v[52:55]
	v_mfma_f32_16x16x128_f8f6f4 v[44:47], v[24:31], v[210:217], v[44:47]
	v_mfma_f32_16x16x128_f8f6f4 v[36:39], v[16:23], v[210:217], v[36:39]
	v_mfma_f32_16x16x128_f8f6f4 v[88:91], v[8:15], v[186:193], v[88:91]
	v_mfma_f32_16x16x128_f8f6f4 v[80:83], v[0:7], v[186:193], v[80:83]
	v_mfma_f32_16x16x128_f8f6f4 v[72:75], v[8:15], v[194:201], v[72:75]
	v_mfma_f32_16x16x128_f8f6f4 v[64:67], v[0:7], v[194:201], v[64:67]
	v_mfma_f32_16x16x128_f8f6f4 v[56:59], v[8:15], v[202:209], v[56:59]
	v_mfma_f32_16x16x128_f8f6f4 v[48:51], v[0:7], v[202:209], v[48:51]
	v_mfma_f32_16x16x128_f8f6f4 v[40:43], v[8:15], v[210:217], v[40:43]
	v_mfma_f32_16x16x128_f8f6f4 v[32:35], v[0:7], v[210:217], v[32:35]
	s_barrier
; #define PG8_LDA(dst, b, h) do { _Pragma("unroll") for (int m = 0; m < 4; ++m) _Pragma("unroll") for (int k = 0; k < 2; ++k) dst[m][k] = *(const PG8_LAS bf16x8*)(lds + PG8_SA(b, h) + aoff + m * 2048 + k * 1024); } while (0)
; #define PG8_LDB(dst, b, h) do { _Pragma("unroll") for (int n = 0; n < 2; ++n) _Pragma("unroll") for (int k = 0; k < 2; ++k) dst[n][k] = *(const PG8_LAS bf16x8*)(lds + PG8_SB(b, h) + boff + n * 2048 + k * 1024); } while (0)
; #define PG8_WAIT_V(n) asm volatile("s_waitcnt vmcnt(" #n ")" ::: "memory")
; #define PG8_WAIT_L(n) asm volatile("s_waitcnt lgkmcnt(" #n ")" ::: "memory")
; #define PG8_BAR __builtin_amdgcn_s_barrier()
; #define PG8_SCHED __builtin_amdgcn_sched_barrier(0)
; template <class Epi, class Sched, bool ALIGN_EPI = false, bool SP2 = false, bool F8 = false, bool I8 = false, bool PF = false>
; __device__ __forceinline__ void gemm_phase(PG8_LAS unsigned char* lds, const Gemm g, const Sched& S, const Epi& E, const int wave_) {
;     ...
;         for (int t = 0; t < nt; t += 2) {
;             const bool last = (t == nt - 2);
;             const char* a1 = cA + (size_t)(t + 1) * kstep;
;             const char* a2 = last ? nA : cA + (size_t)(t + 2) * kstep; const char* b2 = last ? nB : cB + (size_t)(t + 2) * kstep;
;     ...
;             PG8_LDB(B0, 1, 0); PG8_LDB(B1, 1, 1); PG8_SCHED; PG8_LDA(At, 1, 0); PG8_STAGE(PG8_SA(0, 1), a2 + hstep, voffA);
;             PG8_WAIT_V(8); PG8_WAIT_L(0); PG8_BAR; PG8_MMA(0, 0, At, B0); PG8_MMA(0, 1, At, B1); PG8_BAR; PG8_SCHED;
;             PG8_LDA(At, 1, 1); PG8_STAGE(PG8_SB(1, 0), b3, voffB); PG8_STAGE(PG8_SB(1, 1), b3 + hstep, voffB); PG8_STAGE(PG8_SA(1, 0), a3, voffA);
;             PG8_WAIT_V(8); PG8_WAIT_L(0); PG8_BAR; PG8_MMA(1, 0, At, B0); PG8_MMA(1, 1, At, B1); PG8_BAR; PG8_SCHED;
	s_setprio 1
	s_add_i32 s75, 0, 0x18000
	s_add_i32 s76, 0, 0x1c000
	v_add_u32_e32 v12, s75, v180
	v_add_u32_e32 v28, s76, v180
	ds_read_b128 v[0:3], v12
	ds_read_b128 v[4:7], v12 offset:1024
	ds_read_b128 v[8:11], v12 offset:2048
	ds_read_b128 v[12:15], v12 offset:3072
	ds_read_b128 v[16:19], v28
	ds_read_b128 v[20:23], v28 offset:1024
	ds_read_b128 v[24:27], v28 offset:2048
	ds_read_b128 v[28:31], v28 offset:3072
	s_add_u32 s36, s36, 0x20000
	s_addc_u32 s37, s37, 0
	s_mov_b32 m0, s43
	v_lshl_add_u64 v[218:219], s[36:37], 0, v[162:163]
	ds_read_b128 v[186:189], v183 offset:32768
	ds_read_b128 v[190:193], v183 offset:33792
	ds_read_b128 v[194:197], v183 offset:34816
	ds_read_b128 v[198:201], v183 offset:35840
	ds_read_b128 v[202:205], v183 offset:36864
	ds_read_b128 v[206:209], v183 offset:37888
	ds_read_b128 v[210:213], v183 offset:38912
	ds_read_b128 v[214:217], v183 offset:39936
	global_load_lds_dwordx4 v[218:219], off
	v_lshl_add_u64 v[218:219], s[36:37], 0, v[164:165]
	s_mov_b32 m0, s44
	s_nop 0
	global_load_lds_dwordx4 v[218:219], off
	s_waitcnt vmcnt(8)
	s_waitcnt lgkmcnt(0)
	s_setprio 0
	s_barrier
	s_waitcnt lgkmcnt(0)
	v_mfma_f32_16x16x128_f8f6f4 v[156:159], v[0:7], v[186:193], v[156:159]
	v_mfma_f32_16x16x128_f8f6f4 v[148:151], v[8:15], v[186:193], v[148:151]
	v_mfma_f32_16x16x128_f8f6f4 v[140:143], v[0:7], v[194:201], v[140:143]
	v_mfma_f32_16x16x128_f8f6f4 v[132:135], v[8:15], v[194:201], v[132:135]
	v_mfma_f32_16x16x128_f8f6f4 v[124:127], v[0:7], v[202:209], v[124:127]
	v_mfma_f32_16x16x128_f8f6f4 v[116:119], v[8:15], v[202:209], v[116:119]
	v_mfma_f32_16x16x128_f8f6f4 v[108:111], v[0:7], v[210:217], v[108:111]
	v_mfma_f32_16x16x128_f8f6f4 v[100:103], v[8:15], v[210:217], v[100:103]
	v_mfma_f32_16x16x128_f8f6f4 v[152:155], v[16:23], v[186:193], v[152:155]
	v_mfma_f32_16x16x128_f8f6f4 v[144:147], v[24:31], v[186:193], v[144:147]
	v_mfma_f32_16x16x128_f8f6f4 v[136:139], v[16:23], v[194:201], v[136:139]
	v_mfma_f32_16x16x128_f8f6f4 v[128:131], v[24:31], v[194:201], v[128:131]
	v_mfma_f32_16x16x128_f8f6f4 v[120:123], v[16:23], v[202:209], v[120:123]
	v_mfma_f32_16x16x128_f8f6f4 v[112:115], v[24:31], v[202:209], v[112:115]
	v_mfma_f32_16x16x128_f8f6f4 v[104:107], v[16:23], v[210:217], v[104:107]
	v_mfma_f32_16x16x128_f8f6f4 v[96:99], v[24:31], v[210:217], v[96:99]
	s_barrier
	s_setprio 1
	s_add_i32 s36, s75, s39
	v_lshl_add_u64 v[172:173], v[172:173], 0, s[8:9]
	s_mov_b32 m0, s36
	ds_read_b128 v[186:189], v183 offset:49152
	ds_read_b128 v[190:193], v183 offset:50176
	ds_read_b128 v[194:197], v183 offset:51200
	ds_read_b128 v[198:201], v183 offset:52224
	ds_read_b128 v[202:205], v183 offset:53248
	ds_read_b128 v[206:209], v183 offset:54272
	ds_read_b128 v[210:213], v183 offset:55296
	ds_read_b128 v[214:217], v183 offset:56320
	global_load_lds_dwordx4 v[172:173], off
	s_add_i32 m0, s36, 0x2000
	s_add_u32 s34, s34, 0x20080
	v_lshl_add_u64 v[172:173], v[174:175], 0, s[8:9]
	s_addc_u32 s35, s35, 0
	s_add_i32 s36, s76, s39
	global_load_lds_dwordx4 v[172:173], off
	v_lshl_add_u64 v[172:173], s[34:35], 0, v[160:161]
	s_mov_b32 m0, s36
	s_nop 0
	global_load_lds_dwordx4 v[172:173], off
	v_lshl_add_u64 v[172:173], s[34:35], 0, v[166:167]
	s_add_i32 m0, s36, 0x2000
	s_nop 0
	global_load_lds_dwordx4 v[172:173], off
	v_lshl_add_u64 v[172:173], v[176:177], 0, s[8:9]
	s_mov_b32 m0, s48
	s_nop 0
	global_load_lds_dwordx4 v[172:173], off
	v_lshl_add_u64 v[172:173], v[178:179], 0, s[8:9]
	s_mov_b32 m0, s49
	s_nop 0
	global_load_lds_dwordx4 v[172:173], off
	s_waitcnt vmcnt(8)
	s_waitcnt lgkmcnt(0)
	s_setprio 0
	s_barrier
	s_waitcnt lgkmcnt(0)
	v_mfma_f32_16x16x128_f8f6f4 v[92:95], v[0:7], v[186:193], v[92:95]
	v_mfma_f32_16x16x128_f8f6f4 v[84:87], v[8:15], v[186:193], v[84:87]
	v_mfma_f32_16x16x128_f8f6f4 v[76:79], v[0:7], v[194:201], v[76:79]
	v_mfma_f32_16x16x128_f8f6f4 v[68:71], v[8:15], v[194:201], v[68:71]
	v_mfma_f32_16x16x128_f8f6f4 v[60:63], v[0:7], v[202:209], v[60:63]
	v_mfma_f32_16x16x128_f8f6f4 v[52:55], v[8:15], v[202:209], v[52:55]
	v_mfma_f32_16x16x128_f8f6f4 v[44:47], v[0:7], v[210:217], v[44:47]
	v_mfma_f32_16x16x128_f8f6f4 v[36:39], v[8:15], v[210:217], v[36:39]
	v_mfma_f32_16x16x128_f8f6f4 v[88:91], v[16:23], v[186:193], v[88:91]
	v_mfma_f32_16x16x128_f8f6f4 v[80:83], v[24:31], v[186:193], v[80:83]
	v_mfma_f32_16x16x128_f8f6f4 v[72:75], v[16:23], v[194:201], v[72:75]
	v_mfma_f32_16x16x128_f8f6f4 v[64:67], v[24:31], v[194:201], v[64:67]
	v_mfma_f32_16x16x128_f8f6f4 v[56:59], v[16:23], v[202:209], v[56:59]
	v_mfma_f32_16x16x128_f8f6f4 v[48:51], v[24:31], v[202:209], v[48:51]
	v_mfma_f32_16x16x128_f8f6f4 v[40:43], v[16:23], v[210:217], v[40:43]
	v_mfma_f32_16x16x128_f8f6f4 v[32:35], v[24:31], v[210:217], v[32:35]
	s_barrier
	s_setprio 1
	s_add_i32 s74, s74, 2
	s_add_u32 s30, s30, 0x100
	s_addc_u32 s31, s31, 0
	s_add_u32 s72, s72, 0x100
	s_addc_u32 s73, s73, 0
	s_cmp_gt_u32 s74, 5
	s_cbranch_scc0 .LBB0_1540
	s_setprio 0
	s_and_b64 vcc, exec, s[10:11]
	s_cbranch_vccz .LBB0_1543
	s_barrier

; #define PG8_WAIT_V(n) asm volatile("s_waitcnt vmcnt(" #n ")" ::: "memory")
; template <class Epi, class Sched, bool ALIGN_EPI = false, bool SP2 = false, bool F8 = false, bool I8 = false, bool PF = false>
; __device__ __forceinline__ void gemm_phase(PG8_LAS unsigned char* lds, const Gemm g, const Sched& S, const Epi& E, const int wave_) {
;     ...
;         for (int t = 0; t < nt; t += 2) {
;             const bool last = (t == nt - 2);
;             const char* a1 = cA + (size_t)(t + 1) * kstep;
;             const char* a2 = last ? nA : cA + (size_t)(t + 2) * kstep; const char* b2 = last ? nB : cB + (size_t)(t + 2) * kstep;
;             const char* a3 = a2 + kstep; const char* b3 = b2 + kstep;
;             if (last && has_next) S.a_ready(nxt);
;             if constexpr (PF) {
;             PG8_STAGE(wr ? PG8_SA(0, 0) : PG8_SA(1, 1), wr ? a2 : a1 + hstep, voffA); PG8_STAGE(wr ? PG8_SB(0, 0) : PG8_SB(1, 1), wr ? b2 : cB + (size_t)(t + 1) * kstep + hstep, voffB);
;             PG8_WAIT_V(8); PG8_BAR;
;             PG8_X1(0); __builtin_amdgcn_s_waitcnt(0xC07F); PG8_BAR; PG8_SCHED;
;             PG8_STAGE(wr ? PG8_SA(0, 1) : PG8_SA(0, 0), wr ? a2 + hstep : a2, voffA); PG8_STAGE(wr ? PG8_SB(0, 1) : PG8_SB(0, 0), wr ? b2 + hstep : b2, voffB);
;             PG8_WAIT_V(8); PG8_BAR;
;             PG8_X2(0); __builtin_amdgcn_s_waitcnt(0xC07F); PG8_BAR; PG8_SCHED;
;             PG8_STAGE(wr ? PG8_SA(1, 0) : PG8_SA(0, 1), wr ? a3 : a2 + hstep, voffA); PG8_STAGE(wr ? PG8_SB(1, 0) : PG8_SB(0, 1), wr ? b3 : b2 + hstep, voffB);
;             PG8_WAIT_V(8); PG8_BAR;
;             PG8_X1(1); __builtin_amdgcn_s_waitcnt(0xC07F); PG8_BAR; PG8_SCHED;
;             PG8_STAGE(wr ? PG8_SA(1, 1) : PG8_SA(1, 0), wr ? a3 + hstep : a3, voffA); PG8_STAGE(wr ? PG8_SB(1, 1) : PG8_SB(1, 0), wr ? b3 + hstep : b3, voffB);
;             PG8_WAIT_V(8); PG8_BAR;
;             PG8_X2(1); __builtin_amdgcn_s_waitcnt(0xC07F); PG8_BAR; PG8_SCHED;
;             } else
;             if constexpr (SP2) {
;             PG8_LDB(B0, 0, 0); PG8_LDB(B1, 0, 1); PG8_SCHED; PG8_LDA(At, 0, 0); PG8_STAGE(PG8_SA(1, 1), a1 + hstep, voffA);
;             PG8_WAIT_V(8); PG8_WAIT_L(0); PG8_BAR; PG8_MMA(0, 0, At, B0); PG8_MMA(0, 1, At, B1); PG8_BAR; PG8_SCHED;
;             PG8_LDA(At, 0, 1); PG8_STAGE(PG8_SB(0, 0), b2, voffB); PG8_STAGE(PG8_SB(0, 1), b2 + hstep, voffB); PG8_STAGE(PG8_SA(0, 0), a2, voffA);
.LBB0_1621:
	ds_read_b128 v[24:27], v181
	ds_read_b128 v[28:31], v181 offset:1024
	ds_read_b128 v[16:19], v181 offset:2048
	ds_read_b128 v[20:23], v181 offset:3072
	ds_read_b128 v[8:11], v182
	ds_read_b128 v[12:15], v182 offset:1024
	ds_read_b128 v[0:3], v182 offset:2048
	ds_read_b128 v[4:7], v182 offset:3072
	s_add_u32 s30, s34, 0x100
	s_addc_u32 s31, s35, 0
	s_cmp_eq_u32 s73, 24
	s_cselect_b32 s39, s25, s31
	s_cselect_b32 s38, s24, s30
	s_cselect_b32 s37, s27, s72
	s_cselect_b32 s36, s26, s71
	v_lshl_add_u64 v[208:209], s[34:35], 0, v[168:169]
	s_add_i32 m0, s29, 0xc000
	ds_read_b128 v[172:175], v183
	ds_read_b128 v[176:179], v183 offset:1024
	ds_read_b128 v[184:187], v183 offset:2048
	ds_read_b128 v[188:191], v183 offset:3072
	ds_read_b128 v[192:195], v183 offset:4096
	ds_read_b128 v[196:199], v183 offset:5120
	ds_read_b128 v[200:203], v183 offset:6144
	ds_read_b128 v[204:207], v183 offset:7168
	global_load_lds_dwordx4 v[208:209], off
	v_lshl_add_u64 v[208:209], s[34:35], 0, v[170:171]
	s_add_i32 m0, s29, 0xe000
	s_nop 0
	global_load_lds_dwordx4 v[208:209], off
	s_waitcnt vmcnt(8)
	s_waitcnt lgkmcnt(0)
	s_setprio 0
	s_barrier
	s_waitcnt lgkmcnt(0)
	v_mfma_f32_16x16x128_f8f6f4 v[156:159], v[24:31], v[172:179], v[156:159]
	v_mfma_f32_16x16x128_f8f6f4 v[152:155], v[16:23], v[172:179], v[152:155]
	v_mfma_f32_16x16x128_f8f6f4 v[144:147], v[24:31], v[184:191], v[144:147]
	v_mfma_f32_16x16x128_f8f6f4 v[136:139], v[16:23], v[184:191], v[136:139]
	v_mfma_f32_16x16x128_f8f6f4 v[128:131], v[24:31], v[192:199], v[128:131]
	v_mfma_f32_16x16x128_f8f6f4 v[120:123], v[16:23], v[192:199], v[120:123]
	v_mfma_f32_16x16x128_f8f6f4 v[112:115], v[24:31], v[200:207], v[112:115]
	v_mfma_f32_16x16x128_f8f6f4 v[104:107], v[16:23], v[200:207], v[104:107]
	v_mfma_f32_16x16x128_f8f6f4 v[148:151], v[8:15], v[172:179], v[148:151]
	v_mfma_f32_16x16x128_f8f6f4 v[140:143], v[0:7], v[172:179], v[140:143]
	v_mfma_f32_16x16x128_f8f6f4 v[132:135], v[8:15], v[184:191], v[132:135]
	v_mfma_f32_16x16x128_f8f6f4 v[124:127], v[0:7], v[184:191], v[124:127]
	v_mfma_f32_16x16x128_f8f6f4 v[116:119], v[8:15], v[192:199], v[116:119]
	v_mfma_f32_16x16x128_f8f6f4 v[108:111], v[0:7], v[192:199], v[108:111]
	v_mfma_f32_16x16x128_f8f6f4 v[100:103], v[8:15], v[200:207], v[100:103]
	v_mfma_f32_16x16x128_f8f6f4 v[96:99], v[0:7], v[200:207], v[96:99]
	s_barrier
	s_setprio 1
	s_add_i32 s34, s53, s42
	v_lshl_add_u64 v[172:173], s[36:37], 0, v[160:161]
	s_mov_b32 m0, s34
	ds_read_b128 v[184:187], v183 offset:16384
	ds_read_b128 v[188:191], v183 offset:17408
	ds_read_b128 v[192:195], v183 offset:18432
	ds_read_b128 v[196:199], v183 offset:19456
	ds_read_b128 v[200:203], v183 offset:20480
	ds_read_b128 v[204:207], v183 offset:21504
	ds_read_b128 v[208:211], v183 offset:22528
	ds_read_b128 v[212:215], v183 offset:23552
	global_load_lds_dwordx4 v[172:173], off
	s_add_i32 m0, s34, 0x2000
	s_add_u32 s34, s36, 0x70000
	v_lshl_add_u64 v[174:175], s[36:37], 0, v[166:167]
	s_addc_u32 s35, s37, 0
	s_add_i32 s74, s54, s42
	global_load_lds_dwordx4 v[174:175], off
	v_lshl_add_u64 v[176:177], s[34:35], 0, v[160:161]
	s_mov_b32 m0, s74
	v_lshl_add_u64 v[178:179], s[38:39], 0, v[164:165]
	global_load_lds_dwordx4 v[176:177], off
	v_lshl_add_u64 v[176:177], s[34:35], 0, v[166:167]
	s_add_i32 m0, s74, 0x2000
	s_nop 0
	global_load_lds_dwordx4 v[176:177], off
	v_lshl_add_u64 v[176:177], s[38:39], 0, v[162:163]
	s_mov_b32 m0, s29
	s_nop 0
	global_load_lds_dwordx4 v[176:177], off
	s_mov_b32 m0, s45
	s_nop 0
	global_load_lds_dwordx4 v[178:179], off
	s_waitcnt vmcnt(8)
	s_waitcnt lgkmcnt(0)
	s_setprio 0
	s_barrier
	s_waitcnt lgkmcnt(0)
	v_mfma_f32_16x16x128_f8f6f4 v[92:95], v[24:31], v[184:191], v[92:95]
	v_mfma_f32_16x16x128_f8f6f4 v[88:91], v[16:23], v[184:191], v[88:91]
	v_mfma_f32_16x16x128_f8f6f4 v[80:83], v[24:31], v[192:199], v[80:83]
	v_mfma_f32_16x16x128_f8f6f4 v[72:75], v[16:23], v[192:199], v[72:75]
	v_mfma_f32_16x16x128_f8f6f4 v[64:67], v[24:31], v[200:207], v[64:67]
	v_mfma_f32_16x16x128_f8f6f4 v[56:59], v[16:23], v[200:207], v[56:59]
	v_mfma_f32_16x16x128_f8f6f4 v[48:51], v[24:31], v[208:215], v[48:51]
	v_mfma_f32_16x16x128_f8f6f4 v[40:43], v[16:23], v[208:215], v[40:43]
	v_mfma_f32_16x16x128_f8f6f4 v[84:87], v[8:15], v[184:191], v[84:87]
	v_mfma_f32_16x16x128_f8f6f4 v[76:79], v[0:7], v[184:191], v[76:79]
	v_mfma_f32_16x16x128_f8f6f4 v[68:71], v[8:15], v[192:199], v[68:71]
	v_mfma_f32_16x16x128_f8f6f4 v[60:63], v[0:7], v[192:199], v[60:63]
	v_mfma_f32_16x16x128_f8f6f4 v[52:55], v[8:15], v[200:207], v[52:55]
	v_mfma_f32_16x16x128_f8f6f4 v[44:47], v[0:7], v[200:207], v[44:47]
	v_mfma_f32_16x16x128_f8f6f4 v[36:39], v[8:15], v[208:215], v[36:39]
	v_mfma_f32_16x16x128_f8f6f4 v[32:35], v[0:7], v[208:215], v[32:35]
	s_barrier
; #define PG8_LDA(dst, b, h) do { _Pragma("unroll") for (int m = 0; m < 4; ++m) _Pragma("unroll") for (int k = 0; k < 2; ++k) dst[m][k] = *(const PG8_LAS bf16x8*)(lds + PG8_SA(b, h) + aoff + m * 2048 + k * 1024); } while (0)
; #define PG8_LDB(dst, b, h) do { _Pragma("unroll") for (int n = 0; n < 2; ++n) _Pragma("unroll") for (int k = 0; k < 2; ++k) dst[n][k] = *(const PG8_LAS bf16x8*)(lds + PG8_SB(b, h) + boff + n * 2048 + k * 1024); } while (0)
; #define PG8_WAIT_V(n) asm volatile("s_waitcnt vmcnt(" #n ")" ::: "memory")
; #define PG8_WAIT_L(n) asm volatile("s_waitcnt lgkmcnt(" #n ")" ::: "memory")
; #define PG8_BAR __builtin_amdgcn_s_barrier()
; #define PG8_SCHED __builtin_amdgcn_sched_barrier(0)
; template <class Epi, class Sched, bool ALIGN_EPI = false, bool SP2 = false, bool F8 = false, bool I8 = false, bool PF = false>
; __device__ __forceinline__ void gemm_phase(PG8_LAS unsigned char* lds, const Gemm g, const Sched& S, const Epi& E, const int wave_) {
;     ...
;             PG8_LDB(B0, 1, 0); PG8_LDB(B1, 1, 1); PG8_SCHED; PG8_LDA(At, 1, 0); PG8_STAGE(PG8_SA(0, 1), a2 + hstep, voffA);
;             PG8_WAIT_V(8); PG8_WAIT_L(0); PG8_BAR; PG8_MMA(0, 0, At, B0); PG8_MMA(0, 1, At, B1); PG8_BAR; PG8_SCHED;
;             PG8_LDA(At, 1, 1); PG8_STAGE(PG8_SB(1, 0), b3, voffB); PG8_STAGE(PG8_SB(1, 1), b3 + hstep, voffB); PG8_STAGE(PG8_SA(1, 0), a3, voffA);
;             PG8_WAIT_V(8); PG8_WAIT_L(0); PG8_BAR; PG8_MMA(1, 0, At, B0); PG8_MMA(1, 1, At, B1); PG8_BAR; PG8_SCHED;
	s_setprio 1
	s_add_i32 s74, 0, 0x18000
	s_add_i32 s75, 0, 0x1c000
	v_add_u32_e32 v12, s74, v180
	v_add_u32_e32 v28, s75, v180
	ds_read_b128 v[0:3], v12
	ds_read_b128 v[4:7], v12 offset:1024
	ds_read_b128 v[8:11], v12 offset:2048
	ds_read_b128 v[12:15], v12 offset:3072
	ds_read_b128 v[16:19], v28
	ds_read_b128 v[20:23], v28 offset:1024
	ds_read_b128 v[24:27], v28 offset:2048
	ds_read_b128 v[28:31], v28 offset:3072
	s_add_u32 s34, s38, 0x70000
	s_addc_u32 s35, s39, 0
	s_mov_b32 m0, s46
	v_lshl_add_u64 v[216:217], s[34:35], 0, v[162:163]
	ds_read_b128 v[184:187], v183 offset:32768
	ds_read_b128 v[188:191], v183 offset:33792
	ds_read_b128 v[192:195], v183 offset:34816
	ds_read_b128 v[196:199], v183 offset:35840
	ds_read_b128 v[200:203], v183 offset:36864
	ds_read_b128 v[204:207], v183 offset:37888
	ds_read_b128 v[208:211], v183 offset:38912
	ds_read_b128 v[212:215], v183 offset:39936
	global_load_lds_dwordx4 v[216:217], off
	v_lshl_add_u64 v[216:217], s[34:35], 0, v[164:165]
	s_mov_b32 m0, s47
	s_nop 0
	global_load_lds_dwordx4 v[216:217], off
	s_waitcnt vmcnt(8)
	s_waitcnt lgkmcnt(0)
	s_setprio 0
	s_barrier
	s_waitcnt lgkmcnt(0)
	v_mfma_f32_16x16x128_f8f6f4 v[156:159], v[0:7], v[184:191], v[156:159]
	v_mfma_f32_16x16x128_f8f6f4 v[152:155], v[8:15], v[184:191], v[152:155]
	v_mfma_f32_16x16x128_f8f6f4 v[144:147], v[0:7], v[192:199], v[144:147]
	v_mfma_f32_16x16x128_f8f6f4 v[136:139], v[8:15], v[192:199], v[136:139]
	v_mfma_f32_16x16x128_f8f6f4 v[128:131], v[0:7], v[200:207], v[128:131]
	v_mfma_f32_16x16x128_f8f6f4 v[120:123], v[8:15], v[200:207], v[120:123]
	v_mfma_f32_16x16x128_f8f6f4 v[112:115], v[0:7], v[208:215], v[112:115]
	v_mfma_f32_16x16x128_f8f6f4 v[104:107], v[8:15], v[208:215], v[104:107]
	v_mfma_f32_16x16x128_f8f6f4 v[148:151], v[16:23], v[184:191], v[148:151]
	v_mfma_f32_16x16x128_f8f6f4 v[140:143], v[24:31], v[184:191], v[140:143]
	v_mfma_f32_16x16x128_f8f6f4 v[132:135], v[16:23], v[192:199], v[132:135]
	v_mfma_f32_16x16x128_f8f6f4 v[124:127], v[24:31], v[192:199], v[124:127]
	v_mfma_f32_16x16x128_f8f6f4 v[116:119], v[16:23], v[200:207], v[116:119]
	v_mfma_f32_16x16x128_f8f6f4 v[108:111], v[24:31], v[200:207], v[108:111]
	v_mfma_f32_16x16x128_f8f6f4 v[100:103], v[16:23], v[208:215], v[100:103]
	v_mfma_f32_16x16x128_f8f6f4 v[96:99], v[24:31], v[208:215], v[96:99]
	s_barrier
	s_setprio 1
	s_add_i32 s34, s74, s42
	v_lshl_add_u64 v[172:173], v[172:173], 0, s[8:9]
	s_mov_b32 m0, s34
	ds_read_b128 v[184:187], v183 offset:49152
	ds_read_b128 v[188:191], v183 offset:50176
	ds_read_b128 v[192:195], v183 offset:51200
	ds_read_b128 v[196:199], v183 offset:52224
	ds_read_b128 v[200:203], v183 offset:53248
	ds_read_b128 v[204:207], v183 offset:54272
	ds_read_b128 v[208:211], v183 offset:55296
	ds_read_b128 v[212:215], v183 offset:56320
	global_load_lds_dwordx4 v[172:173], off
	s_add_i32 m0, s34, 0x2000
	s_add_u32 s34, s36, 0x70080
	v_lshl_add_u64 v[172:173], v[174:175], 0, s[8:9]
	s_addc_u32 s35, s37, 0
	s_add_i32 s36, s75, s42
	global_load_lds_dwordx4 v[172:173], off
	v_lshl_add_u64 v[172:173], s[34:35], 0, v[160:161]
	s_mov_b32 m0, s36
	s_nop 0
	global_load_lds_dwordx4 v[172:173], off
	v_lshl_add_u64 v[172:173], s[34:35], 0, v[166:167]
	s_add_i32 m0, s36, 0x2000
	s_nop 0
	global_load_lds_dwordx4 v[172:173], off
	v_lshl_add_u64 v[172:173], v[176:177], 0, s[8:9]
	s_mov_b32 m0, s51
	s_nop 0
	global_load_lds_dwordx4 v[172:173], off
	v_lshl_add_u64 v[172:173], v[178:179], 0, s[8:9]
	s_mov_b32 m0, s52
	s_nop 0
	global_load_lds_dwordx4 v[172:173], off
	s_waitcnt vmcnt(8)
	s_waitcnt lgkmcnt(0)
	s_setprio 0
	s_barrier
	s_waitcnt lgkmcnt(0)
	v_mfma_f32_16x16x128_f8f6f4 v[92:95], v[0:7], v[184:191], v[92:95]
	v_mfma_f32_16x16x128_f8f6f4 v[88:91], v[8:15], v[184:191], v[88:91]
	v_mfma_f32_16x16x128_f8f6f4 v[80:83], v[0:7], v[192:199], v[80:83]
	v_mfma_f32_16x16x128_f8f6f4 v[72:75], v[8:15], v[192:199], v[72:75]
	v_mfma_f32_16x16x128_f8f6f4 v[64:67], v[0:7], v[200:207], v[64:67]
	v_mfma_f32_16x16x128_f8f6f4 v[56:59], v[8:15], v[200:207], v[56:59]
	v_mfma_f32_16x16x128_f8f6f4 v[48:51], v[0:7], v[208:215], v[48:51]
	v_mfma_f32_16x16x128_f8f6f4 v[40:43], v[8:15], v[208:215], v[40:43]
	v_mfma_f32_16x16x128_f8f6f4 v[84:87], v[16:23], v[184:191], v[84:87]
	v_mfma_f32_16x16x128_f8f6f4 v[76:79], v[24:31], v[184:191], v[76:79]
	v_mfma_f32_16x16x128_f8f6f4 v[68:71], v[16:23], v[192:199], v[68:71]
	v_mfma_f32_16x16x128_f8f6f4 v[60:63], v[24:31], v[192:199], v[60:63]
	v_mfma_f32_16x16x128_f8f6f4 v[52:55], v[16:23], v[200:207], v[52:55]
	v_mfma_f32_16x16x128_f8f6f4 v[44:47], v[24:31], v[200:207], v[44:47]
	v_mfma_f32_16x16x128_f8f6f4 v[36:39], v[16:23], v[208:215], v[36:39]
	v_mfma_f32_16x16x128_f8f6f4 v[32:35], v[24:31], v[208:215], v[32:35]
	s_barrier
	s_setprio 1
	s_add_i32 s73, s73, 2
	s_add_u32 s71, s71, 0x100
	s_addc_u32 s72, s72, 0
	s_cmp_gt_u32 s73, 25
	s_mov_b64 s[34:35], s[30:31]
	s_cbranch_scc0 .LBB0_1621
	s_setprio 0
	s_and_b64 vcc, exec, s[10:11]
	s_cbranch_vccz .LBB0_1624
	s_barrier

; #define PG8_WAIT_V(n) asm volatile("s_waitcnt vmcnt(" #n ")" ::: "memory")
; template <class Epi, class Sched, bool ALIGN_EPI = false, bool SP2 = false, bool F8 = false, bool I8 = false, bool PF = false>
; __device__ __forceinline__ void gemm_phase(PG8_LAS unsigned char* lds, const Gemm g, const Sched& S, const Epi& E, const int wave_) {
;     ...
;         for (int t = 0; t < nt; t += 2) {
;             const bool last = (t == nt - 2);
;             const char* a1 = cA + (size_t)(t + 1) * kstep;
;             const char* a2 = last ? nA : cA + (size_t)(t + 2) * kstep; const char* b2 = last ? nB : cB + (size_t)(t + 2) * kstep;
;             const char* a3 = a2 + kstep; const char* b3 = b2 + kstep;
;             if (last && has_next) S.a_ready(nxt);
;             if constexpr (PF) {
;             PG8_STAGE(wr ? PG8_SA(0, 0) : PG8_SA(1, 1), wr ? a2 : a1 + hstep, voffA); PG8_STAGE(wr ? PG8_SB(0, 0) : PG8_SB(1, 1), wr ? b2 : cB + (size_t)(t + 1) * kstep + hstep, voffB);
;             PG8_WAIT_V(8); PG8_BAR;
;             PG8_X1(0); __builtin_amdgcn_s_waitcnt(0xC07F); PG8_BAR; PG8_SCHED;
;             PG8_STAGE(wr ? PG8_SA(0, 1) : PG8_SA(0, 0), wr ? a2 + hstep : a2, voffA); PG8_STAGE(wr ? PG8_SB(0, 1) : PG8_SB(0, 0), wr ? b2 + hstep : b2, voffB);
;             PG8_WAIT_V(8); PG8_BAR;
;             PG8_X2(0); __builtin_amdgcn_s_waitcnt(0xC07F); PG8_BAR; PG8_SCHED;
;             PG8_STAGE(wr ? PG8_SA(1, 0) : PG8_SA(0, 1), wr ? a3 : a2 + hstep, voffA); PG8_STAGE(wr ? PG8_SB(1, 0) : PG8_SB(0, 1), wr ? b3 : b2 + hstep, voffB);
;             PG8_WAIT_V(8); PG8_BAR;
;             PG8_X1(1); __builtin_amdgcn_s_waitcnt(0xC07F); PG8_BAR; PG8_SCHED;
;             PG8_STAGE(wr ? PG8_SA(1, 1) : PG8_SA(1, 0), wr ? a3 + hstep : a3, voffA); PG8_STAGE(wr ? PG8_SB(1, 1) : PG8_SB(1, 0), wr ? b3 + hstep : b3, voffB);
;             PG8_WAIT_V(8); PG8_BAR;
;             PG8_X2(1); __builtin_amdgcn_s_waitcnt(0xC07F); PG8_BAR; PG8_SCHED;
;             } else
;             if constexpr (SP2) {
;             PG8_LDB(B0, 0, 0); PG8_LDB(B1, 0, 1); PG8_SCHED; PG8_LDA(At, 0, 0); PG8_STAGE(PG8_SA(1, 1), a1 + hstep, voffA);
;             PG8_WAIT_V(8); PG8_WAIT_L(0); PG8_BAR; PG8_MMA(0, 0, At, B0); PG8_MMA(0, 1, At, B1); PG8_BAR; PG8_SCHED;
;             PG8_LDA(At, 0, 1); PG8_STAGE(PG8_SB(0, 0), b2, voffB); PG8_STAGE(PG8_SB(0, 1), b2 + hstep, voffB); PG8_STAGE(PG8_SA(0, 0), a2, voffA);
.LBB0_1718:
	ds_read_b128 v[24:27], v181
	ds_read_b128 v[28:31], v181 offset:1024
	ds_read_b128 v[16:19], v181 offset:2048
	ds_read_b128 v[20:23], v181 offset:3072
	ds_read_b128 v[8:11], v182
	ds_read_b128 v[12:15], v182 offset:1024
	ds_read_b128 v[0:3], v182 offset:2048
	ds_read_b128 v[4:7], v182 offset:3072
	s_add_u32 s30, s34, 0x100
	s_addc_u32 s31, s35, 0
	s_cmp_eq_u32 s73, 24
	s_cselect_b32 s39, s25, s31
	s_cselect_b32 s38, s24, s30
	s_cselect_b32 s37, s27, s72
	s_cselect_b32 s36, s26, s71
	v_lshl_add_u64 v[208:209], s[34:35], 0, v[168:169]
	s_add_i32 m0, s29, 0xc000
	ds_read_b128 v[172:175], v183
	ds_read_b128 v[176:179], v183 offset:1024
	ds_read_b128 v[184:187], v183 offset:2048
	ds_read_b128 v[188:191], v183 offset:3072
	ds_read_b128 v[192:195], v183 offset:4096
	ds_read_b128 v[196:199], v183 offset:5120
	ds_read_b128 v[200:203], v183 offset:6144
	ds_read_b128 v[204:207], v183 offset:7168
	global_load_lds_dwordx4 v[208:209], off
	v_lshl_add_u64 v[208:209], s[34:35], 0, v[170:171]
	s_add_i32 m0, s29, 0xe000
	s_nop 0
	global_load_lds_dwordx4 v[208:209], off
	s_waitcnt vmcnt(8)
	s_waitcnt lgkmcnt(0)
	s_setprio 0
	s_barrier
	s_waitcnt lgkmcnt(0)
	v_mfma_f32_16x16x128_f8f6f4 v[156:159], v[24:31], v[172:179], v[156:159]
	v_mfma_f32_16x16x128_f8f6f4 v[152:155], v[16:23], v[172:179], v[152:155]
	v_mfma_f32_16x16x128_f8f6f4 v[144:147], v[24:31], v[184:191], v[144:147]
	v_mfma_f32_16x16x128_f8f6f4 v[136:139], v[16:23], v[184:191], v[136:139]
	v_mfma_f32_16x16x128_f8f6f4 v[128:131], v[24:31], v[192:199], v[128:131]
	v_mfma_f32_16x16x128_f8f6f4 v[120:123], v[16:23], v[192:199], v[120:123]
	v_mfma_f32_16x16x128_f8f6f4 v[112:115], v[24:31], v[200:207], v[112:115]
	v_mfma_f32_16x16x128_f8f6f4 v[104:107], v[16:23], v[200:207], v[104:107]
	v_mfma_f32_16x16x128_f8f6f4 v[148:151], v[8:15], v[172:179], v[148:151]
	v_mfma_f32_16x16x128_f8f6f4 v[140:143], v[0:7], v[172:179], v[140:143]
	v_mfma_f32_16x16x128_f8f6f4 v[132:135], v[8:15], v[184:191], v[132:135]
	v_mfma_f32_16x16x128_f8f6f4 v[124:127], v[0:7], v[184:191], v[124:127]
	v_mfma_f32_16x16x128_f8f6f4 v[116:119], v[8:15], v[192:199], v[116:119]
	v_mfma_f32_16x16x128_f8f6f4 v[108:111], v[0:7], v[192:199], v[108:111]
	v_mfma_f32_16x16x128_f8f6f4 v[100:103], v[8:15], v[200:207], v[100:103]
	v_mfma_f32_16x16x128_f8f6f4 v[96:99], v[0:7], v[200:207], v[96:99]
	s_barrier
	s_setprio 1
	s_add_i32 s34, s53, s43
	v_lshl_add_u64 v[172:173], s[36:37], 0, v[160:161]
	s_mov_b32 m0, s34
	ds_read_b128 v[184:187], v183 offset:16384
	ds_read_b128 v[188:191], v183 offset:17408
	ds_read_b128 v[192:195], v183 offset:18432
	ds_read_b128 v[196:199], v183 offset:19456
	ds_read_b128 v[200:203], v183 offset:20480
	ds_read_b128 v[204:207], v183 offset:21504
	ds_read_b128 v[208:211], v183 offset:22528
	ds_read_b128 v[212:215], v183 offset:23552
	global_load_lds_dwordx4 v[172:173], off
	s_add_i32 m0, s34, 0x2000
	s_add_u32 s34, s36, 0x70000
	v_lshl_add_u64 v[174:175], s[36:37], 0, v[162:163]
	s_addc_u32 s35, s37, 0
	s_add_i32 s74, s54, s43
	global_load_lds_dwordx4 v[174:175], off
	v_lshl_add_u64 v[176:177], s[34:35], 0, v[160:161]
	s_mov_b32 m0, s74
	v_lshl_add_u64 v[178:179], s[38:39], 0, v[164:165]
	global_load_lds_dwordx4 v[176:177], off
	v_lshl_add_u64 v[176:177], s[34:35], 0, v[162:163]
	s_add_i32 m0, s74, 0x2000
	s_nop 0
	global_load_lds_dwordx4 v[176:177], off
	v_lshl_add_u64 v[176:177], s[38:39], 0, v[166:167]
	s_mov_b32 m0, s29
	s_nop 0
	global_load_lds_dwordx4 v[176:177], off
	s_mov_b32 m0, s45
	s_nop 0
	global_load_lds_dwordx4 v[178:179], off
	s_waitcnt vmcnt(8)
	s_waitcnt lgkmcnt(0)
	s_setprio 0
	s_barrier
	s_waitcnt lgkmcnt(0)
	v_mfma_f32_16x16x128_f8f6f4 v[92:95], v[24:31], v[184:191], v[92:95]
	v_mfma_f32_16x16x128_f8f6f4 v[88:91], v[16:23], v[184:191], v[88:91]
	v_mfma_f32_16x16x128_f8f6f4 v[80:83], v[24:31], v[192:199], v[80:83]
	v_mfma_f32_16x16x128_f8f6f4 v[72:75], v[16:23], v[192:199], v[72:75]
	v_mfma_f32_16x16x128_f8f6f4 v[64:67], v[24:31], v[200:207], v[64:67]
	v_mfma_f32_16x16x128_f8f6f4 v[56:59], v[16:23], v[200:207], v[56:59]
	v_mfma_f32_16x16x128_f8f6f4 v[48:51], v[24:31], v[208:215], v[48:51]
	v_mfma_f32_16x16x128_f8f6f4 v[40:43], v[16:23], v[208:215], v[40:43]
	v_mfma_f32_16x16x128_f8f6f4 v[84:87], v[8:15], v[184:191], v[84:87]
	v_mfma_f32_16x16x128_f8f6f4 v[76:79], v[0:7], v[184:191], v[76:79]
	v_mfma_f32_16x16x128_f8f6f4 v[68:71], v[8:15], v[192:199], v[68:71]
	v_mfma_f32_16x16x128_f8f6f4 v[60:63], v[0:7], v[192:199], v[60:63]
	v_mfma_f32_16x16x128_f8f6f4 v[52:55], v[8:15], v[200:207], v[52:55]
	v_mfma_f32_16x16x128_f8f6f4 v[44:47], v[0:7], v[200:207], v[44:47]
	v_mfma_f32_16x16x128_f8f6f4 v[36:39], v[8:15], v[208:215], v[36:39]
	v_mfma_f32_16x16x128_f8f6f4 v[32:35], v[0:7], v[208:215], v[32:35]
	s_barrier
; #define PG8_LDA(dst, b, h) do { _Pragma("unroll") for (int m = 0; m < 4; ++m) _Pragma("unroll") for (int k = 0; k < 2; ++k) dst[m][k] = *(const PG8_LAS bf16x8*)(lds + PG8_SA(b, h) + aoff + m * 2048 + k * 1024); } while (0)
; #define PG8_LDB(dst, b, h) do { _Pragma("unroll") for (int n = 0; n < 2; ++n) _Pragma("unroll") for (int k = 0; k < 2; ++k) dst[n][k] = *(const PG8_LAS bf16x8*)(lds + PG8_SB(b, h) + boff + n * 2048 + k * 1024); } while (0)
; #define PG8_WAIT_V(n) asm volatile("s_waitcnt vmcnt(" #n ")" ::: "memory")
; #define PG8_WAIT_L(n) asm volatile("s_waitcnt lgkmcnt(" #n ")" ::: "memory")
; #define PG8_BAR __builtin_amdgcn_s_barrier()
; #define PG8_SCHED __builtin_amdgcn_sched_barrier(0)
; template <class Epi, class Sched, bool ALIGN_EPI = false, bool SP2 = false, bool F8 = false, bool I8 = false, bool PF = false>
; __device__ __forceinline__ void gemm_phase(PG8_LAS unsigned char* lds, const Gemm g, const Sched& S, const Epi& E, const int wave_) {
;     ...
;             PG8_LDB(B0, 1, 0); PG8_LDB(B1, 1, 1); PG8_SCHED; PG8_LDA(At, 1, 0); PG8_STAGE(PG8_SA(0, 1), a2 + hstep, voffA);
;             PG8_WAIT_V(8); PG8_WAIT_L(0); PG8_BAR; PG8_MMA(0, 0, At, B0); PG8_MMA(0, 1, At, B1); PG8_BAR; PG8_SCHED;
;             PG8_LDA(At, 1, 1); PG8_STAGE(PG8_SB(1, 0), b3, voffB); PG8_STAGE(PG8_SB(1, 1), b3 + hstep, voffB); PG8_STAGE(PG8_SA(1, 0), a3, voffA);
;             PG8_WAIT_V(8); PG8_WAIT_L(0); PG8_BAR; PG8_MMA(1, 0, At, B0); PG8_MMA(1, 1, At, B1); PG8_BAR; PG8_SCHED;
	s_setprio 1
	s_add_i32 s74, 0, 0x18000
	s_add_i32 s75, 0, 0x1c000
	v_add_u32_e32 v12, s74, v180
	v_add_u32_e32 v28, s75, v180
	ds_read_b128 v[0:3], v12
	ds_read_b128 v[4:7], v12 offset:1024
	ds_read_b128 v[8:11], v12 offset:2048
	ds_read_b128 v[12:15], v12 offset:3072
	ds_read_b128 v[16:19], v28
	ds_read_b128 v[20:23], v28 offset:1024
	ds_read_b128 v[24:27], v28 offset:2048
	ds_read_b128 v[28:31], v28 offset:3072
	s_add_u32 s34, s38, 0x70000
	s_addc_u32 s35, s39, 0
	s_mov_b32 m0, s46
	v_lshl_add_u64 v[216:217], s[34:35], 0, v[166:167]
	ds_read_b128 v[184:187], v183 offset:32768
	ds_read_b128 v[188:191], v183 offset:33792
	ds_read_b128 v[192:195], v183 offset:34816
	ds_read_b128 v[196:199], v183 offset:35840
	ds_read_b128 v[200:203], v183 offset:36864
	ds_read_b128 v[204:207], v183 offset:37888
	ds_read_b128 v[208:211], v183 offset:38912
	ds_read_b128 v[212:215], v183 offset:39936
	global_load_lds_dwordx4 v[216:217], off
	v_lshl_add_u64 v[216:217], s[34:35], 0, v[164:165]
	s_mov_b32 m0, s47
	s_nop 0
	global_load_lds_dwordx4 v[216:217], off
	s_waitcnt vmcnt(8)
	s_waitcnt lgkmcnt(0)
	s_setprio 0
	s_barrier
	s_waitcnt lgkmcnt(0)
	v_mfma_f32_16x16x128_f8f6f4 v[156:159], v[0:7], v[184:191], v[156:159]
	v_mfma_f32_16x16x128_f8f6f4 v[152:155], v[8:15], v[184:191], v[152:155]
	v_mfma_f32_16x16x128_f8f6f4 v[144:147], v[0:7], v[192:199], v[144:147]
	v_mfma_f32_16x16x128_f8f6f4 v[136:139], v[8:15], v[192:199], v[136:139]
	v_mfma_f32_16x16x128_f8f6f4 v[128:131], v[0:7], v[200:207], v[128:131]
	v_mfma_f32_16x16x128_f8f6f4 v[120:123], v[8:15], v[200:207], v[120:123]
	v_mfma_f32_16x16x128_f8f6f4 v[112:115], v[0:7], v[208:215], v[112:115]
	v_mfma_f32_16x16x128_f8f6f4 v[104:107], v[8:15], v[208:215], v[104:107]
	v_mfma_f32_16x16x128_f8f6f4 v[148:151], v[16:23], v[184:191], v[148:151]
	v_mfma_f32_16x16x128_f8f6f4 v[140:143], v[24:31], v[184:191], v[140:143]
	v_mfma_f32_16x16x128_f8f6f4 v[132:135], v[16:23], v[192:199], v[132:135]
	v_mfma_f32_16x16x128_f8f6f4 v[124:127], v[24:31], v[192:199], v[124:127]
	v_mfma_f32_16x16x128_f8f6f4 v[116:119], v[16:23], v[200:207], v[116:119]
	v_mfma_f32_16x16x128_f8f6f4 v[108:111], v[24:31], v[200:207], v[108:111]
	v_mfma_f32_16x16x128_f8f6f4 v[100:103], v[16:23], v[208:215], v[100:103]
	v_mfma_f32_16x16x128_f8f6f4 v[96:99], v[24:31], v[208:215], v[96:99]
	s_barrier
	s_setprio 1
	s_add_i32 s34, s74, s43
	v_lshl_add_u64 v[172:173], v[172:173], 0, s[8:9]
	s_mov_b32 m0, s34
	ds_read_b128 v[184:187], v183 offset:49152
	ds_read_b128 v[188:191], v183 offset:50176
	ds_read_b128 v[192:195], v183 offset:51200
	ds_read_b128 v[196:199], v183 offset:52224
	ds_read_b128 v[200:203], v183 offset:53248
	ds_read_b128 v[204:207], v183 offset:54272
	ds_read_b128 v[208:211], v183 offset:55296
	ds_read_b128 v[212:215], v183 offset:56320
	global_load_lds_dwordx4 v[172:173], off
	s_add_i32 m0, s34, 0x2000
	s_add_u32 s34, s36, 0x70080
	v_lshl_add_u64 v[172:173], v[174:175], 0, s[8:9]
	s_addc_u32 s35, s37, 0
	s_add_i32 s36, s75, s43
	global_load_lds_dwordx4 v[172:173], off
	v_lshl_add_u64 v[172:173], s[34:35], 0, v[160:161]
	s_mov_b32 m0, s36
	s_nop 0
	global_load_lds_dwordx4 v[172:173], off
	v_lshl_add_u64 v[172:173], s[34:35], 0, v[162:163]
	s_add_i32 m0, s36, 0x2000
	s_nop 0
	global_load_lds_dwordx4 v[172:173], off
	v_lshl_add_u64 v[172:173], v[176:177], 0, s[8:9]
	s_mov_b32 m0, s51
	s_nop 0
	global_load_lds_dwordx4 v[172:173], off
	v_lshl_add_u64 v[172:173], v[178:179], 0, s[8:9]
	s_mov_b32 m0, s52
	s_nop 0
	global_load_lds_dwordx4 v[172:173], off
	s_waitcnt vmcnt(8)
	s_waitcnt lgkmcnt(0)
	s_setprio 0
	s_barrier
	s_waitcnt lgkmcnt(0)
	v_mfma_f32_16x16x128_f8f6f4 v[92:95], v[0:7], v[184:191], v[92:95]
	v_mfma_f32_16x16x128_f8f6f4 v[88:91], v[8:15], v[184:191], v[88:91]
	v_mfma_f32_16x16x128_f8f6f4 v[80:83], v[0:7], v[192:199], v[80:83]
	v_mfma_f32_16x16x128_f8f6f4 v[72:75], v[8:15], v[192:199], v[72:75]
	v_mfma_f32_16x16x128_f8f6f4 v[64:67], v[0:7], v[200:207], v[64:67]
	v_mfma_f32_16x16x128_f8f6f4 v[56:59], v[8:15], v[200:207], v[56:59]
	v_mfma_f32_16x16x128_f8f6f4 v[48:51], v[0:7], v[208:215], v[48:51]
	v_mfma_f32_16x16x128_f8f6f4 v[40:43], v[8:15], v[208:215], v[40:43]
	v_mfma_f32_16x16x128_f8f6f4 v[84:87], v[16:23], v[184:191], v[84:87]
	v_mfma_f32_16x16x128_f8f6f4 v[76:79], v[24:31], v[184:191], v[76:79]
	v_mfma_f32_16x16x128_f8f6f4 v[68:71], v[16:23], v[192:199], v[68:71]
	v_mfma_f32_16x16x128_f8f6f4 v[60:63], v[24:31], v[192:199], v[60:63]
	v_mfma_f32_16x16x128_f8f6f4 v[52:55], v[16:23], v[200:207], v[52:55]
	v_mfma_f32_16x16x128_f8f6f4 v[44:47], v[24:31], v[200:207], v[44:47]
	v_mfma_f32_16x16x128_f8f6f4 v[36:39], v[16:23], v[208:215], v[36:39]
	v_mfma_f32_16x16x128_f8f6f4 v[32:35], v[24:31], v[208:215], v[32:35]
	s_barrier
	s_setprio 1
	s_add_i32 s73, s73, 2
	s_add_u32 s71, s71, 0x100
	s_addc_u32 s72, s72, 0
	s_cmp_gt_u32 s73, 25
	s_mov_b64 s[34:35], s[30:31]
	s_cbranch_scc0 .LBB0_1718
	s_setprio 0
	s_and_b64 vcc, exec, s[10:11]
	s_cbranch_vccz .LBB0_1721
	s_barrier
